# GEMM K loops: MFMA segment head trimmed (s_setprio 1 moved in front of the barrier, redundant lgkmcnt(0) after it removed)
# speedup vs baseline: 1.0007x; 1.0007x over previous
.LBB0_289:
	ds_read_b128 v[130:133], v167
	ds_read_b128 v[134:137], v167 offset:1024
	ds_read_b128 v[138:141], v167 offset:2048
	ds_read_b128 v[142:145], v167 offset:3072
	ds_read_b128 v[178:181], v188
	ds_read_b128 v[182:185], v188 offset:1024
	ds_read_b128 v[190:193], v188 offset:2048
	ds_read_b128 v[194:197], v188 offset:3072
	s_add_u32 s42, s8, 0x80
	s_addc_u32 s43, s9, 0
	s_cmp_eq_u32 s33, 28
	s_cselect_b32 s53, s49, s43
	s_cselect_b32 s52, s48, s42
	s_cselect_b32 s43, s51, s14
	s_cselect_b32 s42, s50, s5
	v_lshl_add_u64 v[186:187], s[8:9], 0, v[172:173]
	s_add_i32 m0, s62, 0xc000
	ds_read_b128 v[198:201], v189
	ds_read_b128 v[202:205], v189 offset:1024
	ds_read_b128 v[206:209], v189 offset:2048
	ds_read_b128 v[210:213], v189 offset:3072
	ds_read_b128 v[214:217], v189 offset:4096
	ds_read_b128 v[218:221], v189 offset:5120
	ds_read_b128 v[222:225], v189 offset:6144
	ds_read_b128 v[230:233], v189 offset:7168
	global_load_lds_dwordx4 v[186:187], off
	v_lshl_add_u64 v[186:187], s[8:9], 0, v[170:171]
	s_add_i32 m0, s62, 0xe000
	s_nop 0
	global_load_lds_dwordx4 v[186:187], off
	s_waitcnt vmcnt(8)
	s_waitcnt lgkmcnt(0)
	s_setprio 1
	s_barrier
	v_mfma_f32_16x16x32_bf16 v[126:129], v[130:133], v[198:201], v[126:129]
	v_mfma_f32_16x16x32_bf16 v[122:125], v[138:141], v[198:201], v[122:125]
	v_mfma_f32_16x16x32_bf16 v[110:113], v[130:133], v[206:209], v[110:113]
	v_mfma_f32_16x16x32_bf16 v[106:109], v[138:141], v[206:209], v[106:109]
	v_mfma_f32_16x16x32_bf16 v[94:97], v[130:133], v[214:217], v[94:97]
	v_mfma_f32_16x16x32_bf16 v[90:93], v[138:141], v[214:217], v[90:93]
	v_mfma_f32_16x16x32_bf16 v[78:81], v[130:133], v[222:225], v[78:81]
	v_mfma_f32_16x16x32_bf16 v[74:77], v[138:141], v[222:225], v[74:77]
	v_mfma_f32_16x16x32_bf16 v[126:129], v[134:137], v[202:205], v[126:129]
	v_mfma_f32_16x16x32_bf16 v[122:125], v[142:145], v[202:205], v[122:125]
	v_mfma_f32_16x16x32_bf16 v[110:113], v[134:137], v[210:213], v[110:113]
	v_mfma_f32_16x16x32_bf16 v[106:109], v[142:145], v[210:213], v[106:109]
	v_mfma_f32_16x16x32_bf16 v[94:97], v[134:137], v[218:221], v[94:97]
	v_mfma_f32_16x16x32_bf16 v[90:93], v[142:145], v[218:221], v[90:93]
	v_mfma_f32_16x16x32_bf16 v[78:81], v[134:137], v[230:233], v[78:81]
	v_mfma_f32_16x16x32_bf16 v[74:77], v[142:145], v[230:233], v[74:77]
	s_setprio 0
	s_setprio 1
	v_mfma_f32_16x16x32_bf16 v[118:121], v[178:181], v[198:201], v[118:121]
	v_mfma_f32_16x16x32_bf16 v[114:117], v[190:193], v[198:201], v[114:117]
	v_mfma_f32_16x16x32_bf16 v[102:105], v[178:181], v[206:209], v[102:105]
	v_mfma_f32_16x16x32_bf16 v[98:101], v[190:193], v[206:209], v[98:101]
	v_mfma_f32_16x16x32_bf16 v[86:89], v[178:181], v[214:217], v[86:89]
	v_mfma_f32_16x16x32_bf16 v[82:85], v[190:193], v[214:217], v[82:85]
	v_mfma_f32_16x16x32_bf16 v[70:73], v[178:181], v[222:225], v[70:73]
	v_mfma_f32_16x16x32_bf16 v[66:69], v[190:193], v[222:225], v[66:69]
	v_mfma_f32_16x16x32_bf16 v[118:121], v[182:185], v[202:205], v[118:121]
	v_mfma_f32_16x16x32_bf16 v[114:117], v[194:197], v[202:205], v[114:117]
	v_mfma_f32_16x16x32_bf16 v[102:105], v[182:185], v[210:213], v[102:105]
	v_mfma_f32_16x16x32_bf16 v[98:101], v[194:197], v[210:213], v[98:101]
	v_mfma_f32_16x16x32_bf16 v[86:89], v[182:185], v[218:221], v[86:89]
	v_mfma_f32_16x16x32_bf16 v[82:85], v[194:197], v[218:221], v[82:85]
	v_mfma_f32_16x16x32_bf16 v[70:73], v[182:185], v[230:233], v[70:73]
	v_mfma_f32_16x16x32_bf16 v[66:69], v[194:197], v[230:233], v[66:69]
	s_setprio 0
	s_barrier
	s_add_i32 s45, s76, s61
	v_lshl_add_u64 v[186:187], s[42:43], 0, v[146:147]
	s_mov_b32 m0, s45
	ds_read_b128 v[198:201], v189 offset:16384
	ds_read_b128 v[202:205], v189 offset:17408
	ds_read_b128 v[206:209], v189 offset:18432
	ds_read_b128 v[210:213], v189 offset:19456
	ds_read_b128 v[214:217], v189 offset:20480
	ds_read_b128 v[218:221], v189 offset:21504
	ds_read_b128 v[222:225], v189 offset:22528
	ds_read_b128 v[230:233], v189 offset:23552
	global_load_lds_dwordx4 v[186:187], off
	s_add_i32 m0, s45, 0x2000
	s_add_u32 s54, s42, 0x80000
	v_lshl_add_u64 v[226:227], s[42:43], 0, v[148:149]
	s_addc_u32 s55, s43, 0
	s_add_i32 s45, s77, s61
	global_load_lds_dwordx4 v[226:227], off
	v_lshl_add_u64 v[234:235], s[54:55], 0, v[146:147]
	s_mov_b32 m0, s45
	v_lshl_add_u64 v[236:237], s[52:53], 0, v[152:153]
	global_load_lds_dwordx4 v[234:235], off
	v_lshl_add_u64 v[234:235], s[54:55], 0, v[148:149]
	s_add_i32 m0, s45, 0x2000
	s_nop 0
	global_load_lds_dwordx4 v[234:235], off
	v_lshl_add_u64 v[234:235], s[52:53], 0, v[150:151]
	s_mov_b32 m0, s62
	s_nop 0
	global_load_lds_dwordx4 v[234:235], off
	s_mov_b32 m0, s63
	s_nop 0
	global_load_lds_dwordx4 v[236:237], off
	s_waitcnt vmcnt(8)
	s_waitcnt lgkmcnt(0)
	s_setprio 1
	s_barrier
	v_mfma_f32_16x16x32_bf16 v[54:57], v[130:133], v[198:201], v[54:57]
	v_mfma_f32_16x16x32_bf16 v[50:53], v[138:141], v[198:201], v[50:53]
	v_mfma_f32_16x16x32_bf16 v[38:41], v[130:133], v[206:209], v[38:41]
	v_mfma_f32_16x16x32_bf16 v[34:37], v[138:141], v[206:209], v[34:37]
	v_mfma_f32_16x16x32_bf16 v[22:25], v[130:133], v[214:217], v[22:25]
	v_mfma_f32_16x16x32_bf16 v[18:21], v[138:141], v[214:217], v[18:21]
	v_mfma_f32_16x16x32_bf16 v[6:9], v[130:133], v[222:225], v[6:9]
	v_mfma_f32_16x16x32_bf16 v[2:5], v[138:141], v[222:225], v[2:5]
	v_mfma_f32_16x16x32_bf16 v[54:57], v[134:137], v[202:205], v[54:57]
	v_mfma_f32_16x16x32_bf16 v[50:53], v[142:145], v[202:205], v[50:53]
	v_mfma_f32_16x16x32_bf16 v[38:41], v[134:137], v[210:213], v[38:41]
	v_mfma_f32_16x16x32_bf16 v[34:37], v[142:145], v[210:213], v[34:37]
	v_mfma_f32_16x16x32_bf16 v[22:25], v[134:137], v[218:221], v[22:25]
	v_mfma_f32_16x16x32_bf16 v[18:21], v[142:145], v[218:221], v[18:21]
	v_mfma_f32_16x16x32_bf16 v[6:9], v[134:137], v[230:233], v[6:9]
	v_mfma_f32_16x16x32_bf16 v[2:5], v[142:145], v[230:233], v[2:5]
	s_setprio 0
	s_setprio 1
	v_mfma_f32_16x16x32_bf16 v[58:61], v[178:181], v[198:201], v[58:61]
	v_mfma_f32_16x16x32_bf16 v[62:65], v[190:193], v[198:201], v[62:65]
	v_mfma_f32_16x16x32_bf16 v[42:45], v[178:181], v[206:209], v[42:45]
	v_mfma_f32_16x16x32_bf16 v[46:49], v[190:193], v[206:209], v[46:49]
	v_mfma_f32_16x16x32_bf16 v[26:29], v[178:181], v[214:217], v[26:29]
	v_mfma_f32_16x16x32_bf16 v[30:33], v[190:193], v[214:217], v[30:33]
	v_mfma_f32_16x16x32_bf16 v[10:13], v[178:181], v[222:225], v[10:13]
	v_mfma_f32_16x16x32_bf16 v[14:17], v[190:193], v[222:225], v[14:17]
	v_mfma_f32_16x16x32_bf16 v[58:61], v[182:185], v[202:205], v[58:61]
	v_mfma_f32_16x16x32_bf16 v[62:65], v[194:197], v[202:205], v[62:65]
	v_mfma_f32_16x16x32_bf16 v[42:45], v[182:185], v[210:213], v[42:45]
	v_mfma_f32_16x16x32_bf16 v[46:49], v[194:197], v[210:213], v[46:49]
	v_mfma_f32_16x16x32_bf16 v[26:29], v[182:185], v[218:221], v[26:29]
	v_mfma_f32_16x16x32_bf16 v[30:33], v[194:197], v[218:221], v[30:33]
	v_mfma_f32_16x16x32_bf16 v[10:13], v[182:185], v[230:233], v[10:13]
	v_mfma_f32_16x16x32_bf16 v[14:17], v[194:197], v[230:233], v[14:17]
	s_setprio 0
	s_barrier
	s_add_i32 s45, 0, 0x18000
	s_add_i32 s47, 0, 0x1c000
	v_add_u32_e32 v142, s45, v163
	v_add_u32_e32 v158, s47, v163
	ds_read_b128 v[130:133], v142
	ds_read_b128 v[134:137], v142 offset:1024
	ds_read_b128 v[138:141], v142 offset:2048
	ds_read_b128 v[142:145], v142 offset:3072
	ds_read_b128 v[178:181], v158
	ds_read_b128 v[182:185], v158 offset:1024
	ds_read_b128 v[190:193], v158 offset:2048
	ds_read_b128 v[194:197], v158 offset:3072
	s_mov_b32 m0, s64
	v_lshl_add_u64 v[238:239], s[52:53], 0, v[154:155]
	ds_read_b128 v[198:201], v189 offset:32768
	ds_read_b128 v[202:205], v189 offset:33792
	ds_read_b128 v[206:209], v189 offset:34816
	ds_read_b128 v[210:213], v189 offset:35840
	ds_read_b128 v[214:217], v189 offset:36864
	ds_read_b128 v[218:221], v189 offset:37888
	ds_read_b128 v[222:225], v189 offset:38912
	ds_read_b128 v[230:233], v189 offset:39936
	global_load_lds_dwordx4 v[238:239], off
	v_lshl_add_u64 v[238:239], s[52:53], 0, v[156:157]
	s_mov_b32 m0, s65
	s_nop 0
	global_load_lds_dwordx4 v[238:239], off
	s_waitcnt vmcnt(8)
	s_waitcnt lgkmcnt(0)
	s_setprio 1
	s_barrier
	v_mfma_f32_16x16x32_bf16 v[126:129], v[130:133], v[198:201], v[126:129]
	v_mfma_f32_16x16x32_bf16 v[122:125], v[138:141], v[198:201], v[122:125]
	v_mfma_f32_16x16x32_bf16 v[110:113], v[130:133], v[206:209], v[110:113]
	v_mfma_f32_16x16x32_bf16 v[106:109], v[138:141], v[206:209], v[106:109]
	v_mfma_f32_16x16x32_bf16 v[94:97], v[130:133], v[214:217], v[94:97]
	v_mfma_f32_16x16x32_bf16 v[90:93], v[138:141], v[214:217], v[90:93]
	v_mfma_f32_16x16x32_bf16 v[78:81], v[130:133], v[222:225], v[78:81]
	v_mfma_f32_16x16x32_bf16 v[74:77], v[138:141], v[222:225], v[74:77]
	v_mfma_f32_16x16x32_bf16 v[126:129], v[134:137], v[202:205], v[126:129]
	v_mfma_f32_16x16x32_bf16 v[122:125], v[142:145], v[202:205], v[122:125]
	v_mfma_f32_16x16x32_bf16 v[110:113], v[134:137], v[210:213], v[110:113]
	v_mfma_f32_16x16x32_bf16 v[106:109], v[142:145], v[210:213], v[106:109]
	v_mfma_f32_16x16x32_bf16 v[94:97], v[134:137], v[218:221], v[94:97]
	v_mfma_f32_16x16x32_bf16 v[90:93], v[142:145], v[218:221], v[90:93]
	v_mfma_f32_16x16x32_bf16 v[78:81], v[134:137], v[230:233], v[78:81]
	v_mfma_f32_16x16x32_bf16 v[74:77], v[142:145], v[230:233], v[74:77]
	s_setprio 0
	s_setprio 1
	v_mfma_f32_16x16x32_bf16 v[118:121], v[178:181], v[198:201], v[118:121]
	v_mfma_f32_16x16x32_bf16 v[114:117], v[190:193], v[198:201], v[114:117]
	v_mfma_f32_16x16x32_bf16 v[102:105], v[178:181], v[206:209], v[102:105]
	v_mfma_f32_16x16x32_bf16 v[98:101], v[190:193], v[206:209], v[98:101]
	v_mfma_f32_16x16x32_bf16 v[86:89], v[178:181], v[214:217], v[86:89]
	v_mfma_f32_16x16x32_bf16 v[82:85], v[190:193], v[214:217], v[82:85]
	v_mfma_f32_16x16x32_bf16 v[70:73], v[178:181], v[222:225], v[70:73]
	v_mfma_f32_16x16x32_bf16 v[66:69], v[190:193], v[222:225], v[66:69]
	v_mfma_f32_16x16x32_bf16 v[118:121], v[182:185], v[202:205], v[118:121]
	v_mfma_f32_16x16x32_bf16 v[114:117], v[194:197], v[202:205], v[114:117]
	v_mfma_f32_16x16x32_bf16 v[102:105], v[182:185], v[210:213], v[102:105]
	v_mfma_f32_16x16x32_bf16 v[98:101], v[194:197], v[210:213], v[98:101]
	v_mfma_f32_16x16x32_bf16 v[86:89], v[182:185], v[218:221], v[86:89]
	v_mfma_f32_16x16x32_bf16 v[82:85], v[194:197], v[218:221], v[82:85]
	v_mfma_f32_16x16x32_bf16 v[70:73], v[182:185], v[230:233], v[70:73]
	v_mfma_f32_16x16x32_bf16 v[66:69], v[194:197], v[230:233], v[66:69]
	s_setprio 0
	s_barrier
	s_add_i32 s45, s45, s61
	v_lshl_add_u64 v[186:187], v[186:187], 0, s[18:19]
	s_mov_b32 m0, s45
	ds_read_b128 v[198:201], v189 offset:49152
	ds_read_b128 v[202:205], v189 offset:50176
	ds_read_b128 v[206:209], v189 offset:51200
	ds_read_b128 v[210:213], v189 offset:52224
	ds_read_b128 v[214:217], v189 offset:53248
	ds_read_b128 v[218:221], v189 offset:54272
	ds_read_b128 v[222:225], v189 offset:55296
	ds_read_b128 v[230:233], v189 offset:56320
	global_load_lds_dwordx4 v[186:187], off
	s_add_i32 m0, s45, 0x2000
	s_add_u32 s42, s42, 0x80080
	v_lshl_add_u64 v[186:187], v[226:227], 0, s[18:19]
	s_addc_u32 s43, s43, 0
	s_add_i32 s45, s47, s61
	global_load_lds_dwordx4 v[186:187], off
	v_lshl_add_u64 v[186:187], s[42:43], 0, v[146:147]
	s_mov_b32 m0, s45
	s_nop 0
	global_load_lds_dwordx4 v[186:187], off
	v_lshl_add_u64 v[186:187], s[42:43], 0, v[148:149]
	s_add_i32 m0, s45, 0x2000
	s_nop 0
	global_load_lds_dwordx4 v[186:187], off
	v_lshl_add_u64 v[186:187], v[234:235], 0, s[18:19]
	s_mov_b32 m0, s68
	s_nop 0
	global_load_lds_dwordx4 v[186:187], off
	v_lshl_add_u64 v[186:187], v[236:237], 0, s[18:19]
	s_mov_b32 m0, s69
	s_nop 0
	global_load_lds_dwordx4 v[186:187], off
	s_waitcnt vmcnt(8)
	s_waitcnt lgkmcnt(0)
	s_setprio 1
	s_barrier
	v_mfma_f32_16x16x32_bf16 v[54:57], v[130:133], v[198:201], v[54:57]
	v_mfma_f32_16x16x32_bf16 v[50:53], v[138:141], v[198:201], v[50:53]
	v_mfma_f32_16x16x32_bf16 v[38:41], v[130:133], v[206:209], v[38:41]
	v_mfma_f32_16x16x32_bf16 v[34:37], v[138:141], v[206:209], v[34:37]
	v_mfma_f32_16x16x32_bf16 v[22:25], v[130:133], v[214:217], v[22:25]
	v_mfma_f32_16x16x32_bf16 v[18:21], v[138:141], v[214:217], v[18:21]
	v_mfma_f32_16x16x32_bf16 v[6:9], v[130:133], v[222:225], v[6:9]
	v_mfma_f32_16x16x32_bf16 v[2:5], v[138:141], v[222:225], v[2:5]
	v_mfma_f32_16x16x32_bf16 v[54:57], v[134:137], v[202:205], v[54:57]
	v_mfma_f32_16x16x32_bf16 v[50:53], v[142:145], v[202:205], v[50:53]
	v_mfma_f32_16x16x32_bf16 v[38:41], v[134:137], v[210:213], v[38:41]
	v_mfma_f32_16x16x32_bf16 v[34:37], v[142:145], v[210:213], v[34:37]
	v_mfma_f32_16x16x32_bf16 v[22:25], v[134:137], v[218:221], v[22:25]
	v_mfma_f32_16x16x32_bf16 v[18:21], v[142:145], v[218:221], v[18:21]
	v_mfma_f32_16x16x32_bf16 v[6:9], v[134:137], v[230:233], v[6:9]
	v_mfma_f32_16x16x32_bf16 v[2:5], v[142:145], v[230:233], v[2:5]
	s_setprio 0
	s_setprio 1
	v_mfma_f32_16x16x32_bf16 v[58:61], v[178:181], v[198:201], v[58:61]
	v_mfma_f32_16x16x32_bf16 v[62:65], v[190:193], v[198:201], v[62:65]
	v_mfma_f32_16x16x32_bf16 v[42:45], v[178:181], v[206:209], v[42:45]
	v_mfma_f32_16x16x32_bf16 v[46:49], v[190:193], v[206:209], v[46:49]
	v_mfma_f32_16x16x32_bf16 v[26:29], v[178:181], v[214:217], v[26:29]
	v_mfma_f32_16x16x32_bf16 v[30:33], v[190:193], v[214:217], v[30:33]
	v_mfma_f32_16x16x32_bf16 v[10:13], v[178:181], v[222:225], v[10:13]
	v_mfma_f32_16x16x32_bf16 v[14:17], v[190:193], v[222:225], v[14:17]
	v_mfma_f32_16x16x32_bf16 v[58:61], v[182:185], v[202:205], v[58:61]
	v_mfma_f32_16x16x32_bf16 v[62:65], v[194:197], v[202:205], v[62:65]
	v_mfma_f32_16x16x32_bf16 v[42:45], v[182:185], v[210:213], v[42:45]
	v_mfma_f32_16x16x32_bf16 v[46:49], v[194:197], v[210:213], v[46:49]
	v_mfma_f32_16x16x32_bf16 v[26:29], v[182:185], v[218:221], v[26:29]
	v_mfma_f32_16x16x32_bf16 v[30:33], v[194:197], v[218:221], v[30:33]
	v_mfma_f32_16x16x32_bf16 v[10:13], v[182:185], v[230:233], v[10:13]
	v_mfma_f32_16x16x32_bf16 v[14:17], v[194:197], v[230:233], v[14:17]
	s_setprio 0
	s_barrier
	s_add_i32 s33, s33, 2
	s_add_u32 s8, s8, 0x100
	s_addc_u32 s9, s9, 0
	s_add_u32 s5, s5, 0x100
	s_addc_u32 s14, s14, 0
	s_cmp_gt_u32 s33, 29
	s_cbranch_scc0 .LBB0_289
	s_and_b64 vcc, exec, s[20:21]
	s_cbranch_vccz .LBB0_292
	s_barrier

.LBB0_421:
	ds_read_b128 v[18:21], v196
	ds_read_b128 v[22:25], v196 offset:1024
	ds_read_b128 v[26:29], v196 offset:2048
	ds_read_b128 v[30:33], v196 offset:3072
	ds_read_b128 v[2:5], v197
	ds_read_b128 v[6:9], v197 offset:1024
	ds_read_b128 v[10:13], v197 offset:2048
	ds_read_b128 v[14:17], v197 offset:3072
	s_add_u32 s38, s36, 0x80
	s_addc_u32 s39, s37, 0
	s_cmp_eq_u32 s59, 12
	s_cselect_b32 s41, s29, s39
	s_cselect_b32 s40, s28, s38
	s_cselect_b32 s39, s31, s58
	s_cselect_b32 s38, s30, s27
	v_lshl_add_u64 v[224:225], s[36:37], 0, v[180:181]
	s_add_i32 m0, s35, 0xc000
	ds_read_b128 v[186:189], v198
	ds_read_b128 v[190:193], v198 offset:1024
	ds_read_b128 v[200:203], v198 offset:2048
	ds_read_b128 v[204:207], v198 offset:3072
	ds_read_b128 v[208:211], v198 offset:4096
	ds_read_b128 v[212:215], v198 offset:5120
	ds_read_b128 v[216:219], v198 offset:6144
	ds_read_b128 v[220:223], v198 offset:7168
	global_load_lds_dwordx4 v[224:225], off
	v_lshl_add_u64 v[224:225], s[36:37], 0, v[178:179]
	s_add_i32 m0, s35, 0xe000
	s_nop 0
	global_load_lds_dwordx4 v[224:225], off
	s_waitcnt vmcnt(8)
	s_waitcnt lgkmcnt(0)
	s_setprio 1
	s_barrier
	s_nop 1
	v_mfma_f32_16x16x128_f8f6f4 v[158:161], v[18:25], v[186:193], v[158:161]
	v_mfma_f32_16x16x128_f8f6f4 v[154:157], v[26:33], v[186:193], v[154:157]
	v_mfma_f32_16x16x128_f8f6f4 v[142:145], v[18:25], v[200:207], v[142:145]
	v_mfma_f32_16x16x128_f8f6f4 v[138:141], v[26:33], v[200:207], v[138:141]
	v_mfma_f32_16x16x128_f8f6f4 v[126:129], v[18:25], v[208:215], v[126:129]
	v_mfma_f32_16x16x128_f8f6f4 v[122:125], v[26:33], v[208:215], v[122:125]
	v_mfma_f32_16x16x128_f8f6f4 v[110:113], v[18:25], v[216:223], v[110:113]
	v_mfma_f32_16x16x128_f8f6f4 v[106:109], v[26:33], v[216:223], v[106:109]
	s_setprio 0
	s_setprio 1
	s_nop 1
	v_mfma_f32_16x16x128_f8f6f4 v[150:153], v[2:9], v[186:193], v[150:153]
	v_mfma_f32_16x16x128_f8f6f4 v[146:149], v[10:17], v[186:193], v[146:149]
	v_mfma_f32_16x16x128_f8f6f4 v[134:137], v[2:9], v[200:207], v[134:137]
	v_mfma_f32_16x16x128_f8f6f4 v[130:133], v[10:17], v[200:207], v[130:133]
	v_mfma_f32_16x16x128_f8f6f4 v[118:121], v[2:9], v[208:215], v[118:121]
	v_mfma_f32_16x16x128_f8f6f4 v[114:117], v[10:17], v[208:215], v[114:117]
	v_mfma_f32_16x16x128_f8f6f4 v[102:105], v[2:9], v[216:223], v[102:105]
	v_mfma_f32_16x16x128_f8f6f4 v[98:101], v[10:17], v[216:223], v[98:101]
	s_setprio 0
	s_barrier
	s_add_i32 s60, s49, s42
	v_lshl_add_u64 v[186:187], s[38:39], 0, v[162:163]
	s_mov_b32 m0, s60
	ds_read_b128 v[200:203], v198 offset:16384
	ds_read_b128 v[204:207], v198 offset:17408
	ds_read_b128 v[208:211], v198 offset:18432
	ds_read_b128 v[212:215], v198 offset:19456
	ds_read_b128 v[216:219], v198 offset:20480
	ds_read_b128 v[220:223], v198 offset:21504
	ds_read_b128 v[230:233], v198 offset:22528
	ds_read_b128 v[234:237], v198 offset:23552
	global_load_lds_dwordx4 v[186:187], off
	s_add_i32 m0, s60, 0x2000
	s_add_u32 s60, s38, 0x40000
	v_lshl_add_u64 v[188:189], s[38:39], 0, v[164:165]
	s_addc_u32 s61, s39, 0
	s_add_i32 s62, s53, s42
	global_load_lds_dwordx4 v[188:189], off
	v_lshl_add_u64 v[190:191], s[60:61], 0, v[162:163]
	s_mov_b32 m0, s62
	v_lshl_add_u64 v[192:193], s[40:41], 0, v[168:169]
	global_load_lds_dwordx4 v[190:191], off
	v_lshl_add_u64 v[190:191], s[60:61], 0, v[164:165]
	s_add_i32 m0, s62, 0x2000
	s_nop 0
	global_load_lds_dwordx4 v[190:191], off
	v_lshl_add_u64 v[190:191], s[40:41], 0, v[166:167]
	s_mov_b32 m0, s35
	s_nop 0
	global_load_lds_dwordx4 v[190:191], off
	s_mov_b32 m0, s43
	s_nop 0
	global_load_lds_dwordx4 v[192:193], off
	s_waitcnt vmcnt(8)
	s_waitcnt lgkmcnt(0)
	s_setprio 1
	s_barrier
	s_nop 1
	v_mfma_f32_16x16x128_f8f6f4 v[90:93], v[18:25], v[200:207], v[90:93]
	v_mfma_f32_16x16x128_f8f6f4 v[82:85], v[26:33], v[200:207], v[82:85]
	v_mfma_f32_16x16x128_f8f6f4 v[70:73], v[18:25], v[208:215], v[70:73]
	v_mfma_f32_16x16x128_f8f6f4 v[66:69], v[26:33], v[208:215], v[66:69]
	v_mfma_f32_16x16x128_f8f6f4 v[54:57], v[18:25], v[216:223], v[54:57]
	v_mfma_f32_16x16x128_f8f6f4 v[50:53], v[26:33], v[216:223], v[50:53]
	v_mfma_f32_16x16x128_f8f6f4 v[38:41], v[18:25], v[230:237], v[38:41]
	v_mfma_f32_16x16x128_f8f6f4 v[34:37], v[26:33], v[230:237], v[34:37]
	s_setprio 0
	s_setprio 1
	s_nop 1
	v_mfma_f32_16x16x128_f8f6f4 v[94:97], v[2:9], v[200:207], v[94:97]
	v_mfma_f32_16x16x128_f8f6f4 v[86:89], v[10:17], v[200:207], v[86:89]
	v_mfma_f32_16x16x128_f8f6f4 v[78:81], v[2:9], v[208:215], v[78:81]
	v_mfma_f32_16x16x128_f8f6f4 v[74:77], v[10:17], v[208:215], v[74:77]
	v_mfma_f32_16x16x128_f8f6f4 v[62:65], v[2:9], v[216:223], v[62:65]
	v_mfma_f32_16x16x128_f8f6f4 v[58:61], v[10:17], v[216:223], v[58:61]
	v_mfma_f32_16x16x128_f8f6f4 v[46:49], v[2:9], v[230:237], v[46:49]
	v_mfma_f32_16x16x128_f8f6f4 v[42:45], v[10:17], v[230:237], v[42:45]
	s_setprio 0
	s_barrier
	s_add_i32 s60, 0, 0x18000
	s_add_i32 s61, 0, 0x1c000
	v_add_u32_e32 v14, s60, v194
	v_add_u32_e32 v30, s61, v194
	ds_read_b128 v[2:5], v14
	ds_read_b128 v[6:9], v14 offset:1024
	ds_read_b128 v[10:13], v14 offset:2048
	ds_read_b128 v[14:17], v14 offset:3072
	ds_read_b128 v[18:21], v30
	ds_read_b128 v[22:25], v30 offset:1024
	ds_read_b128 v[26:29], v30 offset:2048
	ds_read_b128 v[30:33], v30 offset:3072
	s_mov_b32 m0, s44
	v_lshl_add_u64 v[224:225], s[40:41], 0, v[170:171]
	ds_read_b128 v[200:203], v198 offset:32768
	ds_read_b128 v[204:207], v198 offset:33792
	ds_read_b128 v[208:211], v198 offset:34816
	ds_read_b128 v[212:215], v198 offset:35840
	ds_read_b128 v[216:219], v198 offset:36864
	ds_read_b128 v[220:223], v198 offset:37888
	ds_read_b128 v[230:233], v198 offset:38912
	ds_read_b128 v[234:237], v198 offset:39936
	global_load_lds_dwordx4 v[224:225], off
	v_lshl_add_u64 v[224:225], s[40:41], 0, v[172:173]
	s_mov_b32 m0, s45
	s_nop 0
	global_load_lds_dwordx4 v[224:225], off
	s_waitcnt vmcnt(8)
	s_waitcnt lgkmcnt(0)
	s_setprio 1
	s_barrier
	s_nop 1
	v_mfma_f32_16x16x128_f8f6f4 v[158:161], v[2:9], v[200:207], v[158:161]
	v_mfma_f32_16x16x128_f8f6f4 v[154:157], v[10:17], v[200:207], v[154:157]
	v_mfma_f32_16x16x128_f8f6f4 v[142:145], v[2:9], v[208:215], v[142:145]
	v_mfma_f32_16x16x128_f8f6f4 v[138:141], v[10:17], v[208:215], v[138:141]
	v_mfma_f32_16x16x128_f8f6f4 v[126:129], v[2:9], v[216:223], v[126:129]
	v_mfma_f32_16x16x128_f8f6f4 v[122:125], v[10:17], v[216:223], v[122:125]
	v_mfma_f32_16x16x128_f8f6f4 v[110:113], v[2:9], v[230:237], v[110:113]
	v_mfma_f32_16x16x128_f8f6f4 v[106:109], v[10:17], v[230:237], v[106:109]
	s_setprio 0
	s_setprio 1
	s_nop 1
	v_mfma_f32_16x16x128_f8f6f4 v[150:153], v[18:25], v[200:207], v[150:153]
	v_mfma_f32_16x16x128_f8f6f4 v[146:149], v[26:33], v[200:207], v[146:149]
	v_mfma_f32_16x16x128_f8f6f4 v[134:137], v[18:25], v[208:215], v[134:137]
	v_mfma_f32_16x16x128_f8f6f4 v[130:133], v[26:33], v[208:215], v[130:133]
	v_mfma_f32_16x16x128_f8f6f4 v[118:121], v[18:25], v[216:223], v[118:121]
	v_mfma_f32_16x16x128_f8f6f4 v[114:117], v[26:33], v[216:223], v[114:117]
	v_mfma_f32_16x16x128_f8f6f4 v[102:105], v[18:25], v[230:237], v[102:105]
	v_mfma_f32_16x16x128_f8f6f4 v[98:101], v[26:33], v[230:237], v[98:101]
	s_setprio 0
	s_barrier
	s_add_i32 s40, s60, s42
	v_lshl_add_u64 v[186:187], v[186:187], 0, s[14:15]
	s_mov_b32 m0, s40
	ds_read_b128 v[200:203], v198 offset:49152
	ds_read_b128 v[204:207], v198 offset:50176
	ds_read_b128 v[208:211], v198 offset:51200
	ds_read_b128 v[212:215], v198 offset:52224
	ds_read_b128 v[216:219], v198 offset:53248
	ds_read_b128 v[220:223], v198 offset:54272
	ds_read_b128 v[230:233], v198 offset:55296
	ds_read_b128 v[234:237], v198 offset:56320
	global_load_lds_dwordx4 v[186:187], off
	s_add_i32 m0, s40, 0x2000
	s_add_u32 s38, s38, 0x40080
	v_lshl_add_u64 v[186:187], v[188:189], 0, s[14:15]
	s_addc_u32 s39, s39, 0
	s_add_i32 s40, s61, s42
	global_load_lds_dwordx4 v[186:187], off
	v_lshl_add_u64 v[186:187], s[38:39], 0, v[162:163]
	s_mov_b32 m0, s40
	s_nop 0
	global_load_lds_dwordx4 v[186:187], off
	v_lshl_add_u64 v[186:187], s[38:39], 0, v[164:165]
	s_add_i32 m0, s40, 0x2000
	s_nop 0
	global_load_lds_dwordx4 v[186:187], off
	v_lshl_add_u64 v[186:187], v[190:191], 0, s[14:15]
	s_mov_b32 m0, s46
	s_nop 0
	global_load_lds_dwordx4 v[186:187], off
	v_lshl_add_u64 v[186:187], v[192:193], 0, s[14:15]
	s_mov_b32 m0, s47
	s_nop 0
	global_load_lds_dwordx4 v[186:187], off
	s_waitcnt vmcnt(8)
	s_waitcnt lgkmcnt(0)
	s_setprio 1
	s_barrier
	s_nop 1
	v_mfma_f32_16x16x128_f8f6f4 v[90:93], v[2:9], v[200:207], v[90:93]
	v_mfma_f32_16x16x128_f8f6f4 v[82:85], v[10:17], v[200:207], v[82:85]
	v_mfma_f32_16x16x128_f8f6f4 v[70:73], v[2:9], v[208:215], v[70:73]
	v_mfma_f32_16x16x128_f8f6f4 v[66:69], v[10:17], v[208:215], v[66:69]
	v_mfma_f32_16x16x128_f8f6f4 v[54:57], v[2:9], v[216:223], v[54:57]
	v_mfma_f32_16x16x128_f8f6f4 v[50:53], v[10:17], v[216:223], v[50:53]
	v_mfma_f32_16x16x128_f8f6f4 v[38:41], v[2:9], v[230:237], v[38:41]
	v_mfma_f32_16x16x128_f8f6f4 v[34:37], v[10:17], v[230:237], v[34:37]
	s_setprio 0
	s_setprio 1
	s_nop 1
	v_mfma_f32_16x16x128_f8f6f4 v[94:97], v[18:25], v[200:207], v[94:97]
	v_mfma_f32_16x16x128_f8f6f4 v[86:89], v[26:33], v[200:207], v[86:89]
	v_mfma_f32_16x16x128_f8f6f4 v[78:81], v[18:25], v[208:215], v[78:81]
	v_mfma_f32_16x16x128_f8f6f4 v[74:77], v[26:33], v[208:215], v[74:77]
	v_mfma_f32_16x16x128_f8f6f4 v[62:65], v[18:25], v[216:223], v[62:65]
	v_mfma_f32_16x16x128_f8f6f4 v[58:61], v[26:33], v[216:223], v[58:61]
	v_mfma_f32_16x16x128_f8f6f4 v[46:49], v[18:25], v[230:237], v[46:49]
	v_mfma_f32_16x16x128_f8f6f4 v[42:45], v[26:33], v[230:237], v[42:45]
	s_setprio 0
	s_barrier
	s_add_i32 s59, s59, 2
	s_add_u32 s36, s36, 0x100
	s_addc_u32 s37, s37, 0
	s_add_u32 s27, s27, 0x100
	s_addc_u32 s58, s58, 0
	s_cmp_gt_u32 s59, 13
	s_cbranch_scc0 .LBB0_421
	s_and_b64 vcc, exec, s[2:3]
	s_cbranch_vccz .LBB0_424
	s_barrier

.LBB0_459:
	s_and_b64 s[46:47], s[38:39], exec
	s_cselect_b32 s48, s35, s43
	s_cselect_b32 s49, s34, s42
	s_cselect_b32 s66, s37, s45
	s_cselect_b32 s67, s36, s44
	s_add_u32 s42, s42, 0x80
	s_addc_u32 s43, s43, 0
	s_add_u32 s68, s44, 0x100
	s_addc_u32 s69, s45, 0
	s_mov_b32 s70, -2
	ds_read_b128 v[18:21], v194
	ds_read_b128 v[22:25], v194 offset:1024
	ds_read_b128 v[26:29], v194 offset:2048
	ds_read_b128 v[30:33], v194 offset:3072
	ds_read_b128 v[2:5], v195
	ds_read_b128 v[6:9], v195 offset:1024
	ds_read_b128 v[10:13], v195 offset:2048
	ds_read_b128 v[14:17], v195 offset:3072
	s_add_u32 s44, s42, 0x80
	s_addc_u32 s45, s43, 0
	s_cmp_eq_u32 s70, 12
	s_cselect_b32 s47, s48, s45
	s_cselect_b32 s46, s49, s44
	s_cselect_b32 s45, s66, s69
	s_cselect_b32 s44, s67, s68
	v_lshl_add_u64 v[222:223], s[42:43], 0, v[180:181]
	s_add_i32 m0, s41, 0xc000
	ds_read_b128 v[184:187], v196
	ds_read_b128 v[188:191], v196 offset:1024
	ds_read_b128 v[198:201], v196 offset:2048
	ds_read_b128 v[202:205], v196 offset:3072
	ds_read_b128 v[206:209], v196 offset:4096
	ds_read_b128 v[210:213], v196 offset:5120
	ds_read_b128 v[214:217], v196 offset:6144
	ds_read_b128 v[218:221], v196 offset:7168
	global_load_lds_dwordx4 v[222:223], off
	v_lshl_add_u64 v[222:223], s[42:43], 0, v[178:179]
	s_add_i32 m0, s41, 0xe000
	s_nop 0
	global_load_lds_dwordx4 v[222:223], off
	s_waitcnt vmcnt(8)
	s_waitcnt lgkmcnt(0)
	s_setprio 1
	s_barrier
	s_nop 1
	v_mfma_f32_16x16x128_f8f6f4 v[158:161], v[18:25], v[184:191], 0
	v_mfma_f32_16x16x128_f8f6f4 v[154:157], v[26:33], v[184:191], 0
	v_mfma_f32_16x16x128_f8f6f4 v[142:145], v[18:25], v[198:205], 0
	v_mfma_f32_16x16x128_f8f6f4 v[138:141], v[26:33], v[198:205], 0
	v_mfma_f32_16x16x128_f8f6f4 v[126:129], v[18:25], v[206:213], 0
	v_mfma_f32_16x16x128_f8f6f4 v[122:125], v[26:33], v[206:213], 0
	v_mfma_f32_16x16x128_f8f6f4 v[110:113], v[18:25], v[214:221], 0
	v_mfma_f32_16x16x128_f8f6f4 v[106:109], v[26:33], v[214:221], 0
	s_setprio 0
	s_setprio 1
	s_nop 1
	v_mfma_f32_16x16x128_f8f6f4 v[150:153], v[2:9], v[184:191], 0
	v_mfma_f32_16x16x128_f8f6f4 v[146:149], v[10:17], v[184:191], 0
	v_mfma_f32_16x16x128_f8f6f4 v[134:137], v[2:9], v[198:205], 0
	v_mfma_f32_16x16x128_f8f6f4 v[130:133], v[10:17], v[198:205], 0
	v_mfma_f32_16x16x128_f8f6f4 v[118:121], v[2:9], v[206:213], 0
	v_mfma_f32_16x16x128_f8f6f4 v[114:117], v[10:17], v[206:213], 0
	v_mfma_f32_16x16x128_f8f6f4 v[102:105], v[2:9], v[214:221], 0
	v_mfma_f32_16x16x128_f8f6f4 v[98:101], v[10:17], v[214:221], 0
	s_setprio 0
	s_barrier
	s_add_i32 s71, s61, s53
	v_lshl_add_u64 v[184:185], s[44:45], 0, v[162:163]
	s_mov_b32 m0, s71
	ds_read_b128 v[198:201], v196 offset:16384
	ds_read_b128 v[202:205], v196 offset:17408
	ds_read_b128 v[206:209], v196 offset:18432
	ds_read_b128 v[210:213], v196 offset:19456
	ds_read_b128 v[214:217], v196 offset:20480
	ds_read_b128 v[218:221], v196 offset:21504
	ds_read_b128 v[230:233], v196 offset:22528
	ds_read_b128 v[234:237], v196 offset:23552
	global_load_lds_dwordx4 v[184:185], off
	s_add_i32 m0, s71, 0x2000
	s_add_u32 s72, s44, 0x40000
	v_lshl_add_u64 v[186:187], s[44:45], 0, v[164:165]
	s_addc_u32 s73, s45, 0
	s_add_i32 s71, s62, s53
	global_load_lds_dwordx4 v[186:187], off
	v_lshl_add_u64 v[188:189], s[72:73], 0, v[162:163]
	s_mov_b32 m0, s71
	v_lshl_add_u64 v[190:191], s[46:47], 0, v[168:169]
	global_load_lds_dwordx4 v[188:189], off
	v_lshl_add_u64 v[188:189], s[72:73], 0, v[164:165]
	s_add_i32 m0, s71, 0x2000
	s_nop 0
	global_load_lds_dwordx4 v[188:189], off
	v_lshl_add_u64 v[188:189], s[46:47], 0, v[166:167]
	s_mov_b32 m0, s41
	s_nop 0
	global_load_lds_dwordx4 v[188:189], off
	s_mov_b32 m0, s54
	s_nop 0
	global_load_lds_dwordx4 v[190:191], off
	s_waitcnt vmcnt(8)
	s_waitcnt lgkmcnt(0)
	s_setprio 1
	s_barrier
	s_nop 1
	v_mfma_f32_16x16x128_f8f6f4 v[90:93], v[18:25], v[198:205], 0
	v_mfma_f32_16x16x128_f8f6f4 v[82:85], v[26:33], v[198:205], 0
	v_mfma_f32_16x16x128_f8f6f4 v[70:73], v[18:25], v[206:213], 0
	v_mfma_f32_16x16x128_f8f6f4 v[66:69], v[26:33], v[206:213], 0
	v_mfma_f32_16x16x128_f8f6f4 v[54:57], v[18:25], v[214:221], 0
	v_mfma_f32_16x16x128_f8f6f4 v[50:53], v[26:33], v[214:221], 0
	v_mfma_f32_16x16x128_f8f6f4 v[38:41], v[18:25], v[230:237], 0
	v_mfma_f32_16x16x128_f8f6f4 v[34:37], v[26:33], v[230:237], 0
	s_setprio 0
	s_setprio 1
	s_nop 1
	v_mfma_f32_16x16x128_f8f6f4 v[94:97], v[2:9], v[198:205], 0
	v_mfma_f32_16x16x128_f8f6f4 v[86:89], v[10:17], v[198:205], 0
	v_mfma_f32_16x16x128_f8f6f4 v[78:81], v[2:9], v[206:213], 0
	v_mfma_f32_16x16x128_f8f6f4 v[74:77], v[10:17], v[206:213], 0
	v_mfma_f32_16x16x128_f8f6f4 v[62:65], v[2:9], v[214:221], 0
	v_mfma_f32_16x16x128_f8f6f4 v[58:61], v[10:17], v[214:221], 0
	v_mfma_f32_16x16x128_f8f6f4 v[46:49], v[2:9], v[230:237], 0
	v_mfma_f32_16x16x128_f8f6f4 v[42:45], v[10:17], v[230:237], 0
	s_setprio 0
	s_barrier
	s_add_i32 s71, 0, 0x18000
	s_add_i32 s72, 0, 0x1c000
	v_add_u32_e32 v14, s71, v192
	v_add_u32_e32 v30, s72, v192
	ds_read_b128 v[2:5], v14
	ds_read_b128 v[6:9], v14 offset:1024
	ds_read_b128 v[10:13], v14 offset:2048
	ds_read_b128 v[14:17], v14 offset:3072
	ds_read_b128 v[18:21], v30
	ds_read_b128 v[22:25], v30 offset:1024
	ds_read_b128 v[26:29], v30 offset:2048
	ds_read_b128 v[30:33], v30 offset:3072
	s_mov_b32 m0, s55
	v_lshl_add_u64 v[222:223], s[46:47], 0, v[170:171]
	ds_read_b128 v[198:201], v196 offset:32768
	ds_read_b128 v[202:205], v196 offset:33792
	ds_read_b128 v[206:209], v196 offset:34816
	ds_read_b128 v[210:213], v196 offset:35840
	ds_read_b128 v[214:217], v196 offset:36864
	ds_read_b128 v[218:221], v196 offset:37888
	ds_read_b128 v[230:233], v196 offset:38912
	ds_read_b128 v[234:237], v196 offset:39936
	global_load_lds_dwordx4 v[222:223], off
	v_lshl_add_u64 v[222:223], s[46:47], 0, v[172:173]
	s_mov_b32 m0, s58
	s_nop 0
	global_load_lds_dwordx4 v[222:223], off
	s_waitcnt vmcnt(8)
	s_waitcnt lgkmcnt(0)
	s_setprio 1
	s_barrier
	s_nop 1
	v_mfma_f32_16x16x128_f8f6f4 v[158:161], v[2:9], v[198:205], v[158:161]
	v_mfma_f32_16x16x128_f8f6f4 v[154:157], v[10:17], v[198:205], v[154:157]
	v_mfma_f32_16x16x128_f8f6f4 v[142:145], v[2:9], v[206:213], v[142:145]
	v_mfma_f32_16x16x128_f8f6f4 v[138:141], v[10:17], v[206:213], v[138:141]
	v_mfma_f32_16x16x128_f8f6f4 v[126:129], v[2:9], v[214:221], v[126:129]
	v_mfma_f32_16x16x128_f8f6f4 v[122:125], v[10:17], v[214:221], v[122:125]
	v_mfma_f32_16x16x128_f8f6f4 v[110:113], v[2:9], v[230:237], v[110:113]
	v_mfma_f32_16x16x128_f8f6f4 v[106:109], v[10:17], v[230:237], v[106:109]
	s_setprio 0
	s_setprio 1
	s_nop 1
	v_mfma_f32_16x16x128_f8f6f4 v[150:153], v[18:25], v[198:205], v[150:153]
	v_mfma_f32_16x16x128_f8f6f4 v[146:149], v[26:33], v[198:205], v[146:149]
	v_mfma_f32_16x16x128_f8f6f4 v[134:137], v[18:25], v[206:213], v[134:137]
	v_mfma_f32_16x16x128_f8f6f4 v[130:133], v[26:33], v[206:213], v[130:133]
	v_mfma_f32_16x16x128_f8f6f4 v[118:121], v[18:25], v[214:221], v[118:121]
	v_mfma_f32_16x16x128_f8f6f4 v[114:117], v[26:33], v[214:221], v[114:117]
	v_mfma_f32_16x16x128_f8f6f4 v[102:105], v[18:25], v[230:237], v[102:105]
	v_mfma_f32_16x16x128_f8f6f4 v[98:101], v[26:33], v[230:237], v[98:101]
	s_setprio 0
	s_barrier
	s_add_i32 s46, s71, s53
	v_lshl_add_u64 v[184:185], v[184:185], 0, s[12:13]
	s_mov_b32 m0, s46
	ds_read_b128 v[198:201], v196 offset:49152
	ds_read_b128 v[202:205], v196 offset:50176
	ds_read_b128 v[206:209], v196 offset:51200
	ds_read_b128 v[210:213], v196 offset:52224
	ds_read_b128 v[214:217], v196 offset:53248
	ds_read_b128 v[218:221], v196 offset:54272
	ds_read_b128 v[230:233], v196 offset:55296
	ds_read_b128 v[234:237], v196 offset:56320
	global_load_lds_dwordx4 v[184:185], off
	s_add_i32 m0, s46, 0x2000
	s_add_u32 s44, s44, 0x40080
	v_lshl_add_u64 v[184:185], v[186:187], 0, s[12:13]
	s_addc_u32 s45, s45, 0
	s_add_i32 s46, s72, s53
	global_load_lds_dwordx4 v[184:185], off
	v_lshl_add_u64 v[184:185], s[44:45], 0, v[162:163]
	s_mov_b32 m0, s46
	s_nop 0
	global_load_lds_dwordx4 v[184:185], off
	v_lshl_add_u64 v[184:185], s[44:45], 0, v[164:165]
	s_add_i32 m0, s46, 0x2000
	s_nop 0
	global_load_lds_dwordx4 v[184:185], off
	v_lshl_add_u64 v[184:185], v[188:189], 0, s[12:13]
	s_mov_b32 m0, s59
	s_nop 0
	global_load_lds_dwordx4 v[184:185], off
	v_lshl_add_u64 v[184:185], v[190:191], 0, s[12:13]
	s_mov_b32 m0, s60
	s_nop 0
	global_load_lds_dwordx4 v[184:185], off
	s_waitcnt vmcnt(8)
	s_waitcnt lgkmcnt(0)
	s_setprio 1
	s_barrier
	s_nop 1
	v_mfma_f32_16x16x128_f8f6f4 v[90:93], v[2:9], v[198:205], v[90:93]
	v_mfma_f32_16x16x128_f8f6f4 v[82:85], v[10:17], v[198:205], v[82:85]
	v_mfma_f32_16x16x128_f8f6f4 v[70:73], v[2:9], v[206:213], v[70:73]
	v_mfma_f32_16x16x128_f8f6f4 v[66:69], v[10:17], v[206:213], v[66:69]
	v_mfma_f32_16x16x128_f8f6f4 v[54:57], v[2:9], v[214:221], v[54:57]
	v_mfma_f32_16x16x128_f8f6f4 v[50:53], v[10:17], v[214:221], v[50:53]
	v_mfma_f32_16x16x128_f8f6f4 v[38:41], v[2:9], v[230:237], v[38:41]
	v_mfma_f32_16x16x128_f8f6f4 v[34:37], v[10:17], v[230:237], v[34:37]
	s_setprio 0
	s_setprio 1
	s_nop 1
	v_mfma_f32_16x16x128_f8f6f4 v[94:97], v[18:25], v[198:205], v[94:97]
	v_mfma_f32_16x16x128_f8f6f4 v[86:89], v[26:33], v[198:205], v[86:89]
	v_mfma_f32_16x16x128_f8f6f4 v[78:81], v[18:25], v[206:213], v[78:81]
	v_mfma_f32_16x16x128_f8f6f4 v[74:77], v[26:33], v[206:213], v[74:77]
	v_mfma_f32_16x16x128_f8f6f4 v[62:65], v[18:25], v[214:221], v[62:65]
	v_mfma_f32_16x16x128_f8f6f4 v[58:61], v[26:33], v[214:221], v[58:61]
	v_mfma_f32_16x16x128_f8f6f4 v[46:49], v[18:25], v[230:237], v[46:49]
	v_mfma_f32_16x16x128_f8f6f4 v[42:45], v[26:33], v[230:237], v[42:45]
	s_setprio 0
	s_barrier
	s_add_i32 s70, s70, 2
	s_add_u32 s42, s42, 0x100
	s_addc_u32 s43, s43, 0
	s_add_u32 s68, s68, 0x100
	s_addc_u32 s69, s69, 0
	s_cmp_gt_u32 s70, 13
	s_cbranch_scc0 .LBB0_460
	s_branch .Lmy_pexit_p1b
.LBB0_460:
	ds_read_b128 v[18:21], v194
	ds_read_b128 v[22:25], v194 offset:1024
	ds_read_b128 v[26:29], v194 offset:2048
	ds_read_b128 v[30:33], v194 offset:3072
	ds_read_b128 v[2:5], v195
	ds_read_b128 v[6:9], v195 offset:1024
	ds_read_b128 v[10:13], v195 offset:2048
	ds_read_b128 v[14:17], v195 offset:3072
	s_add_u32 s44, s42, 0x80
	s_addc_u32 s45, s43, 0
	s_cmp_eq_u32 s70, 12
	s_cselect_b32 s47, s48, s45
	s_cselect_b32 s46, s49, s44
	s_cselect_b32 s45, s66, s69
	s_cselect_b32 s44, s67, s68
	v_lshl_add_u64 v[222:223], s[42:43], 0, v[180:181]
	s_add_i32 m0, s41, 0xc000
	ds_read_b128 v[184:187], v196
	ds_read_b128 v[188:191], v196 offset:1024
	ds_read_b128 v[198:201], v196 offset:2048
	ds_read_b128 v[202:205], v196 offset:3072
	ds_read_b128 v[206:209], v196 offset:4096
	ds_read_b128 v[210:213], v196 offset:5120
	ds_read_b128 v[214:217], v196 offset:6144
	ds_read_b128 v[218:221], v196 offset:7168
	global_load_lds_dwordx4 v[222:223], off
	v_lshl_add_u64 v[222:223], s[42:43], 0, v[178:179]
	s_add_i32 m0, s41, 0xe000
	s_nop 0
	global_load_lds_dwordx4 v[222:223], off
	s_waitcnt vmcnt(8)
	s_waitcnt lgkmcnt(0)
	s_setprio 1
	s_barrier
	s_nop 1
	v_mfma_f32_16x16x128_f8f6f4 v[158:161], v[18:25], v[184:191], v[158:161]
	v_mfma_f32_16x16x128_f8f6f4 v[154:157], v[26:33], v[184:191], v[154:157]
	v_mfma_f32_16x16x128_f8f6f4 v[142:145], v[18:25], v[198:205], v[142:145]
	v_mfma_f32_16x16x128_f8f6f4 v[138:141], v[26:33], v[198:205], v[138:141]
	v_mfma_f32_16x16x128_f8f6f4 v[126:129], v[18:25], v[206:213], v[126:129]
	v_mfma_f32_16x16x128_f8f6f4 v[122:125], v[26:33], v[206:213], v[122:125]
	v_mfma_f32_16x16x128_f8f6f4 v[110:113], v[18:25], v[214:221], v[110:113]
	v_mfma_f32_16x16x128_f8f6f4 v[106:109], v[26:33], v[214:221], v[106:109]
	s_setprio 0
	s_setprio 1
	s_nop 1
	v_mfma_f32_16x16x128_f8f6f4 v[150:153], v[2:9], v[184:191], v[150:153]
	v_mfma_f32_16x16x128_f8f6f4 v[146:149], v[10:17], v[184:191], v[146:149]
	v_mfma_f32_16x16x128_f8f6f4 v[134:137], v[2:9], v[198:205], v[134:137]
	v_mfma_f32_16x16x128_f8f6f4 v[130:133], v[10:17], v[198:205], v[130:133]
	v_mfma_f32_16x16x128_f8f6f4 v[118:121], v[2:9], v[206:213], v[118:121]
	v_mfma_f32_16x16x128_f8f6f4 v[114:117], v[10:17], v[206:213], v[114:117]
	v_mfma_f32_16x16x128_f8f6f4 v[102:105], v[2:9], v[214:221], v[102:105]
	v_mfma_f32_16x16x128_f8f6f4 v[98:101], v[10:17], v[214:221], v[98:101]
	s_setprio 0
	s_barrier
	s_add_i32 s71, s61, s53
	v_lshl_add_u64 v[184:185], s[44:45], 0, v[162:163]
	s_mov_b32 m0, s71
	ds_read_b128 v[198:201], v196 offset:16384
	ds_read_b128 v[202:205], v196 offset:17408
	ds_read_b128 v[206:209], v196 offset:18432
	ds_read_b128 v[210:213], v196 offset:19456
	ds_read_b128 v[214:217], v196 offset:20480
	ds_read_b128 v[218:221], v196 offset:21504
	ds_read_b128 v[230:233], v196 offset:22528
	ds_read_b128 v[234:237], v196 offset:23552
	global_load_lds_dwordx4 v[184:185], off
	s_add_i32 m0, s71, 0x2000
	s_add_u32 s72, s44, 0x40000
	v_lshl_add_u64 v[186:187], s[44:45], 0, v[164:165]
	s_addc_u32 s73, s45, 0
	s_add_i32 s71, s62, s53
	global_load_lds_dwordx4 v[186:187], off
	v_lshl_add_u64 v[188:189], s[72:73], 0, v[162:163]
	s_mov_b32 m0, s71
	v_lshl_add_u64 v[190:191], s[46:47], 0, v[168:169]
	global_load_lds_dwordx4 v[188:189], off
	v_lshl_add_u64 v[188:189], s[72:73], 0, v[164:165]
	s_add_i32 m0, s71, 0x2000
	s_nop 0
	global_load_lds_dwordx4 v[188:189], off
	v_lshl_add_u64 v[188:189], s[46:47], 0, v[166:167]
	s_mov_b32 m0, s41
	s_nop 0
	global_load_lds_dwordx4 v[188:189], off
	s_mov_b32 m0, s54
	s_nop 0
	global_load_lds_dwordx4 v[190:191], off
	s_waitcnt vmcnt(8)
	s_waitcnt lgkmcnt(0)
	s_setprio 1
	s_barrier
	s_nop 1
	v_mfma_f32_16x16x128_f8f6f4 v[90:93], v[18:25], v[198:205], v[90:93]
	v_mfma_f32_16x16x128_f8f6f4 v[82:85], v[26:33], v[198:205], v[82:85]
	v_mfma_f32_16x16x128_f8f6f4 v[70:73], v[18:25], v[206:213], v[70:73]
	v_mfma_f32_16x16x128_f8f6f4 v[66:69], v[26:33], v[206:213], v[66:69]
	v_mfma_f32_16x16x128_f8f6f4 v[54:57], v[18:25], v[214:221], v[54:57]
	v_mfma_f32_16x16x128_f8f6f4 v[50:53], v[26:33], v[214:221], v[50:53]
	v_mfma_f32_16x16x128_f8f6f4 v[38:41], v[18:25], v[230:237], v[38:41]
	v_mfma_f32_16x16x128_f8f6f4 v[34:37], v[26:33], v[230:237], v[34:37]
	s_setprio 0
	s_setprio 1
	s_nop 1
	v_mfma_f32_16x16x128_f8f6f4 v[94:97], v[2:9], v[198:205], v[94:97]
	v_mfma_f32_16x16x128_f8f6f4 v[86:89], v[10:17], v[198:205], v[86:89]
	v_mfma_f32_16x16x128_f8f6f4 v[78:81], v[2:9], v[206:213], v[78:81]
	v_mfma_f32_16x16x128_f8f6f4 v[74:77], v[10:17], v[206:213], v[74:77]
	v_mfma_f32_16x16x128_f8f6f4 v[62:65], v[2:9], v[214:221], v[62:65]
	v_mfma_f32_16x16x128_f8f6f4 v[58:61], v[10:17], v[214:221], v[58:61]
	v_mfma_f32_16x16x128_f8f6f4 v[46:49], v[2:9], v[230:237], v[46:49]
	v_mfma_f32_16x16x128_f8f6f4 v[42:45], v[10:17], v[230:237], v[42:45]
	s_setprio 0
	s_barrier
	s_add_i32 s71, 0, 0x18000
	s_add_i32 s72, 0, 0x1c000
	v_add_u32_e32 v14, s71, v192
	v_add_u32_e32 v30, s72, v192
	ds_read_b128 v[2:5], v14
	ds_read_b128 v[6:9], v14 offset:1024
	ds_read_b128 v[10:13], v14 offset:2048
	ds_read_b128 v[14:17], v14 offset:3072
	ds_read_b128 v[18:21], v30
	ds_read_b128 v[22:25], v30 offset:1024
	ds_read_b128 v[26:29], v30 offset:2048
	ds_read_b128 v[30:33], v30 offset:3072
	s_mov_b32 m0, s55
	v_lshl_add_u64 v[222:223], s[46:47], 0, v[170:171]
	ds_read_b128 v[198:201], v196 offset:32768
	ds_read_b128 v[202:205], v196 offset:33792
	ds_read_b128 v[206:209], v196 offset:34816
	ds_read_b128 v[210:213], v196 offset:35840
	ds_read_b128 v[214:217], v196 offset:36864
	ds_read_b128 v[218:221], v196 offset:37888
	ds_read_b128 v[230:233], v196 offset:38912
	ds_read_b128 v[234:237], v196 offset:39936
	global_load_lds_dwordx4 v[222:223], off
	v_lshl_add_u64 v[222:223], s[46:47], 0, v[172:173]
	s_mov_b32 m0, s58
	s_nop 0
	global_load_lds_dwordx4 v[222:223], off
	s_waitcnt vmcnt(8)
	s_waitcnt lgkmcnt(0)
	s_setprio 1
	s_barrier
	s_nop 1
	v_mfma_f32_16x16x128_f8f6f4 v[158:161], v[2:9], v[198:205], v[158:161]
	v_mfma_f32_16x16x128_f8f6f4 v[154:157], v[10:17], v[198:205], v[154:157]
	v_mfma_f32_16x16x128_f8f6f4 v[142:145], v[2:9], v[206:213], v[142:145]
	v_mfma_f32_16x16x128_f8f6f4 v[138:141], v[10:17], v[206:213], v[138:141]
	v_mfma_f32_16x16x128_f8f6f4 v[126:129], v[2:9], v[214:221], v[126:129]
	v_mfma_f32_16x16x128_f8f6f4 v[122:125], v[10:17], v[214:221], v[122:125]
	v_mfma_f32_16x16x128_f8f6f4 v[110:113], v[2:9], v[230:237], v[110:113]
	v_mfma_f32_16x16x128_f8f6f4 v[106:109], v[10:17], v[230:237], v[106:109]
	s_setprio 0
	s_setprio 1
	s_nop 1
	v_mfma_f32_16x16x128_f8f6f4 v[150:153], v[18:25], v[198:205], v[150:153]
	v_mfma_f32_16x16x128_f8f6f4 v[146:149], v[26:33], v[198:205], v[146:149]
	v_mfma_f32_16x16x128_f8f6f4 v[134:137], v[18:25], v[206:213], v[134:137]
	v_mfma_f32_16x16x128_f8f6f4 v[130:133], v[26:33], v[206:213], v[130:133]
	v_mfma_f32_16x16x128_f8f6f4 v[118:121], v[18:25], v[214:221], v[118:121]
	v_mfma_f32_16x16x128_f8f6f4 v[114:117], v[26:33], v[214:221], v[114:117]
	v_mfma_f32_16x16x128_f8f6f4 v[102:105], v[18:25], v[230:237], v[102:105]
	v_mfma_f32_16x16x128_f8f6f4 v[98:101], v[26:33], v[230:237], v[98:101]
	s_setprio 0
	s_barrier
	s_add_i32 s46, s71, s53
	v_lshl_add_u64 v[184:185], v[184:185], 0, s[12:13]
	s_mov_b32 m0, s46
	ds_read_b128 v[198:201], v196 offset:49152
	ds_read_b128 v[202:205], v196 offset:50176
	ds_read_b128 v[206:209], v196 offset:51200
	ds_read_b128 v[210:213], v196 offset:52224
	ds_read_b128 v[214:217], v196 offset:53248
	ds_read_b128 v[218:221], v196 offset:54272
	ds_read_b128 v[230:233], v196 offset:55296
	ds_read_b128 v[234:237], v196 offset:56320
	global_load_lds_dwordx4 v[184:185], off
	s_add_i32 m0, s46, 0x2000
	s_add_u32 s44, s44, 0x40080
	v_lshl_add_u64 v[184:185], v[186:187], 0, s[12:13]
	s_addc_u32 s45, s45, 0
	s_add_i32 s46, s72, s53
	global_load_lds_dwordx4 v[184:185], off
	v_lshl_add_u64 v[184:185], s[44:45], 0, v[162:163]
	s_mov_b32 m0, s46
	s_nop 0
	global_load_lds_dwordx4 v[184:185], off
	v_lshl_add_u64 v[184:185], s[44:45], 0, v[164:165]
	s_add_i32 m0, s46, 0x2000
	s_nop 0
	global_load_lds_dwordx4 v[184:185], off
	v_lshl_add_u64 v[184:185], v[188:189], 0, s[12:13]
	s_mov_b32 m0, s59
	s_nop 0
	global_load_lds_dwordx4 v[184:185], off
	v_lshl_add_u64 v[184:185], v[190:191], 0, s[12:13]
	s_mov_b32 m0, s60
	s_nop 0
	global_load_lds_dwordx4 v[184:185], off
	s_waitcnt vmcnt(8)
	s_waitcnt lgkmcnt(0)
	s_setprio 1
	s_barrier
	s_nop 1
	v_mfma_f32_16x16x128_f8f6f4 v[90:93], v[2:9], v[198:205], v[90:93]
	v_mfma_f32_16x16x128_f8f6f4 v[82:85], v[10:17], v[198:205], v[82:85]
	v_mfma_f32_16x16x128_f8f6f4 v[70:73], v[2:9], v[206:213], v[70:73]
	v_mfma_f32_16x16x128_f8f6f4 v[66:69], v[10:17], v[206:213], v[66:69]
	v_mfma_f32_16x16x128_f8f6f4 v[54:57], v[2:9], v[214:221], v[54:57]
	v_mfma_f32_16x16x128_f8f6f4 v[50:53], v[10:17], v[214:221], v[50:53]
	v_mfma_f32_16x16x128_f8f6f4 v[38:41], v[2:9], v[230:237], v[38:41]
	v_mfma_f32_16x16x128_f8f6f4 v[34:37], v[10:17], v[230:237], v[34:37]
	s_setprio 0
	s_setprio 1
	s_nop 1
	v_mfma_f32_16x16x128_f8f6f4 v[94:97], v[18:25], v[198:205], v[94:97]
	v_mfma_f32_16x16x128_f8f6f4 v[86:89], v[26:33], v[198:205], v[86:89]
	v_mfma_f32_16x16x128_f8f6f4 v[78:81], v[18:25], v[206:213], v[78:81]
	v_mfma_f32_16x16x128_f8f6f4 v[74:77], v[26:33], v[206:213], v[74:77]
	v_mfma_f32_16x16x128_f8f6f4 v[62:65], v[18:25], v[214:221], v[62:65]
	v_mfma_f32_16x16x128_f8f6f4 v[58:61], v[26:33], v[214:221], v[58:61]
	v_mfma_f32_16x16x128_f8f6f4 v[46:49], v[18:25], v[230:237], v[46:49]
	v_mfma_f32_16x16x128_f8f6f4 v[42:45], v[26:33], v[230:237], v[42:45]
	s_setprio 0
	s_barrier
	s_add_i32 s70, s70, 2
	s_add_u32 s42, s42, 0x100
	s_addc_u32 s43, s43, 0
	s_add_u32 s68, s68, 0x100
	s_addc_u32 s69, s69, 0
	s_cmp_gt_u32 s70, 13
	s_cbranch_scc0 .LBB0_460

.LBB0_746:
	v_lshrrev_b32_e32 v7, 1, v6
	v_and_b32_e32 v133, 24, v7
	v_and_b32_e32 v132, 15, v6
	v_lshlrev_b32_e32 v7, 1, v133
	v_lshlrev_b32_e32 v6, 2, v6
	v_lshl_or_b32 v7, v132, 6, v7
	s_lshl_b32 s22, s33, 13
	v_and_b32_e32 v6, 32, v6
	v_bitop3_b32 v32, v7, s22, v6 bitop3:0xde
	s_lshl_b32 s22, s35, 5
	s_add_i32 s39, s86, s48
	s_and_b32 s35, s22, 0x60
	v_lshl_add_u64 v[8:9], v[28:29], 0, s[0:1]
	s_mov_b32 m0, s39
	s_add_i32 s41, s39, 0x2000
	s_lshl_b32 s22, s35, 7
	s_waitcnt vmcnt(2)
	s_barrier
	global_load_lds_dwordx4 v[8:9], off
	v_lshl_add_u64 v[10:11], v[30:31], 0, s[0:1]
	s_mov_b32 m0, s41
	s_add_i32 s40, s38, 0x8000
	s_add_i32 s42, s38, 0xa000
	v_bitop3_b32 v33, v7, s22, v6 bitop3:0xde
	global_load_lds_dwordx4 v[10:11], off
	v_lshl_add_u64 v[6:7], v[22:23], 0, s[0:1]
	s_mov_b32 m0, s40
	s_add_u32 s22, s20, 0x100080
	global_load_lds_dwordx4 v[6:7], off
	v_lshl_add_u64 v[12:13], v[24:25], 0, s[0:1]
	s_mov_b32 m0, s42
	s_addc_u32 s23, s21, 0
	s_add_i32 s43, s87, s48
	global_load_lds_dwordx4 v[12:13], off
	v_lshl_add_u64 v[14:15], s[22:23], 0, v[130:131]
	s_mov_b32 m0, s43
	s_add_i32 s44, s43, 0x2000
	global_load_lds_dwordx4 v[14:15], off
	v_lshl_add_u64 v[16:17], s[22:23], 0, v[18:19]
	s_mov_b32 m0, s44
	v_add_u32_e32 v235, s3, v33
	global_load_lds_dwordx4 v[16:17], off
	s_waitcnt vmcnt(6)
	s_barrier
	v_add_u32_e32 v226, 0, v32
	v_add_u32_e32 v227, s87, v33
	v_add_u32_e32 v229, s86, v33
	v_add_u32_e32 v234, s2, v33
	ds_read_b128 v[32:35], v235
	ds_read_b128 v[36:39], v235 offset:1024
	ds_read_b128 v[40:43], v235 offset:2048
	ds_read_b128 v[44:47], v235 offset:3072
	ds_read_b128 v[48:51], v234
	ds_read_b128 v[52:55], v234 offset:1024
	ds_read_b128 v[56:59], v234 offset:2048
	ds_read_b128 v[60:63], v234 offset:3072
	s_add_i32 s47, s3, s48
	s_add_i32 s52, s38, 0xc000
	s_add_i32 s50, s38, 0xe000
	s_add_i32 s46, s47, 0x2000
	s_add_u32 s22, s20, 0x100100
	s_addc_u32 s23, s21, 0
	s_add_i32 s49, s2, s48
	s_add_i32 s48, s49, 0x2000
	s_add_u32 s20, s20, 0x100180
	s_addc_u32 s21, s21, 0
	s_cmpk_gt_u32 s51, 0xff
	s_mov_b32 m0, s52
	v_lshl_add_u64 v[96:97], v[2:3], 0, s[0:1]
	ds_read_b128 v[64:67], v226
	ds_read_b128 v[68:71], v226 offset:1024
	ds_read_b128 v[72:75], v226 offset:2048
	ds_read_b128 v[76:79], v226 offset:3072
	ds_read_b128 v[80:83], v226 offset:4096
	ds_read_b128 v[84:87], v226 offset:5120
	ds_read_b128 v[88:91], v226 offset:6144
	ds_read_b128 v[92:95], v226 offset:7168
	global_load_lds_dwordx4 v[96:97], off
	v_lshl_add_u64 v[96:97], v[4:5], 0, s[0:1]
	s_mov_b32 m0, s50
	s_nop 0
	global_load_lds_dwordx4 v[96:97], off
	s_waitcnt vmcnt(8)
	s_waitcnt lgkmcnt(0)
	s_setprio 1
	s_barrier
	v_mfma_f32_16x16x32_bf16 v[96:99], v[32:35], v[64:67], 0
	v_mfma_f32_16x16x32_bf16 v[100:103], v[40:43], v[64:67], 0
	v_mfma_f32_16x16x32_bf16 v[104:107], v[32:35], v[72:75], 0
	v_mfma_f32_16x16x32_bf16 v[108:111], v[40:43], v[72:75], 0
	v_mfma_f32_16x16x32_bf16 v[112:115], v[32:35], v[80:83], 0
	v_mfma_f32_16x16x32_bf16 v[116:119], v[40:43], v[80:83], 0
	v_mfma_f32_16x16x32_bf16 v[120:123], v[32:35], v[88:91], 0
	v_mfma_f32_16x16x32_bf16 v[124:127], v[40:43], v[88:91], 0
	v_mfma_f32_16x16x32_bf16 v[96:99], v[36:39], v[68:71], v[96:99]
	v_mfma_f32_16x16x32_bf16 v[100:103], v[44:47], v[68:71], v[100:103]
	v_mfma_f32_16x16x32_bf16 v[104:107], v[36:39], v[76:79], v[104:107]
	v_mfma_f32_16x16x32_bf16 v[108:111], v[44:47], v[76:79], v[108:111]
	v_mfma_f32_16x16x32_bf16 v[112:115], v[36:39], v[84:87], v[112:115]
	v_mfma_f32_16x16x32_bf16 v[116:119], v[44:47], v[84:87], v[116:119]
	v_mfma_f32_16x16x32_bf16 v[120:123], v[36:39], v[92:95], v[120:123]
	v_mfma_f32_16x16x32_bf16 v[124:127], v[44:47], v[92:95], v[124:127]
	s_setprio 0
	s_setprio 1
	v_mfma_f32_16x16x32_bf16 v[134:137], v[48:51], v[64:67], 0
	v_mfma_f32_16x16x32_bf16 v[64:67], v[56:59], v[64:67], 0
	v_mfma_f32_16x16x32_bf16 v[134:137], v[52:55], v[68:71], v[134:137]
	v_mfma_f32_16x16x32_bf16 v[64:67], v[60:63], v[68:71], v[64:67]
	v_mfma_f32_16x16x32_bf16 v[68:71], v[48:51], v[72:75], 0
	v_mfma_f32_16x16x32_bf16 v[72:75], v[56:59], v[72:75], 0
	v_mfma_f32_16x16x32_bf16 v[68:71], v[52:55], v[76:79], v[68:71]
	v_mfma_f32_16x16x32_bf16 v[72:75], v[60:63], v[76:79], v[72:75]
	v_mfma_f32_16x16x32_bf16 v[76:79], v[48:51], v[80:83], 0
	v_mfma_f32_16x16x32_bf16 v[80:83], v[56:59], v[80:83], 0
	v_mfma_f32_16x16x32_bf16 v[76:79], v[52:55], v[84:87], v[76:79]
	v_mfma_f32_16x16x32_bf16 v[80:83], v[60:63], v[84:87], v[80:83]
	v_mfma_f32_16x16x32_bf16 v[84:87], v[48:51], v[88:91], 0
	v_mfma_f32_16x16x32_bf16 v[88:91], v[56:59], v[88:91], 0
	v_mfma_f32_16x16x32_bf16 v[84:87], v[52:55], v[92:95], v[84:87]
	v_mfma_f32_16x16x32_bf16 v[88:91], v[60:63], v[92:95], v[88:91]
	s_setprio 0
	s_barrier
	s_mov_b32 m0, s47
	v_lshl_add_u64 v[128:129], v[28:29], 0, s[6:7]
	ds_read_b128 v[92:95], v226 offset:16384
	ds_read_b128 v[138:141], v226 offset:17408
	ds_read_b128 v[142:145], v226 offset:18432
	ds_read_b128 v[146:149], v226 offset:19456
	ds_read_b128 v[150:153], v226 offset:20480
	ds_read_b128 v[154:157], v226 offset:21504
	ds_read_b128 v[158:161], v226 offset:22528
	ds_read_b128 v[162:165], v226 offset:23552
	global_load_lds_dwordx4 v[128:129], off
	v_lshl_add_u64 v[128:129], v[30:31], 0, s[6:7]
	s_mov_b32 m0, s46
	s_nop 0
	global_load_lds_dwordx4 v[128:129], off
	v_lshl_add_u64 v[128:129], s[22:23], 0, v[130:131]
	s_mov_b32 m0, s49
	s_nop 0
	global_load_lds_dwordx4 v[128:129], off
	v_lshl_add_u64 v[128:129], s[22:23], 0, v[18:19]
	s_mov_b32 m0, s48
	s_nop 0
	global_load_lds_dwordx4 v[128:129], off
	v_lshl_add_u64 v[128:129], v[22:23], 0, s[6:7]
	s_mov_b32 m0, s38
	s_nop 0
	global_load_lds_dwordx4 v[128:129], off
	v_lshl_add_u64 v[128:129], v[24:25], 0, s[6:7]
	s_mov_b32 m0, s45
	s_nop 0
	global_load_lds_dwordx4 v[128:129], off
	s_waitcnt vmcnt(8)
	s_waitcnt lgkmcnt(0)
	s_setprio 1
	s_barrier
	v_mfma_f32_16x16x32_bf16 v[166:169], v[32:35], v[92:95], 0
	v_mfma_f32_16x16x32_bf16 v[174:177], v[32:35], v[142:145], 0
	v_mfma_f32_16x16x32_bf16 v[182:185], v[32:35], v[150:153], 0
	v_mfma_f32_16x16x32_bf16 v[32:35], v[32:35], v[158:161], 0
	v_mfma_f32_16x16x32_bf16 v[166:169], v[36:39], v[138:141], v[166:169]
	v_mfma_f32_16x16x32_bf16 v[174:177], v[36:39], v[146:149], v[174:177]
	v_mfma_f32_16x16x32_bf16 v[182:185], v[36:39], v[154:157], v[182:185]
	v_mfma_f32_16x16x32_bf16 v[32:35], v[36:39], v[162:165], v[32:35]
	v_mfma_f32_16x16x32_bf16 v[36:39], v[40:43], v[158:161], 0
	v_mfma_f32_16x16x32_bf16 v[170:173], v[40:43], v[92:95], 0
	v_mfma_f32_16x16x32_bf16 v[178:181], v[40:43], v[142:145], 0
	v_mfma_f32_16x16x32_bf16 v[186:189], v[40:43], v[150:153], 0
	v_mfma_f32_16x16x32_bf16 v[36:39], v[44:47], v[162:165], v[36:39]
	v_mfma_f32_16x16x32_bf16 v[170:173], v[44:47], v[138:141], v[170:173]
	v_mfma_f32_16x16x32_bf16 v[178:181], v[44:47], v[146:149], v[178:181]
	v_mfma_f32_16x16x32_bf16 v[186:189], v[44:47], v[154:157], v[186:189]
	s_setprio 0
	s_setprio 1
	v_mfma_f32_16x16x32_bf16 v[40:43], v[48:51], v[92:95], 0
	v_mfma_f32_16x16x32_bf16 v[44:47], v[56:59], v[92:95], 0
	v_mfma_f32_16x16x32_bf16 v[40:43], v[52:55], v[138:141], v[40:43]
	v_mfma_f32_16x16x32_bf16 v[44:47], v[60:63], v[138:141], v[44:47]
	v_mfma_f32_16x16x32_bf16 v[92:95], v[48:51], v[142:145], 0
	v_mfma_f32_16x16x32_bf16 v[138:141], v[56:59], v[142:145], 0
	v_mfma_f32_16x16x32_bf16 v[142:145], v[48:51], v[150:153], 0
	v_mfma_f32_16x16x32_bf16 v[48:51], v[48:51], v[158:161], 0
	v_mfma_f32_16x16x32_bf16 v[92:95], v[52:55], v[146:149], v[92:95]
	v_mfma_f32_16x16x32_bf16 v[142:145], v[52:55], v[154:157], v[142:145]
	v_mfma_f32_16x16x32_bf16 v[48:51], v[52:55], v[162:165], v[48:51]
	v_mfma_f32_16x16x32_bf16 v[52:55], v[56:59], v[158:161], 0
	v_mfma_f32_16x16x32_bf16 v[138:141], v[60:63], v[146:149], v[138:141]
	v_mfma_f32_16x16x32_bf16 v[146:149], v[56:59], v[150:153], 0
	v_mfma_f32_16x16x32_bf16 v[52:55], v[60:63], v[162:165], v[52:55]
	v_mfma_f32_16x16x32_bf16 v[146:149], v[60:63], v[154:157], v[146:149]
	s_setprio 0
	s_barrier
	ds_read_b128 v[56:59], v229
	ds_read_b128 v[60:63], v229 offset:1024
	ds_read_b128 v[150:153], v229 offset:2048
	ds_read_b128 v[154:157], v229 offset:3072
	ds_read_b128 v[158:161], v227
	ds_read_b128 v[162:165], v227 offset:1024
	ds_read_b128 v[190:193], v227 offset:2048
	ds_read_b128 v[194:197], v227 offset:3072
	s_mov_b32 m0, s36
	v_lshl_add_u64 v[128:129], v[2:3], 0, s[6:7]
	ds_read_b128 v[198:201], v226 offset:32768
	ds_read_b128 v[202:205], v226 offset:33792
	ds_read_b128 v[206:209], v226 offset:34816
	ds_read_b128 v[210:213], v226 offset:35840
	ds_read_b128 v[214:217], v226 offset:36864
	ds_read_b128 v[218:221], v226 offset:37888
	ds_read_b128 v[222:225], v226 offset:38912
	ds_read_b128 v[230:233], v226 offset:39936
	global_load_lds_dwordx4 v[128:129], off
	v_lshl_add_u64 v[128:129], v[4:5], 0, s[6:7]
	s_mov_b32 m0, s37
	s_nop 0
	global_load_lds_dwordx4 v[128:129], off
	s_waitcnt vmcnt(8)
	s_waitcnt lgkmcnt(0)
	s_setprio 1
	s_barrier
	v_mfma_f32_16x16x32_bf16 v[96:99], v[56:59], v[198:201], v[96:99]
	v_mfma_f32_16x16x32_bf16 v[100:103], v[150:153], v[198:201], v[100:103]
	v_mfma_f32_16x16x32_bf16 v[104:107], v[56:59], v[206:209], v[104:107]
	v_mfma_f32_16x16x32_bf16 v[108:111], v[150:153], v[206:209], v[108:111]
	v_mfma_f32_16x16x32_bf16 v[112:115], v[56:59], v[214:217], v[112:115]
	v_mfma_f32_16x16x32_bf16 v[116:119], v[150:153], v[214:217], v[116:119]
	v_mfma_f32_16x16x32_bf16 v[120:123], v[56:59], v[222:225], v[120:123]
	v_mfma_f32_16x16x32_bf16 v[124:127], v[150:153], v[222:225], v[124:127]
	v_mfma_f32_16x16x32_bf16 v[96:99], v[60:63], v[202:205], v[96:99]
	v_mfma_f32_16x16x32_bf16 v[100:103], v[154:157], v[202:205], v[100:103]
	v_mfma_f32_16x16x32_bf16 v[104:107], v[60:63], v[210:213], v[104:107]
	v_mfma_f32_16x16x32_bf16 v[108:111], v[154:157], v[210:213], v[108:111]
	v_mfma_f32_16x16x32_bf16 v[112:115], v[60:63], v[218:221], v[112:115]
	v_mfma_f32_16x16x32_bf16 v[116:119], v[154:157], v[218:221], v[116:119]
	v_mfma_f32_16x16x32_bf16 v[120:123], v[60:63], v[230:233], v[120:123]
	v_mfma_f32_16x16x32_bf16 v[124:127], v[154:157], v[230:233], v[124:127]
	s_setprio 0
	s_setprio 1
	v_mfma_f32_16x16x32_bf16 v[64:67], v[190:193], v[198:201], v[64:67]
	v_mfma_f32_16x16x32_bf16 v[68:71], v[158:161], v[206:209], v[68:71]
	v_mfma_f32_16x16x32_bf16 v[72:75], v[190:193], v[206:209], v[72:75]
	v_mfma_f32_16x16x32_bf16 v[76:79], v[158:161], v[214:217], v[76:79]
	v_mfma_f32_16x16x32_bf16 v[80:83], v[190:193], v[214:217], v[80:83]
	v_mfma_f32_16x16x32_bf16 v[84:87], v[158:161], v[222:225], v[84:87]
	v_mfma_f32_16x16x32_bf16 v[88:91], v[190:193], v[222:225], v[88:91]
	v_mfma_f32_16x16x32_bf16 v[134:137], v[158:161], v[198:201], v[134:137]
	v_mfma_f32_16x16x32_bf16 v[64:67], v[194:197], v[202:205], v[64:67]
	v_mfma_f32_16x16x32_bf16 v[68:71], v[162:165], v[210:213], v[68:71]
	v_mfma_f32_16x16x32_bf16 v[72:75], v[194:197], v[210:213], v[72:75]
	v_mfma_f32_16x16x32_bf16 v[76:79], v[162:165], v[218:221], v[76:79]
	v_mfma_f32_16x16x32_bf16 v[80:83], v[194:197], v[218:221], v[80:83]
	v_mfma_f32_16x16x32_bf16 v[84:87], v[162:165], v[230:233], v[84:87]
	v_mfma_f32_16x16x32_bf16 v[88:91], v[194:197], v[230:233], v[88:91]
	v_mfma_f32_16x16x32_bf16 v[134:137], v[162:165], v[202:205], v[134:137]
	s_setprio 0
	s_barrier
	s_mov_b32 m0, s39
	v_lshl_add_u64 v[128:129], v[28:29], 0, s[8:9]
	ds_read_b128 v[198:201], v226 offset:49152
	ds_read_b128 v[202:205], v226 offset:50176
	ds_read_b128 v[206:209], v226 offset:51200
	ds_read_b128 v[210:213], v226 offset:52224
	ds_read_b128 v[214:217], v226 offset:53248
	ds_read_b128 v[218:221], v226 offset:54272
	ds_read_b128 v[222:225], v226 offset:55296
	ds_read_b128 v[230:233], v226 offset:56320
	global_load_lds_dwordx4 v[128:129], off
	v_lshl_add_u64 v[128:129], v[30:31], 0, s[8:9]
	s_mov_b32 m0, s41
	v_lshl_add_u64 v[18:19], s[20:21], 0, v[18:19]
	global_load_lds_dwordx4 v[128:129], off
	v_lshl_add_u64 v[128:129], s[20:21], 0, v[130:131]
	s_mov_b32 m0, s43
	s_nop 0
	global_load_lds_dwordx4 v[128:129], off
	s_mov_b32 m0, s44
	s_nop 0
	global_load_lds_dwordx4 v[18:19], off
	v_lshl_add_u64 v[18:19], v[22:23], 0, s[8:9]
	s_mov_b32 m0, s40
	s_nop 0
	global_load_lds_dwordx4 v[18:19], off
	v_lshl_add_u64 v[18:19], v[24:25], 0, s[8:9]
	s_mov_b32 m0, s42
	s_nop 0
	global_load_lds_dwordx4 v[18:19], off
	s_waitcnt vmcnt(8)
	s_waitcnt lgkmcnt(0)
	s_setprio 1
	s_barrier
	v_mfma_f32_16x16x32_bf16 v[32:35], v[56:59], v[222:225], v[32:35]
	v_mfma_f32_16x16x32_bf16 v[36:39], v[150:153], v[222:225], v[36:39]
	v_mfma_f32_16x16x32_bf16 v[166:169], v[56:59], v[198:201], v[166:169]
	v_mfma_f32_16x16x32_bf16 v[170:173], v[150:153], v[198:201], v[170:173]
	v_mfma_f32_16x16x32_bf16 v[174:177], v[56:59], v[206:209], v[174:177]
	v_mfma_f32_16x16x32_bf16 v[178:181], v[150:153], v[206:209], v[178:181]
	v_mfma_f32_16x16x32_bf16 v[182:185], v[56:59], v[214:217], v[182:185]
	v_mfma_f32_16x16x32_bf16 v[186:189], v[150:153], v[214:217], v[186:189]
	v_mfma_f32_16x16x32_bf16 v[32:35], v[60:63], v[230:233], v[32:35]
	v_mfma_f32_16x16x32_bf16 v[36:39], v[154:157], v[230:233], v[36:39]
	v_mfma_f32_16x16x32_bf16 v[166:169], v[60:63], v[202:205], v[166:169]
	v_mfma_f32_16x16x32_bf16 v[170:173], v[154:157], v[202:205], v[170:173]
	v_mfma_f32_16x16x32_bf16 v[174:177], v[60:63], v[210:213], v[174:177]
	v_mfma_f32_16x16x32_bf16 v[178:181], v[154:157], v[210:213], v[178:181]
	v_mfma_f32_16x16x32_bf16 v[182:185], v[60:63], v[218:221], v[182:185]
	v_mfma_f32_16x16x32_bf16 v[186:189], v[154:157], v[218:221], v[186:189]
	s_setprio 0
	s_setprio 1
	v_mfma_f32_16x16x32_bf16 v[40:43], v[158:161], v[198:201], v[40:43]
	v_mfma_f32_16x16x32_bf16 v[44:47], v[190:193], v[198:201], v[44:47]
	v_mfma_f32_16x16x32_bf16 v[56:59], v[158:161], v[206:209], v[92:95]
	v_mfma_f32_16x16x32_bf16 v[60:63], v[190:193], v[206:209], v[138:141]
	v_mfma_f32_16x16x32_bf16 v[92:95], v[158:161], v[214:217], v[142:145]
	v_mfma_f32_16x16x32_bf16 v[48:51], v[158:161], v[222:225], v[48:51]
	v_mfma_f32_16x16x32_bf16 v[52:55], v[190:193], v[222:225], v[52:55]
	v_mfma_f32_16x16x32_bf16 v[40:43], v[162:165], v[202:205], v[40:43]
	v_mfma_f32_16x16x32_bf16 v[44:47], v[194:197], v[202:205], v[44:47]
	v_mfma_f32_16x16x32_bf16 v[56:59], v[162:165], v[210:213], v[56:59]
	v_mfma_f32_16x16x32_bf16 v[60:63], v[194:197], v[210:213], v[60:63]
	v_mfma_f32_16x16x32_bf16 v[92:95], v[162:165], v[218:221], v[92:95]
	v_mfma_f32_16x16x32_bf16 v[138:141], v[190:193], v[214:217], v[146:149]
	v_mfma_f32_16x16x32_bf16 v[48:51], v[162:165], v[230:233], v[48:51]
	v_mfma_f32_16x16x32_bf16 v[52:55], v[194:197], v[230:233], v[52:55]
	v_mfma_f32_16x16x32_bf16 v[138:141], v[194:197], v[218:221], v[138:141]
	s_setprio 0
	s_barrier
	ds_read_b128 v[142:145], v235
	ds_read_b128 v[146:149], v235 offset:1024
	ds_read_b128 v[150:153], v235 offset:2048
	ds_read_b128 v[154:157], v235 offset:3072
	ds_read_b128 v[158:161], v234
	ds_read_b128 v[162:165], v234 offset:1024
	ds_read_b128 v[190:193], v234 offset:2048
	ds_read_b128 v[194:197], v234 offset:3072
	s_mov_b32 m0, s52
	v_lshl_add_u64 v[18:19], v[2:3], 0, s[8:9]
	ds_read_b128 v[198:201], v226
	ds_read_b128 v[202:205], v226 offset:1024
	ds_read_b128 v[206:209], v226 offset:2048
	ds_read_b128 v[210:213], v226 offset:3072
	ds_read_b128 v[214:217], v226 offset:4096
	ds_read_b128 v[218:221], v226 offset:5120
	ds_read_b128 v[222:225], v226 offset:6144
	ds_read_b128 v[230:233], v226 offset:7168
	global_load_lds_dwordx4 v[18:19], off
	v_lshl_add_u64 v[18:19], v[4:5], 0, s[8:9]
	s_mov_b32 m0, s50
	s_nop 0
	global_load_lds_dwordx4 v[18:19], off
	s_waitcnt vmcnt(8)
	s_waitcnt lgkmcnt(0)
	s_setprio 1
	s_barrier
	v_mfma_f32_16x16x32_bf16 v[112:115], v[142:145], v[214:217], v[112:115]
	v_mfma_f32_16x16x32_bf16 v[234:237], v[146:149], v[218:221], v[112:115]
	v_mfma_f32_16x16x32_bf16 v[112:115], v[150:153], v[214:217], v[116:119]
	v_mfma_f32_16x16x32_bf16 v[238:241], v[154:157], v[218:221], v[112:115]
	v_mfma_f32_16x16x32_bf16 v[112:115], v[142:145], v[222:225], v[120:123]
	v_mfma_f32_16x16x32_bf16 v[96:99], v[142:145], v[198:201], v[96:99]
	v_mfma_f32_16x16x32_bf16 v[100:103], v[150:153], v[198:201], v[100:103]
	v_mfma_f32_16x16x32_bf16 v[104:107], v[142:145], v[206:209], v[104:107]
	v_mfma_f32_16x16x32_bf16 v[108:111], v[150:153], v[206:209], v[108:111]
	v_mfma_f32_16x16x32_bf16 v[242:245], v[146:149], v[230:233], v[112:115]
	v_mfma_f32_16x16x32_bf16 v[112:115], v[150:153], v[222:225], v[124:127]
	v_mfma_f32_16x16x32_bf16 v[96:99], v[146:149], v[202:205], v[96:99]
	v_mfma_f32_16x16x32_bf16 v[100:103], v[154:157], v[202:205], v[100:103]
	v_mfma_f32_16x16x32_bf16 v[104:107], v[146:149], v[210:213], v[104:107]
	v_mfma_f32_16x16x32_bf16 v[108:111], v[154:157], v[210:213], v[108:111]
	v_mfma_f32_16x16x32_bf16 v[122:125], v[154:157], v[230:233], v[112:115]
	s_setprio 0
	s_setprio 1
	v_mfma_f32_16x16x32_bf16 v[64:67], v[190:193], v[198:201], v[64:67]
	v_mfma_f32_16x16x32_bf16 v[112:115], v[158:161], v[198:201], v[134:137]
	v_mfma_f32_16x16x32_bf16 v[134:137], v[194:197], v[202:205], v[64:67]
	v_mfma_f32_16x16x32_bf16 v[64:67], v[158:161], v[206:209], v[68:71]
	v_mfma_f32_16x16x32_bf16 v[198:201], v[162:165], v[210:213], v[64:67]
	v_mfma_f32_16x16x32_bf16 v[64:67], v[190:193], v[206:209], v[72:75]
	v_mfma_f32_16x16x32_bf16 v[126:129], v[162:165], v[202:205], v[112:115]
	v_mfma_f32_16x16x32_bf16 v[202:205], v[194:197], v[210:213], v[64:67]
	v_mfma_f32_16x16x32_bf16 v[64:67], v[158:161], v[214:217], v[76:79]
	v_mfma_f32_16x16x32_bf16 v[74:77], v[162:165], v[218:221], v[64:67]
	v_mfma_f32_16x16x32_bf16 v[64:67], v[190:193], v[214:217], v[80:83]
	v_mfma_f32_16x16x32_bf16 v[78:81], v[194:197], v[218:221], v[64:67]
	v_mfma_f32_16x16x32_bf16 v[64:67], v[158:161], v[222:225], v[84:87]
	v_mfma_f32_16x16x32_bf16 v[82:85], v[162:165], v[230:233], v[64:67]
	v_mfma_f32_16x16x32_bf16 v[64:67], v[190:193], v[222:225], v[88:91]
	v_mfma_f32_16x16x32_bf16 v[86:89], v[194:197], v[230:233], v[64:67]
	s_setprio 0
	s_barrier
	s_mov_b32 m0, s47
	s_nop 3
	ds_read_b128 v[64:67], v226 offset:16384
	ds_read_b128 v[68:71], v226 offset:17408
	ds_read_b128 v[112:115], v226 offset:18432
	ds_read_b128 v[116:119], v226 offset:19456
	ds_read_b128 v[206:209], v226 offset:20480
	ds_read_b128 v[210:213], v226 offset:21504
	ds_read_b128 v[214:217], v226 offset:22528
	ds_read_b128 v[218:221], v226 offset:23552
	global_load_lds_dwordx4 v[28:29], off
	s_mov_b32 m0, s46
	s_nop 0
	global_load_lds_dwordx4 v[30:31], off
	s_mov_b32 m0, s49
	s_nop 0
	global_load_lds_dwordx4 v[26:27], off
	s_mov_b32 m0, s48
	s_nop 0
	global_load_lds_dwordx4 v[20:21], off
	s_mov_b32 m0, s38
	s_nop 0
	global_load_lds_dwordx4 v[22:23], off
	s_mov_b32 m0, s45
	s_nop 0
	global_load_lds_dwordx4 v[24:25], off
	s_waitcnt vmcnt(8)
	s_waitcnt lgkmcnt(0)
	s_setprio 1
	s_barrier
	v_mfma_f32_16x16x32_bf16 v[18:21], v[142:145], v[64:67], v[166:169]
	v_mfma_f32_16x16x32_bf16 v[22:25], v[150:153], v[64:67], v[170:173]
	v_mfma_f32_16x16x32_bf16 v[26:29], v[142:145], v[112:115], v[174:177]
	v_mfma_f32_16x16x32_bf16 v[30:33], v[142:145], v[214:217], v[32:35]
	v_mfma_f32_16x16x32_bf16 v[18:21], v[146:149], v[68:71], v[18:21]
	v_mfma_f32_16x16x32_bf16 v[22:25], v[154:157], v[68:71], v[22:25]
	v_mfma_f32_16x16x32_bf16 v[26:29], v[146:149], v[116:119], v[26:29]
	v_mfma_f32_16x16x32_bf16 v[166:169], v[150:153], v[112:115], v[178:181]
	v_mfma_f32_16x16x32_bf16 v[170:173], v[142:145], v[206:209], v[182:185]
	v_mfma_f32_16x16x32_bf16 v[174:177], v[150:153], v[206:209], v[186:189]
	v_mfma_f32_16x16x32_bf16 v[30:33], v[146:149], v[218:221], v[30:33]
	v_mfma_f32_16x16x32_bf16 v[34:37], v[150:153], v[214:217], v[36:39]
	v_mfma_f32_16x16x32_bf16 v[166:169], v[154:157], v[116:119], v[166:169]
	v_mfma_f32_16x16x32_bf16 v[170:173], v[146:149], v[210:213], v[170:173]
	v_mfma_f32_16x16x32_bf16 v[174:177], v[154:157], v[210:213], v[174:177]
	v_mfma_f32_16x16x32_bf16 v[142:145], v[154:157], v[218:221], v[34:37]
	s_setprio 0
	s_setprio 1
	v_mfma_f32_16x16x32_bf16 v[34:37], v[158:161], v[64:67], v[40:43]
	v_mfma_f32_16x16x32_bf16 v[146:149], v[162:165], v[68:71], v[34:37]
	v_mfma_f32_16x16x32_bf16 v[34:37], v[190:193], v[64:67], v[44:47]
	v_mfma_f32_16x16x32_bf16 v[150:153], v[194:197], v[68:71], v[34:37]
	v_mfma_f32_16x16x32_bf16 v[34:37], v[158:161], v[112:115], v[56:59]
	v_mfma_f32_16x16x32_bf16 v[154:157], v[162:165], v[116:119], v[34:37]
	v_mfma_f32_16x16x32_bf16 v[34:37], v[190:193], v[112:115], v[60:63]
	v_mfma_f32_16x16x32_bf16 v[62:65], v[194:197], v[116:119], v[34:37]
	v_mfma_f32_16x16x32_bf16 v[34:37], v[158:161], v[206:209], v[92:95]
	v_mfma_f32_16x16x32_bf16 v[178:181], v[162:165], v[210:213], v[34:37]
	v_mfma_f32_16x16x32_bf16 v[34:37], v[190:193], v[206:209], v[138:141]
	v_mfma_f32_16x16x32_bf16 v[138:141], v[194:197], v[210:213], v[34:37]
	v_mfma_f32_16x16x32_bf16 v[34:37], v[158:161], v[214:217], v[48:51]
	v_mfma_f32_16x16x32_bf16 v[158:161], v[162:165], v[218:221], v[34:37]
	v_mfma_f32_16x16x32_bf16 v[34:37], v[190:193], v[214:217], v[52:55]
	v_mfma_f32_16x16x32_bf16 v[162:165], v[194:197], v[218:221], v[34:37]
	s_setprio 0
	s_barrier
	ds_read_b128 v[58:61], v229
	ds_read_b128 v[90:93], v229 offset:1024
	ds_read_b128 v[182:185], v229 offset:2048
	ds_read_b128 v[186:189], v229 offset:3072
	ds_read_b128 v[190:193], v227
	ds_read_b128 v[194:197], v227 offset:1024
	ds_read_b128 v[206:209], v227 offset:2048
	ds_read_b128 v[210:213], v227 offset:3072
	s_mov_b32 m0, s36
	ds_read_b128 v[42:45], v226 offset:32768
	ds_read_b128 v[46:49], v226 offset:33792
	ds_read_b128 v[50:53], v226 offset:34816
	ds_read_b128 v[54:57], v226 offset:35840
	ds_read_b128 v[214:217], v226 offset:36864
	ds_read_b128 v[218:221], v226 offset:37888
	ds_read_b128 v[222:225], v226 offset:38912
	ds_read_b128 v[230:233], v226 offset:39936
	global_load_lds_dwordx4 v[2:3], off
	s_mov_b32 m0, s37
	s_nop 0
	global_load_lds_dwordx4 v[4:5], off
	s_waitcnt vmcnt(8)
	s_waitcnt lgkmcnt(0)
	s_setprio 1
	s_barrier
	v_mfma_f32_16x16x32_bf16 v[2:5], v[58:61], v[42:45], v[96:99]
	v_mfma_f32_16x16x32_bf16 v[114:117], v[90:93], v[46:49], v[2:5]
	v_mfma_f32_16x16x32_bf16 v[2:5], v[182:185], v[42:45], v[100:103]
	v_mfma_f32_16x16x32_bf16 v[118:121], v[186:189], v[46:49], v[2:5]
	v_mfma_f32_16x16x32_bf16 v[2:5], v[58:61], v[50:53], v[104:107]
	v_mfma_f32_16x16x32_bf16 v[98:101], v[90:93], v[54:57], v[2:5]
	v_mfma_f32_16x16x32_bf16 v[2:5], v[182:185], v[50:53], v[108:111]
	v_mfma_f32_16x16x32_bf16 v[102:105], v[186:189], v[54:57], v[2:5]
	v_mfma_f32_16x16x32_bf16 v[2:5], v[58:61], v[214:217], v[234:237]
	v_mfma_f32_16x16x32_bf16 v[66:69], v[90:93], v[218:221], v[2:5]
	v_mfma_f32_16x16x32_bf16 v[2:5], v[182:185], v[214:217], v[238:241]
	v_mfma_f32_16x16x32_bf16 v[70:73], v[186:189], v[218:221], v[2:5]
	v_mfma_f32_16x16x32_bf16 v[2:5], v[58:61], v[222:225], v[242:245]
	v_mfma_f32_16x16x32_bf16 v[34:37], v[90:93], v[230:233], v[2:5]
	v_mfma_f32_16x16x32_bf16 v[2:5], v[182:185], v[222:225], v[122:125]
	v_mfma_f32_16x16x32_bf16 v[38:41], v[186:189], v[230:233], v[2:5]
	s_setprio 0
	s_setprio 1
	v_mfma_f32_16x16x32_bf16 v[2:5], v[190:193], v[42:45], v[126:129]
	v_mfma_f32_16x16x32_bf16 v[122:125], v[194:197], v[46:49], v[2:5]
	v_mfma_f32_16x16x32_bf16 v[2:5], v[206:209], v[42:45], v[134:137]
	v_mfma_f32_16x16x32_bf16 v[126:129], v[210:213], v[46:49], v[2:5]
	v_mfma_f32_16x16x32_bf16 v[2:5], v[190:193], v[50:53], v[198:201]
	v_mfma_f32_16x16x32_bf16 v[106:109], v[194:197], v[54:57], v[2:5]
	v_mfma_f32_16x16x32_bf16 v[2:5], v[206:209], v[50:53], v[202:205]
	v_mfma_f32_16x16x32_bf16 v[110:113], v[210:213], v[54:57], v[2:5]
	v_mfma_f32_16x16x32_bf16 v[2:5], v[190:193], v[214:217], v[74:77]
	v_mfma_f32_16x16x32_bf16 v[74:77], v[194:197], v[218:221], v[2:5]
	v_mfma_f32_16x16x32_bf16 v[2:5], v[206:209], v[214:217], v[78:81]
	v_mfma_f32_16x16x32_bf16 v[78:81], v[210:213], v[218:221], v[2:5]
	v_mfma_f32_16x16x32_bf16 v[2:5], v[190:193], v[222:225], v[82:85]
	v_mfma_f32_16x16x32_bf16 v[42:45], v[194:197], v[230:233], v[2:5]
	v_mfma_f32_16x16x32_bf16 v[2:5], v[206:209], v[222:225], v[86:89]
	v_mfma_f32_16x16x32_bf16 v[46:49], v[210:213], v[230:233], v[2:5]
	s_setprio 0
	s_barrier
	s_mov_b32 m0, s39
	ds_read_b128 v[94:97], v226 offset:49152
	ds_read_b128 v[134:137], v226 offset:50176
	ds_read_b128 v[198:201], v226 offset:51200
	ds_read_b128 v[202:205], v226 offset:52224
	ds_read_b128 v[214:217], v226 offset:53248
	ds_read_b128 v[218:221], v226 offset:54272
	ds_read_b128 v[222:225], v226 offset:55296
	ds_read_b128 v[230:233], v226 offset:56320
	global_load_lds_dwordx4 v[8:9], off
	s_mov_b32 m0, s41
	s_nop 0
	global_load_lds_dwordx4 v[10:11], off
	s_mov_b32 m0, s43
	s_nop 0
	global_load_lds_dwordx4 v[14:15], off
	s_mov_b32 m0, s44
	s_nop 0
	global_load_lds_dwordx4 v[16:17], off
	s_mov_b32 m0, s40
	s_nop 0
	global_load_lds_dwordx4 v[6:7], off
	s_mov_b32 m0, s42
	s_nop 0
	global_load_lds_dwordx4 v[12:13], off
	s_waitcnt vmcnt(8)
	s_waitcnt lgkmcnt(0)
	s_setprio 1
	s_barrier
	v_mfma_f32_16x16x32_bf16 v[2:5], v[58:61], v[94:97], v[18:21]
	v_mfma_f32_16x16x32_bf16 v[82:85], v[90:93], v[134:137], v[2:5]
	v_mfma_f32_16x16x32_bf16 v[2:5], v[182:185], v[94:97], v[22:25]
	v_mfma_f32_16x16x32_bf16 v[86:89], v[186:189], v[134:137], v[2:5]
	v_mfma_f32_16x16x32_bf16 v[2:5], v[58:61], v[198:201], v[26:29]
	v_mfma_f32_16x16x32_bf16 v[50:53], v[90:93], v[202:205], v[2:5]
	v_mfma_f32_16x16x32_bf16 v[2:5], v[182:185], v[198:201], v[166:169]
	v_mfma_f32_16x16x32_bf16 v[54:57], v[186:189], v[202:205], v[2:5]
	v_mfma_f32_16x16x32_bf16 v[2:5], v[58:61], v[214:217], v[170:173]
	v_mfma_f32_16x16x32_bf16 v[18:21], v[90:93], v[218:221], v[2:5]
	v_mfma_f32_16x16x32_bf16 v[2:5], v[182:185], v[214:217], v[174:177]
	v_mfma_f32_16x16x32_bf16 v[22:25], v[186:189], v[218:221], v[2:5]
	v_mfma_f32_16x16x32_bf16 v[2:5], v[58:61], v[222:225], v[30:33]
	v_mfma_f32_16x16x32_bf16 v[6:9], v[182:185], v[222:225], v[142:145]
	v_mfma_f32_16x16x32_bf16 v[2:5], v[90:93], v[230:233], v[2:5]
	v_mfma_f32_16x16x32_bf16 v[6:9], v[186:189], v[230:233], v[6:9]
	s_setprio 0
	s_setprio 1
	v_mfma_f32_16x16x32_bf16 v[10:13], v[190:193], v[94:97], v[146:149]
	v_mfma_f32_16x16x32_bf16 v[90:93], v[194:197], v[134:137], v[10:13]
	v_mfma_f32_16x16x32_bf16 v[10:13], v[206:209], v[94:97], v[150:153]
	v_mfma_f32_16x16x32_bf16 v[94:97], v[210:213], v[134:137], v[10:13]
	v_mfma_f32_16x16x32_bf16 v[10:13], v[190:193], v[198:201], v[154:157]
	v_mfma_f32_16x16x32_bf16 v[58:61], v[194:197], v[202:205], v[10:13]
	v_mfma_f32_16x16x32_bf16 v[10:13], v[206:209], v[198:201], v[62:65]
	v_mfma_f32_16x16x32_bf16 v[62:65], v[210:213], v[202:205], v[10:13]
	v_mfma_f32_16x16x32_bf16 v[10:13], v[190:193], v[214:217], v[178:181]
	v_mfma_f32_16x16x32_bf16 v[26:29], v[194:197], v[218:221], v[10:13]
	v_mfma_f32_16x16x32_bf16 v[10:13], v[206:209], v[214:217], v[138:141]
	v_mfma_f32_16x16x32_bf16 v[30:33], v[210:213], v[218:221], v[10:13]
	v_mfma_f32_16x16x32_bf16 v[10:13], v[190:193], v[222:225], v[158:161]
	v_mfma_f32_16x16x32_bf16 v[14:17], v[206:209], v[222:225], v[162:165]
	v_mfma_f32_16x16x32_bf16 v[10:13], v[194:197], v[230:233], v[10:13]
	v_mfma_f32_16x16x32_bf16 v[14:17], v[210:213], v[230:233], v[14:17]
	s_setprio 0
	s_barrier
	s_cbranch_scc1 .LBB0_741
	s_barrier
	s_branch .LBB0_741

.LBB0_1003:
	v_add_u32_e32 v3, s3, v174
	ds_read_b128 v[134:137], v3
	ds_read_b128 v[138:141], v3 offset:1024
	ds_read_b128 v[142:145], v3 offset:2048
	ds_read_b128 v[146:149], v3 offset:3072
	v_add_u32_e32 v3, s2, v174
	ds_read_b128 v[170:173], v3
	ds_read_b128 v[178:181], v3 offset:1024
	ds_read_b128 v[182:185], v3 offset:2048
	ds_read_b128 v[186:189], v3 offset:3072
	s_add_u32 s38, s36, 0x80
	s_addc_u32 s39, s37, 0
	s_cmp_eq_u32 s61, 12
	s_cselect_b32 s41, s29, s39
	s_cselect_b32 s40, s28, s38
	s_cselect_b32 s39, s31, s60
	s_cselect_b32 s38, s30, s27
	v_lshl_add_u64 v[4:5], s[36:37], 0, v[164:165]
	s_add_i32 m0, s46, 0xc000
	ds_read_b128 v[190:193], v177
	ds_read_b128 v[194:197], v177 offset:1024
	ds_read_b128 v[198:201], v177 offset:2048
	ds_read_b128 v[202:205], v177 offset:3072
	ds_read_b128 v[206:209], v177 offset:4096
	ds_read_b128 v[210:213], v177 offset:5120
	ds_read_b128 v[214:217], v177 offset:6144
	ds_read_b128 v[218:221], v177 offset:7168
	global_load_lds_dwordx4 v[4:5], off
	v_lshl_add_u64 v[4:5], s[36:37], 0, v[162:163]
	s_add_i32 m0, s46, 0xe000
	s_nop 0
	global_load_lds_dwordx4 v[4:5], off
	s_waitcnt vmcnt(8)
	s_waitcnt lgkmcnt(0)
	s_setprio 1
	s_barrier
	v_mfma_f32_16x16x32_bf16 v[98:101], v[134:137], v[190:193], v[98:101]
	v_mfma_f32_16x16x32_bf16 v[94:97], v[142:145], v[190:193], v[94:97]
	v_mfma_f32_16x16x32_bf16 v[90:93], v[134:137], v[198:201], v[90:93]
	v_mfma_f32_16x16x32_bf16 v[86:89], v[142:145], v[198:201], v[86:89]
	v_mfma_f32_16x16x32_bf16 v[82:85], v[134:137], v[206:209], v[82:85]
	v_mfma_f32_16x16x32_bf16 v[78:81], v[142:145], v[206:209], v[78:81]
	v_mfma_f32_16x16x32_bf16 v[74:77], v[134:137], v[214:217], v[74:77]
	v_mfma_f32_16x16x32_bf16 v[70:73], v[142:145], v[214:217], v[70:73]
	v_mfma_f32_16x16x32_bf16 v[98:101], v[138:141], v[194:197], v[98:101]
	v_mfma_f32_16x16x32_bf16 v[94:97], v[146:149], v[194:197], v[94:97]
	v_mfma_f32_16x16x32_bf16 v[90:93], v[138:141], v[202:205], v[90:93]
	v_mfma_f32_16x16x32_bf16 v[86:89], v[146:149], v[202:205], v[86:89]
	v_mfma_f32_16x16x32_bf16 v[82:85], v[138:141], v[210:213], v[82:85]
	v_mfma_f32_16x16x32_bf16 v[78:81], v[146:149], v[210:213], v[78:81]
	v_mfma_f32_16x16x32_bf16 v[74:77], v[138:141], v[218:221], v[74:77]
	v_mfma_f32_16x16x32_bf16 v[70:73], v[146:149], v[218:221], v[70:73]
	s_setprio 0
	s_setprio 1
	v_mfma_f32_16x16x32_bf16 v[66:69], v[170:173], v[190:193], v[66:69]
	v_mfma_f32_16x16x32_bf16 v[62:65], v[182:185], v[190:193], v[62:65]
	v_mfma_f32_16x16x32_bf16 v[58:61], v[170:173], v[198:201], v[58:61]
	v_mfma_f32_16x16x32_bf16 v[54:57], v[182:185], v[198:201], v[54:57]
	v_mfma_f32_16x16x32_bf16 v[50:53], v[170:173], v[206:209], v[50:53]
	v_mfma_f32_16x16x32_bf16 v[46:49], v[182:185], v[206:209], v[46:49]
	v_mfma_f32_16x16x32_bf16 v[42:45], v[170:173], v[214:217], v[42:45]
	v_mfma_f32_16x16x32_bf16 v[38:41], v[182:185], v[214:217], v[38:41]
	v_mfma_f32_16x16x32_bf16 v[66:69], v[178:181], v[194:197], v[66:69]
	v_mfma_f32_16x16x32_bf16 v[62:65], v[186:189], v[194:197], v[62:65]
	v_mfma_f32_16x16x32_bf16 v[58:61], v[178:181], v[202:205], v[58:61]
	v_mfma_f32_16x16x32_bf16 v[54:57], v[186:189], v[202:205], v[54:57]
	v_mfma_f32_16x16x32_bf16 v[50:53], v[178:181], v[210:213], v[50:53]
	v_mfma_f32_16x16x32_bf16 v[46:49], v[186:189], v[210:213], v[46:49]
	v_mfma_f32_16x16x32_bf16 v[42:45], v[178:181], v[218:221], v[42:45]
	v_mfma_f32_16x16x32_bf16 v[38:41], v[186:189], v[218:221], v[38:41]
	s_setprio 0
	s_barrier
	s_add_i32 s62, s3, s45
	v_lshl_add_u64 v[222:223], s[38:39], 0, v[150:151]
	s_mov_b32 m0, s62
	ds_read_b128 v[190:193], v177 offset:16384
	ds_read_b128 v[194:197], v177 offset:17408
	ds_read_b128 v[198:201], v177 offset:18432
	ds_read_b128 v[202:205], v177 offset:19456
	ds_read_b128 v[206:209], v177 offset:20480
	ds_read_b128 v[210:213], v177 offset:21504
	ds_read_b128 v[214:217], v177 offset:22528
	ds_read_b128 v[218:221], v177 offset:23552
	global_load_lds_dwordx4 v[222:223], off
	s_add_i32 m0, s62, 0x2000
	s_add_u32 s62, s38, 0x80000
	v_lshl_add_u64 v[224:225], s[38:39], 0, v[152:153]
	s_addc_u32 s63, s39, 0
	s_add_i32 s64, s2, s45
	global_load_lds_dwordx4 v[224:225], off
	v_lshl_add_u64 v[4:5], s[62:63], 0, v[150:151]
	s_mov_b32 m0, s64
	v_lshl_add_u64 v[226:227], s[40:41], 0, v[154:155]
	global_load_lds_dwordx4 v[4:5], off
	v_lshl_add_u64 v[4:5], s[62:63], 0, v[152:153]
	s_add_i32 m0, s64, 0x2000
	v_lshl_add_u64 v[230:231], s[40:41], 0, v[156:157]
	global_load_lds_dwordx4 v[4:5], off
	s_mov_b32 m0, s46
	s_nop 0
	global_load_lds_dwordx4 v[226:227], off
	s_mov_b32 m0, s47
	s_nop 0
	global_load_lds_dwordx4 v[230:231], off
	s_waitcnt vmcnt(8)
	s_waitcnt lgkmcnt(0)
	s_setprio 1
	s_barrier
	v_mfma_f32_16x16x32_bf16 v[34:37], v[134:137], v[190:193], v[34:37]
	v_mfma_f32_16x16x32_bf16 v[30:33], v[142:145], v[190:193], v[30:33]
	v_mfma_f32_16x16x32_bf16 v[26:29], v[134:137], v[198:201], v[26:29]
	v_mfma_f32_16x16x32_bf16 v[22:25], v[142:145], v[198:201], v[22:25]
	v_mfma_f32_16x16x32_bf16 v[18:21], v[134:137], v[206:209], v[18:21]
	v_mfma_f32_16x16x32_bf16 v[14:17], v[142:145], v[206:209], v[14:17]
	v_mfma_f32_16x16x32_bf16 v[10:13], v[134:137], v[214:217], v[10:13]
	v_mfma_f32_16x16x32_bf16 v[4:7], v[142:145], v[214:217], v[6:9]
	v_mfma_f32_16x16x32_bf16 v[34:37], v[138:141], v[194:197], v[34:37]
	v_mfma_f32_16x16x32_bf16 v[30:33], v[146:149], v[194:197], v[30:33]
	v_mfma_f32_16x16x32_bf16 v[26:29], v[138:141], v[202:205], v[26:29]
	v_mfma_f32_16x16x32_bf16 v[22:25], v[146:149], v[202:205], v[22:25]
	v_mfma_f32_16x16x32_bf16 v[18:21], v[138:141], v[210:213], v[18:21]
	v_mfma_f32_16x16x32_bf16 v[14:17], v[146:149], v[210:213], v[14:17]
	v_mfma_f32_16x16x32_bf16 v[10:13], v[138:141], v[218:221], v[10:13]
	v_mfma_f32_16x16x32_bf16 v[4:7], v[146:149], v[218:221], v[4:7]
	s_setprio 0
	s_setprio 1
	v_mfma_f32_16x16x32_bf16 v[102:105], v[170:173], v[190:193], v[102:105]
	v_mfma_f32_16x16x32_bf16 v[106:109], v[182:185], v[190:193], v[106:109]
	v_mfma_f32_16x16x32_bf16 v[110:113], v[170:173], v[198:201], v[110:113]
	v_mfma_f32_16x16x32_bf16 v[114:117], v[182:185], v[198:201], v[114:117]
	v_mfma_f32_16x16x32_bf16 v[118:121], v[170:173], v[206:209], v[118:121]
	v_mfma_f32_16x16x32_bf16 v[122:125], v[182:185], v[206:209], v[122:125]
	v_mfma_f32_16x16x32_bf16 v[126:129], v[170:173], v[214:217], v[126:129]
	v_mfma_f32_16x16x32_bf16 v[130:133], v[182:185], v[214:217], v[130:133]
	v_mfma_f32_16x16x32_bf16 v[102:105], v[178:181], v[194:197], v[102:105]
	v_mfma_f32_16x16x32_bf16 v[106:109], v[186:189], v[194:197], v[106:109]
	v_mfma_f32_16x16x32_bf16 v[110:113], v[178:181], v[202:205], v[110:113]
	v_mfma_f32_16x16x32_bf16 v[114:117], v[186:189], v[202:205], v[114:117]
	v_mfma_f32_16x16x32_bf16 v[118:121], v[178:181], v[210:213], v[118:121]
	v_mfma_f32_16x16x32_bf16 v[122:125], v[186:189], v[210:213], v[122:125]
	v_mfma_f32_16x16x32_bf16 v[126:129], v[178:181], v[218:221], v[126:129]
	v_mfma_f32_16x16x32_bf16 v[130:133], v[186:189], v[218:221], v[130:133]
	s_setprio 0
	s_barrier
	v_add_u32_e32 v3, s86, v174
	ds_read_b128 v[134:137], v3
	ds_read_b128 v[138:141], v3 offset:1024
	ds_read_b128 v[142:145], v3 offset:2048
	ds_read_b128 v[146:149], v3 offset:3072
	v_add_u32_e32 v3, s87, v174
	ds_read_b128 v[170:173], v3
	ds_read_b128 v[178:181], v3 offset:1024
	ds_read_b128 v[182:185], v3 offset:2048
	ds_read_b128 v[186:189], v3 offset:3072
	s_mov_b32 m0, s48
	v_lshl_add_u64 v[8:9], s[40:41], 0, v[158:159]
	ds_read_b128 v[190:193], v177 offset:32768
	ds_read_b128 v[194:197], v177 offset:33792
	ds_read_b128 v[198:201], v177 offset:34816
	ds_read_b128 v[202:205], v177 offset:35840
	ds_read_b128 v[206:209], v177 offset:36864
	ds_read_b128 v[210:213], v177 offset:37888
	ds_read_b128 v[214:217], v177 offset:38912
	ds_read_b128 v[218:221], v177 offset:39936
	global_load_lds_dwordx4 v[8:9], off
	v_lshl_add_u64 v[8:9], s[40:41], 0, v[160:161]
	s_mov_b32 m0, s49
	s_nop 0
	global_load_lds_dwordx4 v[8:9], off
	s_waitcnt vmcnt(8)
	s_waitcnt lgkmcnt(0)
	s_setprio 1
	s_barrier
	v_mfma_f32_16x16x32_bf16 v[98:101], v[134:137], v[190:193], v[98:101]
	v_mfma_f32_16x16x32_bf16 v[94:97], v[142:145], v[190:193], v[94:97]
	v_mfma_f32_16x16x32_bf16 v[90:93], v[134:137], v[198:201], v[90:93]
	v_mfma_f32_16x16x32_bf16 v[86:89], v[142:145], v[198:201], v[86:89]
	v_mfma_f32_16x16x32_bf16 v[82:85], v[134:137], v[206:209], v[82:85]
	v_mfma_f32_16x16x32_bf16 v[78:81], v[142:145], v[206:209], v[78:81]
	v_mfma_f32_16x16x32_bf16 v[74:77], v[134:137], v[214:217], v[74:77]
	v_mfma_f32_16x16x32_bf16 v[70:73], v[142:145], v[214:217], v[70:73]
	v_mfma_f32_16x16x32_bf16 v[98:101], v[138:141], v[194:197], v[98:101]
	v_mfma_f32_16x16x32_bf16 v[94:97], v[146:149], v[194:197], v[94:97]
	v_mfma_f32_16x16x32_bf16 v[90:93], v[138:141], v[202:205], v[90:93]
	v_mfma_f32_16x16x32_bf16 v[86:89], v[146:149], v[202:205], v[86:89]
	v_mfma_f32_16x16x32_bf16 v[82:85], v[138:141], v[210:213], v[82:85]
	v_mfma_f32_16x16x32_bf16 v[78:81], v[146:149], v[210:213], v[78:81]
	v_mfma_f32_16x16x32_bf16 v[74:77], v[138:141], v[218:221], v[74:77]
	v_mfma_f32_16x16x32_bf16 v[70:73], v[146:149], v[218:221], v[70:73]
	s_setprio 0
	s_setprio 1
	v_mfma_f32_16x16x32_bf16 v[66:69], v[170:173], v[190:193], v[66:69]
	v_mfma_f32_16x16x32_bf16 v[62:65], v[182:185], v[190:193], v[62:65]
	v_mfma_f32_16x16x32_bf16 v[58:61], v[170:173], v[198:201], v[58:61]
	v_mfma_f32_16x16x32_bf16 v[54:57], v[182:185], v[198:201], v[54:57]
	v_mfma_f32_16x16x32_bf16 v[50:53], v[170:173], v[206:209], v[50:53]
	v_mfma_f32_16x16x32_bf16 v[46:49], v[182:185], v[206:209], v[46:49]
	v_mfma_f32_16x16x32_bf16 v[42:45], v[170:173], v[214:217], v[42:45]
	v_mfma_f32_16x16x32_bf16 v[38:41], v[182:185], v[214:217], v[38:41]
	v_mfma_f32_16x16x32_bf16 v[66:69], v[178:181], v[194:197], v[66:69]
	v_mfma_f32_16x16x32_bf16 v[62:65], v[186:189], v[194:197], v[62:65]
	v_mfma_f32_16x16x32_bf16 v[58:61], v[178:181], v[202:205], v[58:61]
	v_mfma_f32_16x16x32_bf16 v[54:57], v[186:189], v[202:205], v[54:57]
	v_mfma_f32_16x16x32_bf16 v[50:53], v[178:181], v[210:213], v[50:53]
	v_mfma_f32_16x16x32_bf16 v[46:49], v[186:189], v[210:213], v[46:49]
	v_mfma_f32_16x16x32_bf16 v[42:45], v[178:181], v[218:221], v[42:45]
	v_mfma_f32_16x16x32_bf16 v[38:41], v[186:189], v[218:221], v[38:41]
	s_setprio 0
	s_barrier
	s_add_i32 s40, s86, s45
	v_lshl_add_u64 v[8:9], v[222:223], 0, s[6:7]
	s_mov_b32 m0, s40
	ds_read_b128 v[190:193], v177 offset:49152
	ds_read_b128 v[194:197], v177 offset:50176
	ds_read_b128 v[198:201], v177 offset:51200
	ds_read_b128 v[202:205], v177 offset:52224
	ds_read_b128 v[206:209], v177 offset:53248
	ds_read_b128 v[210:213], v177 offset:54272
	ds_read_b128 v[214:217], v177 offset:55296
	ds_read_b128 v[218:221], v177 offset:56320
	global_load_lds_dwordx4 v[8:9], off
	s_add_i32 m0, s40, 0x2000
	s_add_u32 s38, s38, 0x80080
	v_lshl_add_u64 v[8:9], v[224:225], 0, s[6:7]
	s_addc_u32 s39, s39, 0
	s_add_i32 s40, s87, s45
	global_load_lds_dwordx4 v[8:9], off
	v_lshl_add_u64 v[8:9], s[38:39], 0, v[150:151]
	s_mov_b32 m0, s40
	s_nop 0
	global_load_lds_dwordx4 v[8:9], off
	v_lshl_add_u64 v[8:9], s[38:39], 0, v[152:153]
	s_add_i32 m0, s40, 0x2000
	s_nop 0
	global_load_lds_dwordx4 v[8:9], off
	v_lshl_add_u64 v[8:9], v[226:227], 0, s[6:7]
	s_mov_b32 m0, s51
	s_nop 0
	global_load_lds_dwordx4 v[8:9], off
	v_lshl_add_u64 v[8:9], v[230:231], 0, s[6:7]
	s_mov_b32 m0, s52
	s_nop 0
	global_load_lds_dwordx4 v[8:9], off
	s_waitcnt vmcnt(8)
	s_waitcnt lgkmcnt(0)
	s_setprio 1
	s_barrier
	v_mfma_f32_16x16x32_bf16 v[34:37], v[134:137], v[190:193], v[34:37]
	v_mfma_f32_16x16x32_bf16 v[30:33], v[142:145], v[190:193], v[30:33]
	v_mfma_f32_16x16x32_bf16 v[26:29], v[134:137], v[198:201], v[26:29]
	v_mfma_f32_16x16x32_bf16 v[22:25], v[142:145], v[198:201], v[22:25]
	v_mfma_f32_16x16x32_bf16 v[18:21], v[134:137], v[206:209], v[18:21]
	v_mfma_f32_16x16x32_bf16 v[14:17], v[142:145], v[206:209], v[14:17]
	v_mfma_f32_16x16x32_bf16 v[8:11], v[134:137], v[214:217], v[10:13]
	v_mfma_f32_16x16x32_bf16 v[4:7], v[142:145], v[214:217], v[4:7]
	v_mfma_f32_16x16x32_bf16 v[34:37], v[138:141], v[194:197], v[34:37]
	v_mfma_f32_16x16x32_bf16 v[30:33], v[146:149], v[194:197], v[30:33]
	v_mfma_f32_16x16x32_bf16 v[26:29], v[138:141], v[202:205], v[26:29]
	v_mfma_f32_16x16x32_bf16 v[22:25], v[146:149], v[202:205], v[22:25]
	v_mfma_f32_16x16x32_bf16 v[18:21], v[138:141], v[210:213], v[18:21]
	v_mfma_f32_16x16x32_bf16 v[14:17], v[146:149], v[210:213], v[14:17]
	v_mfma_f32_16x16x32_bf16 v[10:13], v[138:141], v[218:221], v[8:11]
	v_mfma_f32_16x16x32_bf16 v[6:9], v[146:149], v[218:221], v[4:7]
	s_setprio 0
	s_setprio 1
	v_mfma_f32_16x16x32_bf16 v[102:105], v[170:173], v[190:193], v[102:105]
	v_mfma_f32_16x16x32_bf16 v[106:109], v[182:185], v[190:193], v[106:109]
	v_mfma_f32_16x16x32_bf16 v[110:113], v[170:173], v[198:201], v[110:113]
	v_mfma_f32_16x16x32_bf16 v[114:117], v[182:185], v[198:201], v[114:117]
	v_mfma_f32_16x16x32_bf16 v[118:121], v[170:173], v[206:209], v[118:121]
	v_mfma_f32_16x16x32_bf16 v[122:125], v[182:185], v[206:209], v[122:125]
	v_mfma_f32_16x16x32_bf16 v[126:129], v[170:173], v[214:217], v[126:129]
	v_mfma_f32_16x16x32_bf16 v[130:133], v[182:185], v[214:217], v[130:133]
	v_mfma_f32_16x16x32_bf16 v[102:105], v[178:181], v[194:197], v[102:105]
	v_mfma_f32_16x16x32_bf16 v[106:109], v[186:189], v[194:197], v[106:109]
	v_mfma_f32_16x16x32_bf16 v[110:113], v[178:181], v[202:205], v[110:113]
	v_mfma_f32_16x16x32_bf16 v[114:117], v[186:189], v[202:205], v[114:117]
	v_mfma_f32_16x16x32_bf16 v[118:121], v[178:181], v[210:213], v[118:121]
	v_mfma_f32_16x16x32_bf16 v[122:125], v[186:189], v[210:213], v[122:125]
	v_mfma_f32_16x16x32_bf16 v[126:129], v[178:181], v[218:221], v[126:129]
	v_mfma_f32_16x16x32_bf16 v[130:133], v[186:189], v[218:221], v[130:133]
	s_setprio 0
	s_barrier
	s_add_i32 s61, s61, 2
	s_add_u32 s36, s36, 0x100
	s_addc_u32 s37, s37, 0
	s_add_u32 s27, s27, 0x100
	s_addc_u32 s60, s60, 0
	s_cmp_gt_u32 s61, 13
	s_cbranch_scc0 .LBB0_1003
	s_and_b64 vcc, exec, s[10:11]
	s_cbranch_vccz .LBB0_1006
	s_barrier

.LBB0_1089:
	ds_read_b128 v[150:153], v156
	ds_read_b128 v[160:163], v156 offset:1024
	ds_read_b128 v[164:167], v156 offset:2048
	ds_read_b128 v[168:171], v156 offset:3072
	ds_read_b128 v[172:175], v157
	ds_read_b128 v[176:179], v157 offset:1024
	ds_read_b128 v[180:183], v157 offset:2048
	ds_read_b128 v[184:187], v157 offset:3072
	s_add_u32 s28, s26, 0x80
	s_addc_u32 s29, s27, 0
	s_cmp_eq_u32 s49, 28
	s_cselect_b32 s31, s23, s29
	s_cselect_b32 s30, s22, s28
	s_cselect_b32 s29, s25, s21
	s_cselect_b32 s28, s24, s19
	v_lshl_add_u64 v[220:221], s[26:27], 0, v[144:145]
	s_add_i32 m0, s38, 0xc000
	ds_read_b128 v[188:191], v158
	ds_read_b128 v[192:195], v158 offset:1024
	ds_read_b128 v[196:199], v158 offset:2048
	ds_read_b128 v[200:203], v158 offset:3072
	ds_read_b128 v[204:207], v158 offset:4096
	ds_read_b128 v[208:211], v158 offset:5120
	ds_read_b128 v[212:215], v158 offset:6144
	ds_read_b128 v[216:219], v158 offset:7168
	global_load_lds_dwordx4 v[220:221], off
	v_lshl_add_u64 v[220:221], s[26:27], 0, v[142:143]
	s_add_i32 m0, s38, 0xe000
	s_nop 0
	global_load_lds_dwordx4 v[220:221], off
	s_waitcnt vmcnt(8)
	s_waitcnt lgkmcnt(0)
	s_setprio 1
	s_barrier
	v_mfma_f32_16x16x32_bf16 v[126:129], v[150:153], v[188:191], v[126:129]
	v_mfma_f32_16x16x32_bf16 v[122:125], v[164:167], v[188:191], v[122:125]
	v_mfma_f32_16x16x32_bf16 v[110:113], v[150:153], v[196:199], v[110:113]
	v_mfma_f32_16x16x32_bf16 v[106:109], v[164:167], v[196:199], v[106:109]
	v_mfma_f32_16x16x32_bf16 v[94:97], v[150:153], v[204:207], v[94:97]
	v_mfma_f32_16x16x32_bf16 v[90:93], v[164:167], v[204:207], v[90:93]
	v_mfma_f32_16x16x32_bf16 v[78:81], v[150:153], v[212:215], v[78:81]
	v_mfma_f32_16x16x32_bf16 v[74:77], v[164:167], v[212:215], v[74:77]
	v_mfma_f32_16x16x32_bf16 v[126:129], v[160:163], v[192:195], v[126:129]
	v_mfma_f32_16x16x32_bf16 v[122:125], v[168:171], v[192:195], v[122:125]
	v_mfma_f32_16x16x32_bf16 v[110:113], v[160:163], v[200:203], v[110:113]
	v_mfma_f32_16x16x32_bf16 v[106:109], v[168:171], v[200:203], v[106:109]
	v_mfma_f32_16x16x32_bf16 v[94:97], v[160:163], v[208:211], v[94:97]
	v_mfma_f32_16x16x32_bf16 v[90:93], v[168:171], v[208:211], v[90:93]
	v_mfma_f32_16x16x32_bf16 v[78:81], v[160:163], v[216:219], v[78:81]
	v_mfma_f32_16x16x32_bf16 v[74:77], v[168:171], v[216:219], v[74:77]
	s_setprio 0
	s_setprio 1
	v_mfma_f32_16x16x32_bf16 v[118:121], v[172:175], v[188:191], v[118:121]
	v_mfma_f32_16x16x32_bf16 v[114:117], v[180:183], v[188:191], v[114:117]
	v_mfma_f32_16x16x32_bf16 v[102:105], v[172:175], v[196:199], v[102:105]
	v_mfma_f32_16x16x32_bf16 v[98:101], v[180:183], v[196:199], v[98:101]
	v_mfma_f32_16x16x32_bf16 v[86:89], v[172:175], v[204:207], v[86:89]
	v_mfma_f32_16x16x32_bf16 v[82:85], v[180:183], v[204:207], v[82:85]
	v_mfma_f32_16x16x32_bf16 v[70:73], v[172:175], v[212:215], v[70:73]
	v_mfma_f32_16x16x32_bf16 v[66:69], v[180:183], v[212:215], v[66:69]
	v_mfma_f32_16x16x32_bf16 v[118:121], v[176:179], v[192:195], v[118:121]
	v_mfma_f32_16x16x32_bf16 v[114:117], v[184:187], v[192:195], v[114:117]
	v_mfma_f32_16x16x32_bf16 v[102:105], v[176:179], v[200:203], v[102:105]
	v_mfma_f32_16x16x32_bf16 v[98:101], v[184:187], v[200:203], v[98:101]
	v_mfma_f32_16x16x32_bf16 v[86:89], v[176:179], v[208:211], v[86:89]
	v_mfma_f32_16x16x32_bf16 v[82:85], v[184:187], v[208:211], v[82:85]
	v_mfma_f32_16x16x32_bf16 v[70:73], v[176:179], v[216:219], v[70:73]
	v_mfma_f32_16x16x32_bf16 v[66:69], v[184:187], v[216:219], v[66:69]
	s_setprio 0
	s_barrier
	s_add_i32 s50, s3, s37
	v_lshl_add_u64 v[220:221], s[28:29], 0, v[130:131]
	s_mov_b32 m0, s50
	ds_read_b128 v[188:191], v158 offset:16384
	ds_read_b128 v[192:195], v158 offset:17408
	ds_read_b128 v[196:199], v158 offset:18432
	ds_read_b128 v[200:203], v158 offset:19456
	ds_read_b128 v[204:207], v158 offset:20480
	ds_read_b128 v[208:211], v158 offset:21504
	ds_read_b128 v[212:215], v158 offset:22528
	ds_read_b128 v[216:219], v158 offset:23552
	global_load_lds_dwordx4 v[220:221], off
	s_add_i32 m0, s50, 0x2000
	s_add_u32 s50, s28, 0x80000
	v_lshl_add_u64 v[222:223], s[28:29], 0, v[132:133]
	s_addc_u32 s51, s29, 0
	s_add_i32 s52, s2, s37
	global_load_lds_dwordx4 v[222:223], off
	v_lshl_add_u64 v[224:225], s[50:51], 0, v[130:131]
	s_mov_b32 m0, s52
	v_lshl_add_u64 v[226:227], s[30:31], 0, v[136:137]
	global_load_lds_dwordx4 v[224:225], off
	v_lshl_add_u64 v[224:225], s[50:51], 0, v[132:133]
	s_add_i32 m0, s52, 0x2000
	s_nop 0
	global_load_lds_dwordx4 v[224:225], off
	v_lshl_add_u64 v[224:225], s[30:31], 0, v[134:135]
	s_mov_b32 m0, s38
	s_nop 0
	global_load_lds_dwordx4 v[224:225], off
	s_mov_b32 m0, s39
	s_nop 0
	global_load_lds_dwordx4 v[226:227], off
	s_waitcnt vmcnt(8)
	s_waitcnt lgkmcnt(0)
	s_setprio 1
	s_barrier
	v_mfma_f32_16x16x32_bf16 v[54:57], v[150:153], v[188:191], v[54:57]
	v_mfma_f32_16x16x32_bf16 v[50:53], v[164:167], v[188:191], v[50:53]
	v_mfma_f32_16x16x32_bf16 v[38:41], v[150:153], v[196:199], v[38:41]
	v_mfma_f32_16x16x32_bf16 v[34:37], v[164:167], v[196:199], v[34:37]
	v_mfma_f32_16x16x32_bf16 v[22:25], v[150:153], v[204:207], v[22:25]
	v_mfma_f32_16x16x32_bf16 v[18:21], v[164:167], v[204:207], v[18:21]
	v_mfma_f32_16x16x32_bf16 v[6:9], v[150:153], v[212:215], v[6:9]
	v_mfma_f32_16x16x32_bf16 v[2:5], v[164:167], v[212:215], v[2:5]
	v_mfma_f32_16x16x32_bf16 v[54:57], v[160:163], v[192:195], v[54:57]
	v_mfma_f32_16x16x32_bf16 v[50:53], v[168:171], v[192:195], v[50:53]
	v_mfma_f32_16x16x32_bf16 v[38:41], v[160:163], v[200:203], v[38:41]
	v_mfma_f32_16x16x32_bf16 v[34:37], v[168:171], v[200:203], v[34:37]
	v_mfma_f32_16x16x32_bf16 v[22:25], v[160:163], v[208:211], v[22:25]
	v_mfma_f32_16x16x32_bf16 v[18:21], v[168:171], v[208:211], v[18:21]
	v_mfma_f32_16x16x32_bf16 v[6:9], v[160:163], v[216:219], v[6:9]
	v_mfma_f32_16x16x32_bf16 v[2:5], v[168:171], v[216:219], v[2:5]
	s_setprio 0
	s_setprio 1
	v_mfma_f32_16x16x32_bf16 v[62:65], v[172:175], v[188:191], v[62:65]
	v_mfma_f32_16x16x32_bf16 v[58:61], v[180:183], v[188:191], v[58:61]
	v_mfma_f32_16x16x32_bf16 v[46:49], v[172:175], v[196:199], v[46:49]
	v_mfma_f32_16x16x32_bf16 v[42:45], v[180:183], v[196:199], v[42:45]
	v_mfma_f32_16x16x32_bf16 v[30:33], v[172:175], v[204:207], v[30:33]
	v_mfma_f32_16x16x32_bf16 v[26:29], v[180:183], v[204:207], v[26:29]
	v_mfma_f32_16x16x32_bf16 v[14:17], v[172:175], v[212:215], v[14:17]
	v_mfma_f32_16x16x32_bf16 v[10:13], v[180:183], v[212:215], v[10:13]
	v_mfma_f32_16x16x32_bf16 v[62:65], v[176:179], v[192:195], v[62:65]
	v_mfma_f32_16x16x32_bf16 v[58:61], v[184:187], v[192:195], v[58:61]
	v_mfma_f32_16x16x32_bf16 v[46:49], v[176:179], v[200:203], v[46:49]
	v_mfma_f32_16x16x32_bf16 v[42:45], v[184:187], v[200:203], v[42:45]
	v_mfma_f32_16x16x32_bf16 v[30:33], v[176:179], v[208:211], v[30:33]
	v_mfma_f32_16x16x32_bf16 v[26:29], v[184:187], v[208:211], v[26:29]
	v_mfma_f32_16x16x32_bf16 v[14:17], v[176:179], v[216:219], v[14:17]
	v_mfma_f32_16x16x32_bf16 v[10:13], v[184:187], v[216:219], v[10:13]
	s_setprio 0
	s_barrier
	v_add_u32_e32 v168, s86, v154
	v_add_u32_e32 v184, s87, v154
	ds_read_b128 v[150:153], v168
	ds_read_b128 v[160:163], v168 offset:1024
	ds_read_b128 v[164:167], v168 offset:2048
	ds_read_b128 v[168:171], v168 offset:3072
	ds_read_b128 v[172:175], v184
	ds_read_b128 v[176:179], v184 offset:1024
	ds_read_b128 v[180:183], v184 offset:2048
	ds_read_b128 v[184:187], v184 offset:3072
	s_mov_b32 m0, s40
	v_lshl_add_u64 v[230:231], s[30:31], 0, v[138:139]
	ds_read_b128 v[188:191], v158 offset:32768
	ds_read_b128 v[192:195], v158 offset:33792
	ds_read_b128 v[196:199], v158 offset:34816
	ds_read_b128 v[200:203], v158 offset:35840
	ds_read_b128 v[204:207], v158 offset:36864
	ds_read_b128 v[208:211], v158 offset:37888
	ds_read_b128 v[212:215], v158 offset:38912
	ds_read_b128 v[216:219], v158 offset:39936
	global_load_lds_dwordx4 v[230:231], off
	v_lshl_add_u64 v[230:231], s[30:31], 0, v[140:141]
	s_mov_b32 m0, s41
	s_nop 0
	global_load_lds_dwordx4 v[230:231], off
	s_waitcnt vmcnt(8)
	s_waitcnt lgkmcnt(0)
	s_setprio 1
	s_barrier
	v_mfma_f32_16x16x32_bf16 v[126:129], v[150:153], v[188:191], v[126:129]
	v_mfma_f32_16x16x32_bf16 v[122:125], v[164:167], v[188:191], v[122:125]
	v_mfma_f32_16x16x32_bf16 v[110:113], v[150:153], v[196:199], v[110:113]
	v_mfma_f32_16x16x32_bf16 v[106:109], v[164:167], v[196:199], v[106:109]
	v_mfma_f32_16x16x32_bf16 v[94:97], v[150:153], v[204:207], v[94:97]
	v_mfma_f32_16x16x32_bf16 v[90:93], v[164:167], v[204:207], v[90:93]
	v_mfma_f32_16x16x32_bf16 v[78:81], v[150:153], v[212:215], v[78:81]
	v_mfma_f32_16x16x32_bf16 v[74:77], v[164:167], v[212:215], v[74:77]
	v_mfma_f32_16x16x32_bf16 v[126:129], v[160:163], v[192:195], v[126:129]
	v_mfma_f32_16x16x32_bf16 v[122:125], v[168:171], v[192:195], v[122:125]
	v_mfma_f32_16x16x32_bf16 v[110:113], v[160:163], v[200:203], v[110:113]
	v_mfma_f32_16x16x32_bf16 v[106:109], v[168:171], v[200:203], v[106:109]
	v_mfma_f32_16x16x32_bf16 v[94:97], v[160:163], v[208:211], v[94:97]
	v_mfma_f32_16x16x32_bf16 v[90:93], v[168:171], v[208:211], v[90:93]
	v_mfma_f32_16x16x32_bf16 v[78:81], v[160:163], v[216:219], v[78:81]
	v_mfma_f32_16x16x32_bf16 v[74:77], v[168:171], v[216:219], v[74:77]
	s_setprio 0
	s_setprio 1
	v_mfma_f32_16x16x32_bf16 v[118:121], v[172:175], v[188:191], v[118:121]
	v_mfma_f32_16x16x32_bf16 v[114:117], v[180:183], v[188:191], v[114:117]
	v_mfma_f32_16x16x32_bf16 v[102:105], v[172:175], v[196:199], v[102:105]
	v_mfma_f32_16x16x32_bf16 v[98:101], v[180:183], v[196:199], v[98:101]
	v_mfma_f32_16x16x32_bf16 v[86:89], v[172:175], v[204:207], v[86:89]
	v_mfma_f32_16x16x32_bf16 v[82:85], v[180:183], v[204:207], v[82:85]
	v_mfma_f32_16x16x32_bf16 v[70:73], v[172:175], v[212:215], v[70:73]
	v_mfma_f32_16x16x32_bf16 v[66:69], v[180:183], v[212:215], v[66:69]
	v_mfma_f32_16x16x32_bf16 v[118:121], v[176:179], v[192:195], v[118:121]
	v_mfma_f32_16x16x32_bf16 v[114:117], v[184:187], v[192:195], v[114:117]
	v_mfma_f32_16x16x32_bf16 v[102:105], v[176:179], v[200:203], v[102:105]
	v_mfma_f32_16x16x32_bf16 v[98:101], v[184:187], v[200:203], v[98:101]
	v_mfma_f32_16x16x32_bf16 v[86:89], v[176:179], v[208:211], v[86:89]
	v_mfma_f32_16x16x32_bf16 v[82:85], v[184:187], v[208:211], v[82:85]
	v_mfma_f32_16x16x32_bf16 v[70:73], v[176:179], v[216:219], v[70:73]
	v_mfma_f32_16x16x32_bf16 v[66:69], v[184:187], v[216:219], v[66:69]
	s_setprio 0
	s_barrier
	s_add_i32 s30, s86, s37
	v_lshl_add_u64 v[220:221], v[220:221], 0, s[14:15]
	s_mov_b32 m0, s30
	ds_read_b128 v[188:191], v158 offset:49152
	ds_read_b128 v[192:195], v158 offset:50176
	ds_read_b128 v[196:199], v158 offset:51200
	ds_read_b128 v[200:203], v158 offset:52224
	ds_read_b128 v[204:207], v158 offset:53248
	ds_read_b128 v[208:211], v158 offset:54272
	ds_read_b128 v[212:215], v158 offset:55296
	ds_read_b128 v[216:219], v158 offset:56320
	global_load_lds_dwordx4 v[220:221], off
	s_add_i32 m0, s30, 0x2000
	s_add_u32 s28, s28, 0x80080
	v_lshl_add_u64 v[220:221], v[222:223], 0, s[14:15]
	s_addc_u32 s29, s29, 0
	s_add_i32 s30, s87, s37
	global_load_lds_dwordx4 v[220:221], off
	v_lshl_add_u64 v[220:221], s[28:29], 0, v[130:131]
	s_mov_b32 m0, s30
	s_nop 0
	global_load_lds_dwordx4 v[220:221], off
	v_lshl_add_u64 v[220:221], s[28:29], 0, v[132:133]
	s_add_i32 m0, s30, 0x2000
	s_nop 0
	global_load_lds_dwordx4 v[220:221], off
	v_lshl_add_u64 v[220:221], v[224:225], 0, s[14:15]
	s_mov_b32 m0, s43
	s_nop 0
	global_load_lds_dwordx4 v[220:221], off
	v_lshl_add_u64 v[220:221], v[226:227], 0, s[14:15]
	s_mov_b32 m0, s44
	s_nop 0
	global_load_lds_dwordx4 v[220:221], off
	s_waitcnt vmcnt(8)
	s_waitcnt lgkmcnt(0)
	s_setprio 1
	s_barrier
	v_mfma_f32_16x16x32_bf16 v[54:57], v[150:153], v[188:191], v[54:57]
	v_mfma_f32_16x16x32_bf16 v[50:53], v[164:167], v[188:191], v[50:53]
	v_mfma_f32_16x16x32_bf16 v[38:41], v[150:153], v[196:199], v[38:41]
	v_mfma_f32_16x16x32_bf16 v[34:37], v[164:167], v[196:199], v[34:37]
	v_mfma_f32_16x16x32_bf16 v[22:25], v[150:153], v[204:207], v[22:25]
	v_mfma_f32_16x16x32_bf16 v[18:21], v[164:167], v[204:207], v[18:21]
	v_mfma_f32_16x16x32_bf16 v[6:9], v[150:153], v[212:215], v[6:9]
	v_mfma_f32_16x16x32_bf16 v[2:5], v[164:167], v[212:215], v[2:5]
	v_mfma_f32_16x16x32_bf16 v[54:57], v[160:163], v[192:195], v[54:57]
	v_mfma_f32_16x16x32_bf16 v[50:53], v[168:171], v[192:195], v[50:53]
	v_mfma_f32_16x16x32_bf16 v[38:41], v[160:163], v[200:203], v[38:41]
	v_mfma_f32_16x16x32_bf16 v[34:37], v[168:171], v[200:203], v[34:37]
	v_mfma_f32_16x16x32_bf16 v[22:25], v[160:163], v[208:211], v[22:25]
	v_mfma_f32_16x16x32_bf16 v[18:21], v[168:171], v[208:211], v[18:21]
	v_mfma_f32_16x16x32_bf16 v[6:9], v[160:163], v[216:219], v[6:9]
	v_mfma_f32_16x16x32_bf16 v[2:5], v[168:171], v[216:219], v[2:5]
	s_setprio 0
	s_setprio 1
	v_mfma_f32_16x16x32_bf16 v[62:65], v[172:175], v[188:191], v[62:65]
	v_mfma_f32_16x16x32_bf16 v[58:61], v[180:183], v[188:191], v[58:61]
	v_mfma_f32_16x16x32_bf16 v[46:49], v[172:175], v[196:199], v[46:49]
	v_mfma_f32_16x16x32_bf16 v[42:45], v[180:183], v[196:199], v[42:45]
	v_mfma_f32_16x16x32_bf16 v[30:33], v[172:175], v[204:207], v[30:33]
	v_mfma_f32_16x16x32_bf16 v[26:29], v[180:183], v[204:207], v[26:29]
	v_mfma_f32_16x16x32_bf16 v[14:17], v[172:175], v[212:215], v[14:17]
	v_mfma_f32_16x16x32_bf16 v[10:13], v[180:183], v[212:215], v[10:13]
	v_mfma_f32_16x16x32_bf16 v[62:65], v[176:179], v[192:195], v[62:65]
	v_mfma_f32_16x16x32_bf16 v[58:61], v[184:187], v[192:195], v[58:61]
	v_mfma_f32_16x16x32_bf16 v[46:49], v[176:179], v[200:203], v[46:49]
	v_mfma_f32_16x16x32_bf16 v[42:45], v[184:187], v[200:203], v[42:45]
	v_mfma_f32_16x16x32_bf16 v[30:33], v[176:179], v[208:211], v[30:33]
	v_mfma_f32_16x16x32_bf16 v[26:29], v[184:187], v[208:211], v[26:29]
	v_mfma_f32_16x16x32_bf16 v[14:17], v[176:179], v[216:219], v[14:17]
	v_mfma_f32_16x16x32_bf16 v[10:13], v[184:187], v[216:219], v[10:13]
	s_setprio 0
	s_barrier
	s_add_i32 s49, s49, 2
	s_add_u32 s26, s26, 0x100
	s_addc_u32 s27, s27, 0
	s_add_u32 s19, s19, 0x100
	s_addc_u32 s21, s21, 0
	s_cmp_gt_u32 s49, 29
	s_cbranch_scc0 .LBB0_1089
	s_and_b64 vcc, exec, s[16:17]
	s_cbranch_vccz .LBB0_1092
	s_barrier

.LBB0_1346:
	s_ashr_i32 s17, s16, 31
	s_lshl_b64 s[24:25], s[16:17], 16
	s_add_i32 s17, s50, 0x80
	v_add_u32_e32 v202, s17, v1
	v_add_u32_e32 v203, s17, v190
	s_lshl_b32 s17, s16, 2
	s_add_i32 s17, s17, 0
	s_add_i32 s17, s17, 0x20000
	s_add_u32 s24, s18, s24
	s_addc_u32 s25, s19, s25
	v_mov_b32_e32 v175, v167
	v_mov_b32_e32 v173, v167
	s_add_u32 s56, s26, 0x100
	v_add_u32_e32 v200, s50, v1
	v_add_u32_e32 v201, s50, v190
	v_lshl_add_u64 v[178:179], s[10:11], 0, v[172:173]
	v_lshl_add_u64 v[180:181], s[10:11], 0, v[174:175]
	s_addc_u32 s57, s27, 0
	s_mov_b32 s58, -2
	s_mov_b64 s[26:27], 0
	s_xor_b64 s[28:29], s[22:23], -1
	v_mov_b32_e32 v169, v199
	v_mov_b32_e32 v171, v176
	v_mov_b32_e32 v173, v174
	v_mov_b32_e32 v175, v172
	s_add_u32 s30, s84, s26
	s_addc_u32 s31, s85, s27
	v_add_u32_e32 v2, s3, v193
	v_add_u32_e32 v14, s2, v193
	s_add_u32 s34, s30, 0x35400100
	ds_read_b128 v[18:21], v2
	ds_read_b128 v[22:25], v2 offset:1024
	ds_read_b128 v[26:29], v2 offset:2048
	ds_read_b128 v[30:33], v2 offset:3072
	ds_read_b128 v[2:5], v14
	ds_read_b128 v[6:9], v14 offset:1024
	ds_read_b128 v[10:13], v14 offset:2048
	ds_read_b128 v[14:17], v14 offset:3072
	s_addc_u32 s35, s31, 0
	s_add_u32 s59, s56, s26
	s_addc_u32 s60, s57, s27
	s_cmpk_eq_i32 s26, 0x700
	s_cselect_b64 vcc, -1, 0
	s_and_b64 s[30:31], vcc, exec
	v_cndmask_b32_e32 v166, v199, v169, vcc
	s_cselect_b32 s35, s5, s35
	s_cselect_b32 s34, s4, s34
	v_cndmask_b32_e32 v238, v176, v171, vcc
	v_cndmask_b32_e32 v229, v174, v173, vcc
	v_cndmask_b32_e32 v240, v172, v175, vcc
	s_cselect_b32 s31, s21, s60
	s_cselect_b32 s30, s20, s59
	v_lshl_add_u64 v[230:231], v[180:181], 0, s[26:27]
	s_add_i32 m0, s39, 0xc000
	ds_read_b128 v[182:185], v197
	ds_read_b128 v[186:189], v197 offset:1024
	ds_read_b128 v[204:207], v197 offset:2048
	ds_read_b128 v[208:211], v197 offset:3072
	ds_read_b128 v[212:215], v197 offset:4096
	ds_read_b128 v[216:219], v197 offset:5120
	ds_read_b128 v[220:223], v197 offset:6144
	ds_read_b128 v[224:227], v197 offset:7168
	global_load_lds_dwordx4 v[230:231], off
	v_lshl_add_u64 v[230:231], v[178:179], 0, s[26:27]
	s_add_i32 m0, s39, 0xe000
	s_nop 0
	global_load_lds_dwordx4 v[230:231], off
	s_waitcnt vmcnt(8)
	s_waitcnt lgkmcnt(0)
	s_setprio 1
	s_barrier
	s_nop 1
	v_mfma_f32_16x16x128_f8f6f4 v[158:161], v[18:25], v[182:189], 0
	v_mfma_f32_16x16x128_f8f6f4 v[150:153], v[26:33], v[182:189], 0
	v_mfma_f32_16x16x128_f8f6f4 v[142:145], v[18:25], v[204:211], 0
	v_mfma_f32_16x16x128_f8f6f4 v[134:137], v[26:33], v[204:211], 0
	v_mfma_f32_16x16x128_f8f6f4 v[126:129], v[18:25], v[212:219], 0
	v_mfma_f32_16x16x128_f8f6f4 v[118:121], v[26:33], v[212:219], 0
	v_mfma_f32_16x16x128_f8f6f4 v[110:113], v[18:25], v[220:227], 0
	v_mfma_f32_16x16x128_f8f6f4 v[102:105], v[26:33], v[220:227], 0
	s_setprio 0
	s_setprio 1
	s_nop 1
	v_mfma_f32_16x16x128_f8f6f4 v[154:157], v[2:9], v[182:189], 0
	v_mfma_f32_16x16x128_f8f6f4 v[146:149], v[10:17], v[182:189], 0
	v_mfma_f32_16x16x128_f8f6f4 v[138:141], v[2:9], v[204:211], 0
	v_mfma_f32_16x16x128_f8f6f4 v[130:133], v[10:17], v[204:211], 0
	v_mfma_f32_16x16x128_f8f6f4 v[122:125], v[2:9], v[212:219], 0
	v_mfma_f32_16x16x128_f8f6f4 v[114:117], v[10:17], v[212:219], 0
	v_mfma_f32_16x16x128_f8f6f4 v[106:109], v[2:9], v[220:227], 0
	v_mfma_f32_16x16x128_f8f6f4 v[98:101], v[10:17], v[220:227], 0
	s_setprio 0
	s_barrier
	s_add_i32 s59, s3, s38
	v_lshl_add_u64 v[182:183], s[30:31], 0, v[164:165]
	s_mov_b32 m0, s59
	ds_read_b128 v[204:207], v197 offset:16384
	ds_read_b128 v[208:211], v197 offset:17408
	ds_read_b128 v[212:215], v197 offset:18432
	ds_read_b128 v[216:219], v197 offset:19456
	ds_read_b128 v[220:223], v197 offset:20480
	ds_read_b128 v[224:227], v197 offset:21504
	ds_read_b128 v[230:233], v197 offset:22528
	ds_read_b128 v[234:237], v197 offset:23552
	global_load_lds_dwordx4 v[182:183], off
	s_add_i32 m0, s59, 0x2000
	s_add_u32 s60, s30, 0x40000
	v_lshl_add_u64 v[184:185], s[30:31], 0, v[162:163]
	s_addc_u32 s61, s31, 0
	s_add_i32 s59, s2, s38
	global_load_lds_dwordx4 v[184:185], off
	v_lshl_add_u64 v[186:187], s[60:61], 0, v[164:165]
	s_mov_b32 m0, s59
	v_mov_b32_e32 v239, v167
	global_load_lds_dwordx4 v[186:187], off
	v_lshl_add_u64 v[186:187], s[60:61], 0, v[162:163]
	s_add_i32 m0, s59, 0x2000
	v_lshl_add_u64 v[188:189], s[34:35], 0, v[166:167]
	global_load_lds_dwordx4 v[186:187], off
	s_mov_b32 m0, s39
	v_lshl_add_u64 v[186:187], s[34:35], 0, v[238:239]
	global_load_lds_dwordx4 v166, s[34:35]
	s_mov_b32 m0, s40
	s_nop 0
	global_load_lds_dwordx4 v238, s[34:35]
	s_waitcnt vmcnt(8)
	s_waitcnt lgkmcnt(0)
	s_setprio 1
	s_barrier
	s_nop 1
	v_mfma_f32_16x16x128_f8f6f4 v[94:97], v[18:25], v[204:211], 0
	v_mfma_f32_16x16x128_f8f6f4 v[86:89], v[26:33], v[204:211], 0
	v_mfma_f32_16x16x128_f8f6f4 v[78:81], v[18:25], v[212:219], 0
	v_mfma_f32_16x16x128_f8f6f4 v[66:69], v[26:33], v[212:219], 0
	v_mfma_f32_16x16x128_f8f6f4 v[54:57], v[18:25], v[220:227], 0
	v_mfma_f32_16x16x128_f8f6f4 v[46:49], v[26:33], v[220:227], 0
	v_mfma_f32_16x16x128_f8f6f4 v[38:41], v[18:25], v[230:237], 0
	v_mfma_f32_16x16x128_f8f6f4 v[34:37], v[26:33], v[230:237], 0
	s_setprio 0
	s_setprio 1
	s_nop 1
	v_mfma_f32_16x16x128_f8f6f4 v[90:93], v[2:9], v[204:211], 0
	v_mfma_f32_16x16x128_f8f6f4 v[82:85], v[10:17], v[204:211], 0
	v_mfma_f32_16x16x128_f8f6f4 v[74:77], v[2:9], v[212:219], 0
	v_mfma_f32_16x16x128_f8f6f4 v[58:61], v[10:17], v[212:219], 0
	v_mfma_f32_16x16x128_f8f6f4 v[70:73], v[2:9], v[220:227], 0
	v_mfma_f32_16x16x128_f8f6f4 v[62:65], v[10:17], v[220:227], 0
	v_mfma_f32_16x16x128_f8f6f4 v[50:53], v[2:9], v[230:237], 0
	v_mfma_f32_16x16x128_f8f6f4 v[42:45], v[10:17], v[230:237], 0
	s_setprio 0
	s_barrier
	v_add_u32_e32 v14, s86, v193
	v_add_u32_e32 v30, s87, v193
	ds_read_b128 v[2:5], v14
	ds_read_b128 v[6:9], v14 offset:1024
	ds_read_b128 v[10:13], v14 offset:2048
	ds_read_b128 v[14:17], v14 offset:3072
	ds_read_b128 v[18:21], v30
	ds_read_b128 v[22:25], v30 offset:1024
	ds_read_b128 v[26:29], v30 offset:2048
	ds_read_b128 v[30:33], v30 offset:3072
	s_mov_b32 m0, s41
	ds_read_b128 v[204:207], v197 offset:32768
	ds_read_b128 v[208:211], v197 offset:33792
	ds_read_b128 v[212:215], v197 offset:34816
	ds_read_b128 v[216:219], v197 offset:35840
	ds_read_b128 v[220:223], v197 offset:36864
	ds_read_b128 v[224:227], v197 offset:37888
	ds_read_b128 v[230:233], v197 offset:38912
	ds_read_b128 v[234:237], v197 offset:39936
	global_load_lds_dwordx4 v229, s[34:35]
	s_mov_b32 m0, s42
	s_nop 0
	global_load_lds_dwordx4 v240, s[34:35]
	s_waitcnt vmcnt(8)
	s_waitcnt lgkmcnt(0)
	s_setprio 1
	s_barrier
	s_nop 1
	v_mfma_f32_16x16x128_f8f6f4 v[158:161], v[2:9], v[204:211], v[158:161]
	v_mfma_f32_16x16x128_f8f6f4 v[150:153], v[10:17], v[204:211], v[150:153]
	v_mfma_f32_16x16x128_f8f6f4 v[142:145], v[2:9], v[212:219], v[142:145]
	v_mfma_f32_16x16x128_f8f6f4 v[134:137], v[10:17], v[212:219], v[134:137]
	v_mfma_f32_16x16x128_f8f6f4 v[126:129], v[2:9], v[220:227], v[126:129]
	v_mfma_f32_16x16x128_f8f6f4 v[118:121], v[10:17], v[220:227], v[118:121]
	v_mfma_f32_16x16x128_f8f6f4 v[110:113], v[2:9], v[230:237], v[110:113]
	v_mfma_f32_16x16x128_f8f6f4 v[102:105], v[10:17], v[230:237], v[102:105]
	s_setprio 0
	s_setprio 1
	s_nop 1
	v_mfma_f32_16x16x128_f8f6f4 v[154:157], v[18:25], v[204:211], v[154:157]
	v_mfma_f32_16x16x128_f8f6f4 v[146:149], v[26:33], v[204:211], v[146:149]
	v_mfma_f32_16x16x128_f8f6f4 v[138:141], v[18:25], v[212:219], v[138:141]
	v_mfma_f32_16x16x128_f8f6f4 v[130:133], v[26:33], v[212:219], v[130:133]
	v_mfma_f32_16x16x128_f8f6f4 v[122:125], v[18:25], v[220:227], v[122:125]
	v_mfma_f32_16x16x128_f8f6f4 v[114:117], v[26:33], v[220:227], v[114:117]
	v_mfma_f32_16x16x128_f8f6f4 v[106:109], v[18:25], v[230:237], v[106:109]
	v_mfma_f32_16x16x128_f8f6f4 v[98:101], v[26:33], v[230:237], v[98:101]
	s_setprio 0
	s_barrier
	s_add_i32 s34, s86, s38
	v_lshl_add_u64 v[182:183], v[182:183], 0, s[8:9]
	s_mov_b32 m0, s34
	ds_read_b128 v[204:207], v197 offset:49152
	ds_read_b128 v[208:211], v197 offset:50176
	ds_read_b128 v[212:215], v197 offset:51200
	ds_read_b128 v[216:219], v197 offset:52224
	ds_read_b128 v[220:223], v197 offset:53248
	ds_read_b128 v[224:227], v197 offset:54272
	ds_read_b128 v[230:233], v197 offset:55296
	ds_read_b128 v[234:237], v197 offset:56320
	global_load_lds_dwordx4 v[182:183], off
	s_add_i32 m0, s34, 0x2000
	s_add_u32 s30, s30, 0x40080
	v_lshl_add_u64 v[182:183], v[184:185], 0, s[8:9]
	s_addc_u32 s31, s31, 0
	s_add_i32 s34, s87, s38
	global_load_lds_dwordx4 v[182:183], off
	v_lshl_add_u64 v[182:183], s[30:31], 0, v[164:165]
	s_mov_b32 m0, s34
	s_nop 0
	global_load_lds_dwordx4 v[182:183], off
	v_lshl_add_u64 v[182:183], s[30:31], 0, v[162:163]
	s_add_i32 m0, s34, 0x2000
	s_nop 0
	global_load_lds_dwordx4 v[182:183], off
	v_lshl_add_u64 v[182:183], v[188:189], 0, s[8:9]
	s_mov_b32 m0, s43
	s_nop 0
	global_load_lds_dwordx4 v[182:183], off
	v_lshl_add_u64 v[182:183], v[186:187], 0, s[8:9]
	s_mov_b32 m0, s44
	s_nop 0
	global_load_lds_dwordx4 v[182:183], off
	s_waitcnt vmcnt(8)
	s_waitcnt lgkmcnt(0)
	s_setprio 1
	s_barrier
	s_nop 1
	v_mfma_f32_16x16x128_f8f6f4 v[94:97], v[2:9], v[204:211], v[94:97]
	v_mfma_f32_16x16x128_f8f6f4 v[86:89], v[10:17], v[204:211], v[86:89]
	v_mfma_f32_16x16x128_f8f6f4 v[78:81], v[2:9], v[212:219], v[78:81]
	v_mfma_f32_16x16x128_f8f6f4 v[66:69], v[10:17], v[212:219], v[66:69]
	v_mfma_f32_16x16x128_f8f6f4 v[54:57], v[2:9], v[220:227], v[54:57]
	v_mfma_f32_16x16x128_f8f6f4 v[46:49], v[10:17], v[220:227], v[46:49]
	v_mfma_f32_16x16x128_f8f6f4 v[38:41], v[2:9], v[230:237], v[38:41]
	v_mfma_f32_16x16x128_f8f6f4 v[34:37], v[10:17], v[230:237], v[34:37]
	s_setprio 0
	s_setprio 1
	s_nop 1
	v_mfma_f32_16x16x128_f8f6f4 v[90:93], v[18:25], v[204:211], v[90:93]
	v_mfma_f32_16x16x128_f8f6f4 v[82:85], v[26:33], v[204:211], v[82:85]
	v_mfma_f32_16x16x128_f8f6f4 v[74:77], v[18:25], v[212:219], v[74:77]
	v_mfma_f32_16x16x128_f8f6f4 v[58:61], v[26:33], v[212:219], v[58:61]
	v_mfma_f32_16x16x128_f8f6f4 v[70:73], v[18:25], v[220:227], v[70:73]
	v_mfma_f32_16x16x128_f8f6f4 v[62:65], v[26:33], v[220:227], v[62:65]
	v_mfma_f32_16x16x128_f8f6f4 v[50:53], v[18:25], v[230:237], v[50:53]
	v_mfma_f32_16x16x128_f8f6f4 v[42:45], v[26:33], v[230:237], v[42:45]
	s_setprio 0
	s_barrier
	s_add_i32 s58, s58, 2
	s_add_u32 s26, s26, 0x100
	s_addc_u32 s27, s27, 0
	s_cmp_gt_u32 s58, 13
	s_cbranch_scc1 .LBB0_1350
	s_branch .LBB0_1348
.LBB0_1347:
	s_add_u32 s30, s84, s26
	s_addc_u32 s31, s85, s27
	v_add_u32_e32 v2, s3, v193
	v_add_u32_e32 v14, s2, v193
	s_add_u32 s34, s30, 0x35400100
	ds_read_b128 v[18:21], v2
	ds_read_b128 v[22:25], v2 offset:1024
	ds_read_b128 v[26:29], v2 offset:2048
	ds_read_b128 v[30:33], v2 offset:3072
	ds_read_b128 v[2:5], v14
	ds_read_b128 v[6:9], v14 offset:1024
	ds_read_b128 v[10:13], v14 offset:2048
	ds_read_b128 v[14:17], v14 offset:3072
	s_addc_u32 s35, s31, 0
	s_add_u32 s59, s56, s26
	s_addc_u32 s60, s57, s27
	s_cmpk_eq_i32 s26, 0x700
	s_cselect_b64 vcc, -1, 0
	s_and_b64 s[30:31], vcc, exec
	v_cndmask_b32_e32 v166, v199, v169, vcc
	s_cselect_b32 s35, s5, s35
	s_cselect_b32 s34, s4, s34
	v_cndmask_b32_e32 v238, v176, v171, vcc
	v_cndmask_b32_e32 v229, v174, v173, vcc
	v_cndmask_b32_e32 v240, v172, v175, vcc
	s_cselect_b32 s31, s21, s60
	s_cselect_b32 s30, s20, s59
	v_lshl_add_u64 v[230:231], v[180:181], 0, s[26:27]
	s_add_i32 m0, s39, 0xc000
	ds_read_b128 v[182:185], v197
	ds_read_b128 v[186:189], v197 offset:1024
	ds_read_b128 v[204:207], v197 offset:2048
	ds_read_b128 v[208:211], v197 offset:3072
	ds_read_b128 v[212:215], v197 offset:4096
	ds_read_b128 v[216:219], v197 offset:5120
	ds_read_b128 v[220:223], v197 offset:6144
	ds_read_b128 v[224:227], v197 offset:7168
	global_load_lds_dwordx4 v[230:231], off
	v_lshl_add_u64 v[230:231], v[178:179], 0, s[26:27]
	s_add_i32 m0, s39, 0xe000
	s_nop 0
	global_load_lds_dwordx4 v[230:231], off
	s_waitcnt vmcnt(8)
	s_waitcnt lgkmcnt(0)
	s_setprio 1
	s_barrier
	s_nop 1
	v_mfma_f32_16x16x128_f8f6f4 v[158:161], v[18:25], v[182:189], v[158:161]
	v_mfma_f32_16x16x128_f8f6f4 v[150:153], v[26:33], v[182:189], v[150:153]
	v_mfma_f32_16x16x128_f8f6f4 v[142:145], v[18:25], v[204:211], v[142:145]
	v_mfma_f32_16x16x128_f8f6f4 v[134:137], v[26:33], v[204:211], v[134:137]
	v_mfma_f32_16x16x128_f8f6f4 v[126:129], v[18:25], v[212:219], v[126:129]
	v_mfma_f32_16x16x128_f8f6f4 v[118:121], v[26:33], v[212:219], v[118:121]
	v_mfma_f32_16x16x128_f8f6f4 v[110:113], v[18:25], v[220:227], v[110:113]
	v_mfma_f32_16x16x128_f8f6f4 v[102:105], v[26:33], v[220:227], v[102:105]
	s_setprio 0
	s_setprio 1
	s_nop 1
	v_mfma_f32_16x16x128_f8f6f4 v[154:157], v[2:9], v[182:189], v[154:157]
	v_mfma_f32_16x16x128_f8f6f4 v[146:149], v[10:17], v[182:189], v[146:149]
	v_mfma_f32_16x16x128_f8f6f4 v[138:141], v[2:9], v[204:211], v[138:141]
	v_mfma_f32_16x16x128_f8f6f4 v[130:133], v[10:17], v[204:211], v[130:133]
	v_mfma_f32_16x16x128_f8f6f4 v[122:125], v[2:9], v[212:219], v[122:125]
	v_mfma_f32_16x16x128_f8f6f4 v[114:117], v[10:17], v[212:219], v[114:117]
	v_mfma_f32_16x16x128_f8f6f4 v[106:109], v[2:9], v[220:227], v[106:109]
	v_mfma_f32_16x16x128_f8f6f4 v[98:101], v[10:17], v[220:227], v[98:101]
	s_setprio 0
	s_barrier
	s_add_i32 s59, s3, s38
	v_lshl_add_u64 v[182:183], s[30:31], 0, v[164:165]
	s_mov_b32 m0, s59
	ds_read_b128 v[204:207], v197 offset:16384
	ds_read_b128 v[208:211], v197 offset:17408
	ds_read_b128 v[212:215], v197 offset:18432
	ds_read_b128 v[216:219], v197 offset:19456
	ds_read_b128 v[220:223], v197 offset:20480
	ds_read_b128 v[224:227], v197 offset:21504
	ds_read_b128 v[230:233], v197 offset:22528
	ds_read_b128 v[234:237], v197 offset:23552
	global_load_lds_dwordx4 v[182:183], off
	s_add_i32 m0, s59, 0x2000
	s_add_u32 s60, s30, 0x40000
	v_lshl_add_u64 v[184:185], s[30:31], 0, v[162:163]
	s_addc_u32 s61, s31, 0
	s_add_i32 s59, s2, s38
	global_load_lds_dwordx4 v[184:185], off
	v_lshl_add_u64 v[186:187], s[60:61], 0, v[164:165]
	s_mov_b32 m0, s59
	v_mov_b32_e32 v239, v167
	global_load_lds_dwordx4 v[186:187], off
	v_lshl_add_u64 v[186:187], s[60:61], 0, v[162:163]
	s_add_i32 m0, s59, 0x2000
	v_lshl_add_u64 v[188:189], s[34:35], 0, v[166:167]
	global_load_lds_dwordx4 v[186:187], off
	s_mov_b32 m0, s39
	v_lshl_add_u64 v[186:187], s[34:35], 0, v[238:239]
	global_load_lds_dwordx4 v166, s[34:35]
	s_mov_b32 m0, s40
	s_nop 0
	global_load_lds_dwordx4 v238, s[34:35]
	s_waitcnt vmcnt(8)
	s_waitcnt lgkmcnt(0)
	s_setprio 1
	s_barrier
	s_nop 1
	v_mfma_f32_16x16x128_f8f6f4 v[94:97], v[18:25], v[204:211], v[94:97]
	v_mfma_f32_16x16x128_f8f6f4 v[86:89], v[26:33], v[204:211], v[86:89]
	v_mfma_f32_16x16x128_f8f6f4 v[78:81], v[18:25], v[212:219], v[78:81]
	v_mfma_f32_16x16x128_f8f6f4 v[66:69], v[26:33], v[212:219], v[66:69]
	v_mfma_f32_16x16x128_f8f6f4 v[54:57], v[18:25], v[220:227], v[54:57]
	v_mfma_f32_16x16x128_f8f6f4 v[46:49], v[26:33], v[220:227], v[46:49]
	v_mfma_f32_16x16x128_f8f6f4 v[38:41], v[18:25], v[230:237], v[38:41]
	v_mfma_f32_16x16x128_f8f6f4 v[34:37], v[26:33], v[230:237], v[34:37]
	s_setprio 0
	s_setprio 1
	s_nop 1
	v_mfma_f32_16x16x128_f8f6f4 v[90:93], v[2:9], v[204:211], v[90:93]
	v_mfma_f32_16x16x128_f8f6f4 v[82:85], v[10:17], v[204:211], v[82:85]
	v_mfma_f32_16x16x128_f8f6f4 v[74:77], v[2:9], v[212:219], v[74:77]
	v_mfma_f32_16x16x128_f8f6f4 v[58:61], v[10:17], v[212:219], v[58:61]
	v_mfma_f32_16x16x128_f8f6f4 v[70:73], v[2:9], v[220:227], v[70:73]
	v_mfma_f32_16x16x128_f8f6f4 v[62:65], v[10:17], v[220:227], v[62:65]
	v_mfma_f32_16x16x128_f8f6f4 v[50:53], v[2:9], v[230:237], v[50:53]
	v_mfma_f32_16x16x128_f8f6f4 v[42:45], v[10:17], v[230:237], v[42:45]
	s_setprio 0
	s_barrier
	v_add_u32_e32 v14, s86, v193
	v_add_u32_e32 v30, s87, v193
	ds_read_b128 v[2:5], v14
	ds_read_b128 v[6:9], v14 offset:1024
	ds_read_b128 v[10:13], v14 offset:2048
	ds_read_b128 v[14:17], v14 offset:3072
	ds_read_b128 v[18:21], v30
	ds_read_b128 v[22:25], v30 offset:1024
	ds_read_b128 v[26:29], v30 offset:2048
	ds_read_b128 v[30:33], v30 offset:3072
	s_mov_b32 m0, s41
	ds_read_b128 v[204:207], v197 offset:32768
	ds_read_b128 v[208:211], v197 offset:33792
	ds_read_b128 v[212:215], v197 offset:34816
	ds_read_b128 v[216:219], v197 offset:35840
	ds_read_b128 v[220:223], v197 offset:36864
	ds_read_b128 v[224:227], v197 offset:37888
	ds_read_b128 v[230:233], v197 offset:38912
	ds_read_b128 v[234:237], v197 offset:39936
	global_load_lds_dwordx4 v229, s[34:35]
	s_mov_b32 m0, s42
	s_nop 0
	global_load_lds_dwordx4 v240, s[34:35]
	s_waitcnt vmcnt(8)
	s_waitcnt lgkmcnt(0)
	s_setprio 1
	s_barrier
	s_nop 1
	v_mfma_f32_16x16x128_f8f6f4 v[158:161], v[2:9], v[204:211], v[158:161]
	v_mfma_f32_16x16x128_f8f6f4 v[150:153], v[10:17], v[204:211], v[150:153]
	v_mfma_f32_16x16x128_f8f6f4 v[142:145], v[2:9], v[212:219], v[142:145]
	v_mfma_f32_16x16x128_f8f6f4 v[134:137], v[10:17], v[212:219], v[134:137]
	v_mfma_f32_16x16x128_f8f6f4 v[126:129], v[2:9], v[220:227], v[126:129]
	v_mfma_f32_16x16x128_f8f6f4 v[118:121], v[10:17], v[220:227], v[118:121]
	v_mfma_f32_16x16x128_f8f6f4 v[110:113], v[2:9], v[230:237], v[110:113]
	v_mfma_f32_16x16x128_f8f6f4 v[102:105], v[10:17], v[230:237], v[102:105]
	s_setprio 0
	s_setprio 1
	s_nop 1
	v_mfma_f32_16x16x128_f8f6f4 v[154:157], v[18:25], v[204:211], v[154:157]
	v_mfma_f32_16x16x128_f8f6f4 v[146:149], v[26:33], v[204:211], v[146:149]
	v_mfma_f32_16x16x128_f8f6f4 v[138:141], v[18:25], v[212:219], v[138:141]
	v_mfma_f32_16x16x128_f8f6f4 v[130:133], v[26:33], v[212:219], v[130:133]
	v_mfma_f32_16x16x128_f8f6f4 v[122:125], v[18:25], v[220:227], v[122:125]
	v_mfma_f32_16x16x128_f8f6f4 v[114:117], v[26:33], v[220:227], v[114:117]
	v_mfma_f32_16x16x128_f8f6f4 v[106:109], v[18:25], v[230:237], v[106:109]
	v_mfma_f32_16x16x128_f8f6f4 v[98:101], v[26:33], v[230:237], v[98:101]
	s_setprio 0
	s_barrier
	s_add_i32 s34, s86, s38
	v_lshl_add_u64 v[182:183], v[182:183], 0, s[8:9]
	s_mov_b32 m0, s34
	ds_read_b128 v[204:207], v197 offset:49152
	ds_read_b128 v[208:211], v197 offset:50176
	ds_read_b128 v[212:215], v197 offset:51200
	ds_read_b128 v[216:219], v197 offset:52224
	ds_read_b128 v[220:223], v197 offset:53248
	ds_read_b128 v[224:227], v197 offset:54272
	ds_read_b128 v[230:233], v197 offset:55296
	ds_read_b128 v[234:237], v197 offset:56320
	global_load_lds_dwordx4 v[182:183], off
	s_add_i32 m0, s34, 0x2000
	s_add_u32 s30, s30, 0x40080
	v_lshl_add_u64 v[182:183], v[184:185], 0, s[8:9]
	s_addc_u32 s31, s31, 0
	s_add_i32 s34, s87, s38
	global_load_lds_dwordx4 v[182:183], off
	v_lshl_add_u64 v[182:183], s[30:31], 0, v[164:165]
	s_mov_b32 m0, s34
	s_nop 0
	global_load_lds_dwordx4 v[182:183], off
	v_lshl_add_u64 v[182:183], s[30:31], 0, v[162:163]
	s_add_i32 m0, s34, 0x2000
	s_nop 0
	global_load_lds_dwordx4 v[182:183], off
	v_lshl_add_u64 v[182:183], v[188:189], 0, s[8:9]
	s_mov_b32 m0, s43
	s_nop 0
	global_load_lds_dwordx4 v[182:183], off
	v_lshl_add_u64 v[182:183], v[186:187], 0, s[8:9]
	s_mov_b32 m0, s44
	s_nop 0
	global_load_lds_dwordx4 v[182:183], off
	s_waitcnt vmcnt(8)
	s_waitcnt lgkmcnt(0)
	s_setprio 1
	s_barrier
	s_nop 1
	v_mfma_f32_16x16x128_f8f6f4 v[94:97], v[2:9], v[204:211], v[94:97]
	v_mfma_f32_16x16x128_f8f6f4 v[86:89], v[10:17], v[204:211], v[86:89]
	v_mfma_f32_16x16x128_f8f6f4 v[78:81], v[2:9], v[212:219], v[78:81]
	v_mfma_f32_16x16x128_f8f6f4 v[66:69], v[10:17], v[212:219], v[66:69]
	v_mfma_f32_16x16x128_f8f6f4 v[54:57], v[2:9], v[220:227], v[54:57]
	v_mfma_f32_16x16x128_f8f6f4 v[46:49], v[10:17], v[220:227], v[46:49]
	v_mfma_f32_16x16x128_f8f6f4 v[38:41], v[2:9], v[230:237], v[38:41]
	v_mfma_f32_16x16x128_f8f6f4 v[34:37], v[10:17], v[230:237], v[34:37]
	s_setprio 0
	s_setprio 1
	s_nop 1
	v_mfma_f32_16x16x128_f8f6f4 v[90:93], v[18:25], v[204:211], v[90:93]
	v_mfma_f32_16x16x128_f8f6f4 v[82:85], v[26:33], v[204:211], v[82:85]
	v_mfma_f32_16x16x128_f8f6f4 v[74:77], v[18:25], v[212:219], v[74:77]
	v_mfma_f32_16x16x128_f8f6f4 v[58:61], v[26:33], v[212:219], v[58:61]
	v_mfma_f32_16x16x128_f8f6f4 v[70:73], v[18:25], v[220:227], v[70:73]
	v_mfma_f32_16x16x128_f8f6f4 v[62:65], v[26:33], v[220:227], v[62:65]
	v_mfma_f32_16x16x128_f8f6f4 v[50:53], v[18:25], v[230:237], v[50:53]
	v_mfma_f32_16x16x128_f8f6f4 v[42:45], v[26:33], v[230:237], v[42:45]
	s_setprio 0
	s_barrier
	s_add_i32 s58, s58, 2
	s_add_u32 s26, s26, 0x100
	s_addc_u32 s27, s27, 0
	s_cmp_gt_u32 s58, 13
	s_cbranch_scc1 .LBB0_1350

.LBB0_1418:
	s_add_u32 s26, s26, 0x80
	s_addc_u32 s27, s27, 0
	s_add_u32 s34, s30, 0x100
	s_addc_u32 s35, s31, 0
	s_mov_b32 s50, -2
	ds_read_b128 v[18:21], v192
	ds_read_b128 v[22:25], v192 offset:1024
	ds_read_b128 v[26:29], v192 offset:2048
	ds_read_b128 v[30:33], v192 offset:3072
	ds_read_b128 v[2:5], v193
	ds_read_b128 v[6:9], v193 offset:1024
	ds_read_b128 v[10:13], v193 offset:2048
	ds_read_b128 v[14:17], v193 offset:3072
	s_add_u32 s28, s26, 0x80
	s_addc_u32 s29, s27, 0
	s_cmp_eq_u32 s50, 12
	s_cselect_b32 s31, s19, s29
	s_cselect_b32 s30, s18, s28
	s_cselect_b32 s29, s21, s35
	s_cselect_b32 s28, s20, s34
	v_lshl_add_u64 v[220:221], s[26:27], 0, v[178:179]
	s_add_i32 m0, s38, 0xc000
	ds_read_b128 v[180:183], v194
	ds_read_b128 v[184:187], v194 offset:1024
	ds_read_b128 v[196:199], v194 offset:2048
	ds_read_b128 v[200:203], v194 offset:3072
	ds_read_b128 v[204:207], v194 offset:4096
	ds_read_b128 v[208:211], v194 offset:5120
	ds_read_b128 v[212:215], v194 offset:6144
	ds_read_b128 v[216:219], v194 offset:7168
	global_load_lds_dwordx4 v[220:221], off
	v_lshl_add_u64 v[220:221], s[26:27], 0, v[176:177]
	s_add_i32 m0, s38, 0xe000
	s_nop 0
	global_load_lds_dwordx4 v[220:221], off
	s_waitcnt vmcnt(8)
	s_waitcnt lgkmcnt(0)
	s_setprio 1
	s_barrier
	s_nop 1
	v_mfma_f32_16x16x128_f8f6f4 v[158:161], v[18:25], v[180:187], 0
	v_mfma_f32_16x16x128_f8f6f4 v[154:157], v[26:33], v[180:187], 0
	v_mfma_f32_16x16x128_f8f6f4 v[142:145], v[18:25], v[196:203], 0
	v_mfma_f32_16x16x128_f8f6f4 v[138:141], v[26:33], v[196:203], 0
	v_mfma_f32_16x16x128_f8f6f4 v[126:129], v[18:25], v[204:211], 0
	v_mfma_f32_16x16x128_f8f6f4 v[122:125], v[26:33], v[204:211], 0
	v_mfma_f32_16x16x128_f8f6f4 v[110:113], v[18:25], v[212:219], 0
	v_mfma_f32_16x16x128_f8f6f4 v[106:109], v[26:33], v[212:219], 0
	s_setprio 0
	s_setprio 1
	s_nop 1
	v_mfma_f32_16x16x128_f8f6f4 v[150:153], v[2:9], v[180:187], 0
	v_mfma_f32_16x16x128_f8f6f4 v[146:149], v[10:17], v[180:187], 0
	v_mfma_f32_16x16x128_f8f6f4 v[134:137], v[2:9], v[196:203], 0
	v_mfma_f32_16x16x128_f8f6f4 v[130:133], v[10:17], v[196:203], 0
	v_mfma_f32_16x16x128_f8f6f4 v[118:121], v[2:9], v[204:211], 0
	v_mfma_f32_16x16x128_f8f6f4 v[114:117], v[10:17], v[204:211], 0
	v_mfma_f32_16x16x128_f8f6f4 v[94:97], v[2:9], v[212:219], 0
	v_mfma_f32_16x16x128_f8f6f4 v[90:93], v[10:17], v[212:219], 0
	s_setprio 0
	s_barrier
	s_add_i32 s51, s3, s37
	v_lshl_add_u64 v[180:181], s[28:29], 0, v[164:165]
	s_mov_b32 m0, s51
	ds_read_b128 v[196:199], v194 offset:16384
	ds_read_b128 v[200:203], v194 offset:17408
	ds_read_b128 v[204:207], v194 offset:18432
	ds_read_b128 v[208:211], v194 offset:19456
	ds_read_b128 v[212:215], v194 offset:20480
	ds_read_b128 v[216:219], v194 offset:21504
	ds_read_b128 v[220:223], v194 offset:22528
	ds_read_b128 v[224:227], v194 offset:23552
	global_load_lds_dwordx4 v[180:181], off
	s_add_i32 m0, s51, 0x2000
	s_add_u32 s52, s28, 0x40000
	v_lshl_add_u64 v[182:183], s[28:29], 0, v[162:163]
	s_addc_u32 s53, s29, 0
	s_add_i32 s51, s2, s37
	global_load_lds_dwordx4 v[182:183], off
	v_lshl_add_u64 v[184:185], s[52:53], 0, v[164:165]
	s_mov_b32 m0, s51
	v_lshl_add_u64 v[186:187], s[30:31], 0, v[168:169]
	global_load_lds_dwordx4 v[184:185], off
	v_lshl_add_u64 v[184:185], s[52:53], 0, v[162:163]
	s_add_i32 m0, s51, 0x2000
	s_nop 0
	global_load_lds_dwordx4 v[184:185], off
	v_lshl_add_u64 v[184:185], s[30:31], 0, v[166:167]
	s_mov_b32 m0, s38
	s_nop 0
	global_load_lds_dwordx4 v[184:185], off
	s_mov_b32 m0, s39
	s_nop 0
	global_load_lds_dwordx4 v[186:187], off
	s_waitcnt vmcnt(8)
	s_waitcnt lgkmcnt(0)
	s_setprio 1
	s_barrier
	s_nop 1
	v_mfma_f32_16x16x128_f8f6f4 v[78:81], v[18:25], v[196:203], 0
	v_mfma_f32_16x16x128_f8f6f4 v[74:77], v[26:33], v[196:203], 0
	v_mfma_f32_16x16x128_f8f6f4 v[62:65], v[18:25], v[204:211], 0
	v_mfma_f32_16x16x128_f8f6f4 v[58:61], v[26:33], v[204:211], 0
	v_mfma_f32_16x16x128_f8f6f4 v[46:49], v[18:25], v[212:219], 0
	v_mfma_f32_16x16x128_f8f6f4 v[42:45], v[26:33], v[212:219], 0
	v_mfma_f32_16x16x128_f8f6f4 v[38:41], v[18:25], v[220:227], 0
	v_mfma_f32_16x16x128_f8f6f4 v[34:37], v[26:33], v[220:227], 0
	s_setprio 0
	s_setprio 1
	s_nop 1
	v_mfma_f32_16x16x128_f8f6f4 v[98:101], v[2:9], v[196:203], 0
	v_mfma_f32_16x16x128_f8f6f4 v[102:105], v[10:17], v[196:203], 0
	v_mfma_f32_16x16x128_f8f6f4 v[82:85], v[2:9], v[204:211], 0
	v_mfma_f32_16x16x128_f8f6f4 v[86:89], v[10:17], v[204:211], 0
	v_mfma_f32_16x16x128_f8f6f4 v[66:69], v[2:9], v[212:219], 0
	v_mfma_f32_16x16x128_f8f6f4 v[70:73], v[10:17], v[212:219], 0
	v_mfma_f32_16x16x128_f8f6f4 v[50:53], v[2:9], v[220:227], 0
	v_mfma_f32_16x16x128_f8f6f4 v[54:57], v[10:17], v[220:227], 0
	s_setprio 0
	s_barrier
	v_add_u32_e32 v14, s86, v188
	v_add_u32_e32 v30, s87, v188
	ds_read_b128 v[2:5], v14
	ds_read_b128 v[6:9], v14 offset:1024
	ds_read_b128 v[10:13], v14 offset:2048
	ds_read_b128 v[14:17], v14 offset:3072
	ds_read_b128 v[18:21], v30
	ds_read_b128 v[22:25], v30 offset:1024
	ds_read_b128 v[26:29], v30 offset:2048
	ds_read_b128 v[30:33], v30 offset:3072
	s_mov_b32 m0, s40
	v_lshl_add_u64 v[230:231], s[30:31], 0, v[170:171]
	ds_read_b128 v[196:199], v194 offset:32768
	ds_read_b128 v[200:203], v194 offset:33792
	ds_read_b128 v[204:207], v194 offset:34816
	ds_read_b128 v[208:211], v194 offset:35840
	ds_read_b128 v[212:215], v194 offset:36864
	ds_read_b128 v[216:219], v194 offset:37888
	ds_read_b128 v[220:223], v194 offset:38912
	ds_read_b128 v[224:227], v194 offset:39936
	global_load_lds_dwordx4 v[230:231], off
	v_lshl_add_u64 v[230:231], s[30:31], 0, v[172:173]
	s_mov_b32 m0, s41
	s_nop 0
	global_load_lds_dwordx4 v[230:231], off
	s_waitcnt vmcnt(8)
	s_waitcnt lgkmcnt(0)
	s_setprio 1
	s_barrier
	s_nop 1
	v_mfma_f32_16x16x128_f8f6f4 v[158:161], v[2:9], v[196:203], v[158:161]
	v_mfma_f32_16x16x128_f8f6f4 v[154:157], v[10:17], v[196:203], v[154:157]
	v_mfma_f32_16x16x128_f8f6f4 v[142:145], v[2:9], v[204:211], v[142:145]
	v_mfma_f32_16x16x128_f8f6f4 v[138:141], v[10:17], v[204:211], v[138:141]
	v_mfma_f32_16x16x128_f8f6f4 v[126:129], v[2:9], v[212:219], v[126:129]
	v_mfma_f32_16x16x128_f8f6f4 v[122:125], v[10:17], v[212:219], v[122:125]
	v_mfma_f32_16x16x128_f8f6f4 v[110:113], v[2:9], v[220:227], v[110:113]
	v_mfma_f32_16x16x128_f8f6f4 v[106:109], v[10:17], v[220:227], v[106:109]
	s_setprio 0
	s_setprio 1
	s_nop 1
	v_mfma_f32_16x16x128_f8f6f4 v[150:153], v[18:25], v[196:203], v[150:153]
	v_mfma_f32_16x16x128_f8f6f4 v[146:149], v[26:33], v[196:203], v[146:149]
	v_mfma_f32_16x16x128_f8f6f4 v[134:137], v[18:25], v[204:211], v[134:137]
	v_mfma_f32_16x16x128_f8f6f4 v[130:133], v[26:33], v[204:211], v[130:133]
	v_mfma_f32_16x16x128_f8f6f4 v[118:121], v[18:25], v[212:219], v[118:121]
	v_mfma_f32_16x16x128_f8f6f4 v[114:117], v[26:33], v[212:219], v[114:117]
	v_mfma_f32_16x16x128_f8f6f4 v[94:97], v[18:25], v[220:227], v[94:97]
	v_mfma_f32_16x16x128_f8f6f4 v[90:93], v[26:33], v[220:227], v[90:93]
	s_setprio 0
	s_barrier
	s_add_i32 s30, s86, s37
	v_lshl_add_u64 v[180:181], v[180:181], 0, s[8:9]
	s_mov_b32 m0, s30
	ds_read_b128 v[196:199], v194 offset:49152
	ds_read_b128 v[200:203], v194 offset:50176
	ds_read_b128 v[204:207], v194 offset:51200
	ds_read_b128 v[208:211], v194 offset:52224
	ds_read_b128 v[212:215], v194 offset:53248
	ds_read_b128 v[216:219], v194 offset:54272
	ds_read_b128 v[220:223], v194 offset:55296
	ds_read_b128 v[224:227], v194 offset:56320
	global_load_lds_dwordx4 v[180:181], off
	s_add_i32 m0, s30, 0x2000
	s_add_u32 s28, s28, 0x40080
	v_lshl_add_u64 v[180:181], v[182:183], 0, s[8:9]
	s_addc_u32 s29, s29, 0
	s_add_i32 s30, s87, s37
	global_load_lds_dwordx4 v[180:181], off
	v_lshl_add_u64 v[180:181], s[28:29], 0, v[164:165]
	s_mov_b32 m0, s30
	s_nop 0
	global_load_lds_dwordx4 v[180:181], off
	v_lshl_add_u64 v[180:181], s[28:29], 0, v[162:163]
	s_add_i32 m0, s30, 0x2000
	s_nop 0
	global_load_lds_dwordx4 v[180:181], off
	v_lshl_add_u64 v[180:181], v[184:185], 0, s[8:9]
	s_mov_b32 m0, s43
	s_nop 0
	global_load_lds_dwordx4 v[180:181], off
	v_lshl_add_u64 v[180:181], v[186:187], 0, s[8:9]
	s_mov_b32 m0, s44
	s_nop 0
	global_load_lds_dwordx4 v[180:181], off
	s_waitcnt vmcnt(8)
	s_waitcnt lgkmcnt(0)
	s_setprio 1
	s_barrier
	s_nop 1
	v_mfma_f32_16x16x128_f8f6f4 v[78:81], v[2:9], v[196:203], v[78:81]
	v_mfma_f32_16x16x128_f8f6f4 v[74:77], v[10:17], v[196:203], v[74:77]
	v_mfma_f32_16x16x128_f8f6f4 v[62:65], v[2:9], v[204:211], v[62:65]
	v_mfma_f32_16x16x128_f8f6f4 v[58:61], v[10:17], v[204:211], v[58:61]
	v_mfma_f32_16x16x128_f8f6f4 v[46:49], v[2:9], v[212:219], v[46:49]
	v_mfma_f32_16x16x128_f8f6f4 v[42:45], v[10:17], v[212:219], v[42:45]
	v_mfma_f32_16x16x128_f8f6f4 v[38:41], v[2:9], v[220:227], v[38:41]
	v_mfma_f32_16x16x128_f8f6f4 v[34:37], v[10:17], v[220:227], v[34:37]
	s_setprio 0
	s_setprio 1
	s_nop 1
	v_mfma_f32_16x16x128_f8f6f4 v[98:101], v[18:25], v[196:203], v[98:101]
	v_mfma_f32_16x16x128_f8f6f4 v[102:105], v[26:33], v[196:203], v[102:105]
	v_mfma_f32_16x16x128_f8f6f4 v[82:85], v[18:25], v[204:211], v[82:85]
	v_mfma_f32_16x16x128_f8f6f4 v[86:89], v[26:33], v[204:211], v[86:89]
	v_mfma_f32_16x16x128_f8f6f4 v[66:69], v[18:25], v[212:219], v[66:69]
	v_mfma_f32_16x16x128_f8f6f4 v[70:73], v[26:33], v[212:219], v[70:73]
	v_mfma_f32_16x16x128_f8f6f4 v[50:53], v[18:25], v[220:227], v[50:53]
	v_mfma_f32_16x16x128_f8f6f4 v[54:57], v[26:33], v[220:227], v[54:57]
	s_setprio 0
	s_barrier
	s_add_i32 s50, s50, 2
	s_add_u32 s26, s26, 0x100
	s_addc_u32 s27, s27, 0
	s_add_u32 s34, s34, 0x100
	s_addc_u32 s35, s35, 0
	s_cmp_gt_u32 s50, 13
	s_cbranch_scc0 .LBB0_1419
	s_branch .Lmy_pexit_p9
.LBB0_1419:
	ds_read_b128 v[18:21], v192
	ds_read_b128 v[22:25], v192 offset:1024
	ds_read_b128 v[26:29], v192 offset:2048
	ds_read_b128 v[30:33], v192 offset:3072
	ds_read_b128 v[2:5], v193
	ds_read_b128 v[6:9], v193 offset:1024
	ds_read_b128 v[10:13], v193 offset:2048
	ds_read_b128 v[14:17], v193 offset:3072
	s_add_u32 s28, s26, 0x80
	s_addc_u32 s29, s27, 0
	s_cmp_eq_u32 s50, 12
	s_cselect_b32 s31, s19, s29
	s_cselect_b32 s30, s18, s28
	s_cselect_b32 s29, s21, s35
	s_cselect_b32 s28, s20, s34
	v_lshl_add_u64 v[220:221], s[26:27], 0, v[178:179]
	s_add_i32 m0, s38, 0xc000
	ds_read_b128 v[180:183], v194
	ds_read_b128 v[184:187], v194 offset:1024
	ds_read_b128 v[196:199], v194 offset:2048
	ds_read_b128 v[200:203], v194 offset:3072
	ds_read_b128 v[204:207], v194 offset:4096
	ds_read_b128 v[208:211], v194 offset:5120
	ds_read_b128 v[212:215], v194 offset:6144
	ds_read_b128 v[216:219], v194 offset:7168
	global_load_lds_dwordx4 v[220:221], off
	v_lshl_add_u64 v[220:221], s[26:27], 0, v[176:177]
	s_add_i32 m0, s38, 0xe000
	s_nop 0
	global_load_lds_dwordx4 v[220:221], off
	s_waitcnt vmcnt(8)
	s_waitcnt lgkmcnt(0)
	s_setprio 1
	s_barrier
	s_nop 1
	v_mfma_f32_16x16x128_f8f6f4 v[158:161], v[18:25], v[180:187], v[158:161]
	v_mfma_f32_16x16x128_f8f6f4 v[154:157], v[26:33], v[180:187], v[154:157]
	v_mfma_f32_16x16x128_f8f6f4 v[142:145], v[18:25], v[196:203], v[142:145]
	v_mfma_f32_16x16x128_f8f6f4 v[138:141], v[26:33], v[196:203], v[138:141]
	v_mfma_f32_16x16x128_f8f6f4 v[126:129], v[18:25], v[204:211], v[126:129]
	v_mfma_f32_16x16x128_f8f6f4 v[122:125], v[26:33], v[204:211], v[122:125]
	v_mfma_f32_16x16x128_f8f6f4 v[110:113], v[18:25], v[212:219], v[110:113]
	v_mfma_f32_16x16x128_f8f6f4 v[106:109], v[26:33], v[212:219], v[106:109]
	s_setprio 0
	s_setprio 1
	s_nop 1
	v_mfma_f32_16x16x128_f8f6f4 v[150:153], v[2:9], v[180:187], v[150:153]
	v_mfma_f32_16x16x128_f8f6f4 v[146:149], v[10:17], v[180:187], v[146:149]
	v_mfma_f32_16x16x128_f8f6f4 v[134:137], v[2:9], v[196:203], v[134:137]
	v_mfma_f32_16x16x128_f8f6f4 v[130:133], v[10:17], v[196:203], v[130:133]
	v_mfma_f32_16x16x128_f8f6f4 v[118:121], v[2:9], v[204:211], v[118:121]
	v_mfma_f32_16x16x128_f8f6f4 v[114:117], v[10:17], v[204:211], v[114:117]
	v_mfma_f32_16x16x128_f8f6f4 v[94:97], v[2:9], v[212:219], v[94:97]
	v_mfma_f32_16x16x128_f8f6f4 v[90:93], v[10:17], v[212:219], v[90:93]
	s_setprio 0
	s_barrier
	s_add_i32 s51, s3, s37
	v_lshl_add_u64 v[180:181], s[28:29], 0, v[164:165]
	s_mov_b32 m0, s51
	ds_read_b128 v[196:199], v194 offset:16384
	ds_read_b128 v[200:203], v194 offset:17408
	ds_read_b128 v[204:207], v194 offset:18432
	ds_read_b128 v[208:211], v194 offset:19456
	ds_read_b128 v[212:215], v194 offset:20480
	ds_read_b128 v[216:219], v194 offset:21504
	ds_read_b128 v[220:223], v194 offset:22528
	ds_read_b128 v[224:227], v194 offset:23552
	global_load_lds_dwordx4 v[180:181], off
	s_add_i32 m0, s51, 0x2000
	s_add_u32 s52, s28, 0x40000
	v_lshl_add_u64 v[182:183], s[28:29], 0, v[162:163]
	s_addc_u32 s53, s29, 0
	s_add_i32 s51, s2, s37
	global_load_lds_dwordx4 v[182:183], off
	v_lshl_add_u64 v[184:185], s[52:53], 0, v[164:165]
	s_mov_b32 m0, s51
	v_lshl_add_u64 v[186:187], s[30:31], 0, v[168:169]
	global_load_lds_dwordx4 v[184:185], off
	v_lshl_add_u64 v[184:185], s[52:53], 0, v[162:163]
	s_add_i32 m0, s51, 0x2000
	s_nop 0
	global_load_lds_dwordx4 v[184:185], off
	v_lshl_add_u64 v[184:185], s[30:31], 0, v[166:167]
	s_mov_b32 m0, s38
	s_nop 0
	global_load_lds_dwordx4 v[184:185], off
	s_mov_b32 m0, s39
	s_nop 0
	global_load_lds_dwordx4 v[186:187], off
	s_waitcnt vmcnt(8)
	s_waitcnt lgkmcnt(0)
	s_setprio 1
	s_barrier
	s_nop 1
	v_mfma_f32_16x16x128_f8f6f4 v[78:81], v[18:25], v[196:203], v[78:81]
	v_mfma_f32_16x16x128_f8f6f4 v[74:77], v[26:33], v[196:203], v[74:77]
	v_mfma_f32_16x16x128_f8f6f4 v[62:65], v[18:25], v[204:211], v[62:65]
	v_mfma_f32_16x16x128_f8f6f4 v[58:61], v[26:33], v[204:211], v[58:61]
	v_mfma_f32_16x16x128_f8f6f4 v[46:49], v[18:25], v[212:219], v[46:49]
	v_mfma_f32_16x16x128_f8f6f4 v[42:45], v[26:33], v[212:219], v[42:45]
	v_mfma_f32_16x16x128_f8f6f4 v[38:41], v[18:25], v[220:227], v[38:41]
	v_mfma_f32_16x16x128_f8f6f4 v[34:37], v[26:33], v[220:227], v[34:37]
	s_setprio 0
	s_setprio 1
	s_nop 1
	v_mfma_f32_16x16x128_f8f6f4 v[98:101], v[2:9], v[196:203], v[98:101]
	v_mfma_f32_16x16x128_f8f6f4 v[102:105], v[10:17], v[196:203], v[102:105]
	v_mfma_f32_16x16x128_f8f6f4 v[82:85], v[2:9], v[204:211], v[82:85]
	v_mfma_f32_16x16x128_f8f6f4 v[86:89], v[10:17], v[204:211], v[86:89]
	v_mfma_f32_16x16x128_f8f6f4 v[66:69], v[2:9], v[212:219], v[66:69]
	v_mfma_f32_16x16x128_f8f6f4 v[70:73], v[10:17], v[212:219], v[70:73]
	v_mfma_f32_16x16x128_f8f6f4 v[50:53], v[2:9], v[220:227], v[50:53]
	v_mfma_f32_16x16x128_f8f6f4 v[54:57], v[10:17], v[220:227], v[54:57]
	s_setprio 0
	s_barrier
	v_add_u32_e32 v14, s86, v188
	v_add_u32_e32 v30, s87, v188
	ds_read_b128 v[2:5], v14
	ds_read_b128 v[6:9], v14 offset:1024
	ds_read_b128 v[10:13], v14 offset:2048
	ds_read_b128 v[14:17], v14 offset:3072
	ds_read_b128 v[18:21], v30
	ds_read_b128 v[22:25], v30 offset:1024
	ds_read_b128 v[26:29], v30 offset:2048
	ds_read_b128 v[30:33], v30 offset:3072
	s_mov_b32 m0, s40
	v_lshl_add_u64 v[230:231], s[30:31], 0, v[170:171]
	ds_read_b128 v[196:199], v194 offset:32768
	ds_read_b128 v[200:203], v194 offset:33792
	ds_read_b128 v[204:207], v194 offset:34816
	ds_read_b128 v[208:211], v194 offset:35840
	ds_read_b128 v[212:215], v194 offset:36864
	ds_read_b128 v[216:219], v194 offset:37888
	ds_read_b128 v[220:223], v194 offset:38912
	ds_read_b128 v[224:227], v194 offset:39936
	global_load_lds_dwordx4 v[230:231], off
	v_lshl_add_u64 v[230:231], s[30:31], 0, v[172:173]
	s_mov_b32 m0, s41
	s_nop 0
	global_load_lds_dwordx4 v[230:231], off
	s_waitcnt vmcnt(8)
	s_waitcnt lgkmcnt(0)
	s_setprio 1
	s_barrier
	s_nop 1
	v_mfma_f32_16x16x128_f8f6f4 v[158:161], v[2:9], v[196:203], v[158:161]
	v_mfma_f32_16x16x128_f8f6f4 v[154:157], v[10:17], v[196:203], v[154:157]
	v_mfma_f32_16x16x128_f8f6f4 v[142:145], v[2:9], v[204:211], v[142:145]
	v_mfma_f32_16x16x128_f8f6f4 v[138:141], v[10:17], v[204:211], v[138:141]
	v_mfma_f32_16x16x128_f8f6f4 v[126:129], v[2:9], v[212:219], v[126:129]
	v_mfma_f32_16x16x128_f8f6f4 v[122:125], v[10:17], v[212:219], v[122:125]
	v_mfma_f32_16x16x128_f8f6f4 v[110:113], v[2:9], v[220:227], v[110:113]
	v_mfma_f32_16x16x128_f8f6f4 v[106:109], v[10:17], v[220:227], v[106:109]
	s_setprio 0
	s_setprio 1
	s_nop 1
	v_mfma_f32_16x16x128_f8f6f4 v[150:153], v[18:25], v[196:203], v[150:153]
	v_mfma_f32_16x16x128_f8f6f4 v[146:149], v[26:33], v[196:203], v[146:149]
	v_mfma_f32_16x16x128_f8f6f4 v[134:137], v[18:25], v[204:211], v[134:137]
	v_mfma_f32_16x16x128_f8f6f4 v[130:133], v[26:33], v[204:211], v[130:133]
	v_mfma_f32_16x16x128_f8f6f4 v[118:121], v[18:25], v[212:219], v[118:121]
	v_mfma_f32_16x16x128_f8f6f4 v[114:117], v[26:33], v[212:219], v[114:117]
	v_mfma_f32_16x16x128_f8f6f4 v[94:97], v[18:25], v[220:227], v[94:97]
	v_mfma_f32_16x16x128_f8f6f4 v[90:93], v[26:33], v[220:227], v[90:93]
	s_setprio 0
	s_barrier
	s_add_i32 s30, s86, s37
	v_lshl_add_u64 v[180:181], v[180:181], 0, s[8:9]
	s_mov_b32 m0, s30
	ds_read_b128 v[196:199], v194 offset:49152
	ds_read_b128 v[200:203], v194 offset:50176
	ds_read_b128 v[204:207], v194 offset:51200
	ds_read_b128 v[208:211], v194 offset:52224
	ds_read_b128 v[212:215], v194 offset:53248
	ds_read_b128 v[216:219], v194 offset:54272
	ds_read_b128 v[220:223], v194 offset:55296
	ds_read_b128 v[224:227], v194 offset:56320
	global_load_lds_dwordx4 v[180:181], off
	s_add_i32 m0, s30, 0x2000
	s_add_u32 s28, s28, 0x40080
	v_lshl_add_u64 v[180:181], v[182:183], 0, s[8:9]
	s_addc_u32 s29, s29, 0
	s_add_i32 s30, s87, s37
	global_load_lds_dwordx4 v[180:181], off
	v_lshl_add_u64 v[180:181], s[28:29], 0, v[164:165]
	s_mov_b32 m0, s30
	s_nop 0
	global_load_lds_dwordx4 v[180:181], off
	v_lshl_add_u64 v[180:181], s[28:29], 0, v[162:163]
	s_add_i32 m0, s30, 0x2000
	s_nop 0
	global_load_lds_dwordx4 v[180:181], off
	v_lshl_add_u64 v[180:181], v[184:185], 0, s[8:9]
	s_mov_b32 m0, s43
	s_nop 0
	global_load_lds_dwordx4 v[180:181], off
	v_lshl_add_u64 v[180:181], v[186:187], 0, s[8:9]
	s_mov_b32 m0, s44
	s_nop 0
	global_load_lds_dwordx4 v[180:181], off
	s_waitcnt vmcnt(8)
	s_waitcnt lgkmcnt(0)
	s_setprio 1
	s_barrier
	s_nop 1
	v_mfma_f32_16x16x128_f8f6f4 v[78:81], v[2:9], v[196:203], v[78:81]
	v_mfma_f32_16x16x128_f8f6f4 v[74:77], v[10:17], v[196:203], v[74:77]
	v_mfma_f32_16x16x128_f8f6f4 v[62:65], v[2:9], v[204:211], v[62:65]
	v_mfma_f32_16x16x128_f8f6f4 v[58:61], v[10:17], v[204:211], v[58:61]
	v_mfma_f32_16x16x128_f8f6f4 v[46:49], v[2:9], v[212:219], v[46:49]
	v_mfma_f32_16x16x128_f8f6f4 v[42:45], v[10:17], v[212:219], v[42:45]
	v_mfma_f32_16x16x128_f8f6f4 v[38:41], v[2:9], v[220:227], v[38:41]
	v_mfma_f32_16x16x128_f8f6f4 v[34:37], v[10:17], v[220:227], v[34:37]
	s_setprio 0
	s_setprio 1
	s_nop 1
	v_mfma_f32_16x16x128_f8f6f4 v[98:101], v[18:25], v[196:203], v[98:101]
	v_mfma_f32_16x16x128_f8f6f4 v[102:105], v[26:33], v[196:203], v[102:105]
	v_mfma_f32_16x16x128_f8f6f4 v[82:85], v[18:25], v[204:211], v[82:85]
	v_mfma_f32_16x16x128_f8f6f4 v[86:89], v[26:33], v[204:211], v[86:89]
	v_mfma_f32_16x16x128_f8f6f4 v[66:69], v[18:25], v[212:219], v[66:69]
	v_mfma_f32_16x16x128_f8f6f4 v[70:73], v[26:33], v[212:219], v[70:73]
	v_mfma_f32_16x16x128_f8f6f4 v[50:53], v[18:25], v[220:227], v[50:53]
	v_mfma_f32_16x16x128_f8f6f4 v[54:57], v[26:33], v[220:227], v[54:57]
	s_setprio 0
	s_barrier
	s_add_i32 s50, s50, 2
	s_add_u32 s26, s26, 0x100
	s_addc_u32 s27, s27, 0
	s_add_u32 s34, s34, 0x100
	s_addc_u32 s35, s35, 0
	s_cmp_gt_u32 s50, 13
	s_cbranch_scc0 .LBB0_1419
